# grid barrier: L1/L2 invalidate issued at arrival (after the arrive atomic) instead of after release; late buffer_inv removed; plain stores
# speedup vs baseline: 1.0026x; 1.0026x over previous
.LBB0_98:
	s_waitcnt vmcnt(0)
	v_pk_mul_f32 v[86:87], v[86:87], v[94:95] op_sel_hi:[1,0]
	v_add_u32_e32 v38, 0x8000, v57
	v_pk_mul_f32 v[84:85], v[84:85], v[94:95] op_sel_hi:[1,0]
	ds_write2_b32 v38, v86, v87 offset1:1
	v_add_u32_e32 v38, 0x8008, v57
	ds_write2_b32 v38, v84, v85 offset1:1
	v_pk_mul_f32 v[80:81], v[80:81], v[92:93] op_sel_hi:[1,0]
	v_add_u32_e32 v38, 0x8000, v67
	v_pk_mul_f32 v[78:79], v[78:79], v[92:93] op_sel_hi:[1,0]
	ds_write2_b32 v38, v80, v81 offset1:1
	v_add_u32_e32 v38, 0x8008, v67
	ds_write2_b32 v38, v78, v79 offset1:1
	v_pk_mul_f32 v[76:77], v[76:77], v[90:91] op_sel_hi:[1,0]
	v_add_u32_e32 v38, 0x8420, v67
	v_pk_mul_f32 v[72:73], v[72:73], v[90:91] op_sel_hi:[1,0]
	ds_write2_b32 v38, v76, v77 offset1:1
	v_add_u32_e32 v38, 0x8428, v67
	ds_write2_b32 v38, v72, v73 offset1:1
	v_pk_mul_f32 v[70:71], v[70:71], v[88:89] op_sel_hi:[1,0]
	v_add_u32_e32 v38, 0x8840, v67
	v_pk_mul_f32 v[68:69], v[68:69], v[88:89] op_sel_hi:[1,0]
	ds_write2_b32 v38, v70, v71 offset1:1
	v_add_u32_e32 v38, 0x8848, v67
	ds_write2_b32 v38, v68, v69 offset1:1
	v_pk_mul_f32 v[64:65], v[64:65], v[82:83] op_sel_hi:[1,0]
	v_add_u32_e32 v38, 0x8c60, v67
	v_pk_mul_f32 v[62:63], v[62:63], v[82:83] op_sel_hi:[1,0]
	ds_write2_b32 v38, v64, v65 offset1:1
	v_add_u32_e32 v38, 0x8c68, v67
	ds_write2_b32 v38, v62, v63 offset1:1
	v_pk_mul_f32 v[60:61], v[60:61], v[74:75] op_sel_hi:[1,0]
	v_add_u32_e32 v38, 0x9080, v67
	v_pk_mul_f32 v[58:59], v[58:59], v[74:75] op_sel_hi:[1,0]
	ds_write2_b32 v38, v60, v61 offset1:1
	v_add_u32_e32 v38, 0x9088, v67
	ds_write2_b32 v38, v58, v59 offset1:1
	v_pk_mul_f32 v[54:55], v[54:55], v[66:67] op_sel_hi:[1,0]
	v_add_u32_e32 v38, 0x94a0, v67
	v_pk_mul_f32 v[52:53], v[52:53], v[66:67] op_sel_hi:[1,0]
	ds_write2_b32 v38, v54, v55 offset1:1
	v_add_u32_e32 v38, 0x94a8, v67
	ds_write2_b32 v38, v52, v53 offset1:1
	v_pk_mul_f32 v[2:3], v[2:3], v[56:57] op_sel_hi:[1,0]
	v_add_u32_e32 v38, 0x98c0, v67
	v_pk_mul_f32 v[4:5], v[4:5], v[56:57] op_sel_hi:[1,0]
	ds_write2_b32 v38, v2, v3 offset1:1
	v_add_u32_e32 v2, 0x98c8, v67
	ds_write2_b32 v2, v4, v5 offset1:1
	s_waitcnt lgkmcnt(0)
	v_add_u32_e32 v38, 0x8000, v47
	ds_read2_b32 v[2:3], v38 offset1:33
	ds_read2_b32 v[4:5], v38 offset0:66 offset1:99
	ds_read2_b32 v[54:55], v38 offset0:132 offset1:165
	ds_read2_b32 v[58:59], v38 offset0:198 offset1:231
	v_mov_b32_e32 v51, v39
	v_lshl_add_u64 v[52:53], s[12:13], 0, v[50:51]
	s_cmp_lg_u32 s8, 0
	s_waitcnt lgkmcnt(3)
	v_cvt_pk_bf16_f32 v2, v2, v3
	s_waitcnt lgkmcnt(2)
	v_cvt_pk_bf16_f32 v3, v4, v5
	s_waitcnt lgkmcnt(1)
	v_cvt_pk_bf16_f32 v4, v54, v55
	v_mad_u64_u32 v[54:55], s[6:7], s36, v40, 0
	s_cselect_b64 s[12:13], -1, 0
	s_cmp_eq_u32 s8, 0
	s_waitcnt lgkmcnt(0)
	v_cvt_pk_bf16_f32 v5, v58, v59
	v_lshl_add_u64 v[54:55], v[54:55], 1, v[52:53]
	global_store_dwordx4 v[54:55], v[2:5], off
	s_cbranch_scc1 .LBB0_100
	v_lshl_add_u64 v[54:55], s[8:9], 1, v[54:55]
	global_store_dwordx4 v[54:55], v[2:5], off
.LBB0_100:
	ds_read2_b32 v[2:3], v38 offset0:8 offset1:41
	ds_read2_b32 v[4:5], v38 offset0:74 offset1:107
	ds_read2_b32 v[54:55], v38 offset0:140 offset1:173
	ds_read2_b32 v[58:59], v38 offset0:206 offset1:239
	v_cndmask_b32_e64 v51, 0, 1, s[12:13]
	s_waitcnt lgkmcnt(3)
	v_cvt_pk_bf16_f32 v2, v2, v3
	s_waitcnt lgkmcnt(2)
	v_cvt_pk_bf16_f32 v3, v4, v5
	s_waitcnt lgkmcnt(1)
	v_cvt_pk_bf16_f32 v4, v54, v55
	v_mad_u64_u32 v[54:55], s[6:7], s36, v42, 0
	s_waitcnt lgkmcnt(0)
	v_cvt_pk_bf16_f32 v5, v58, v59
	v_lshl_add_u64 v[54:55], v[54:55], 1, v[52:53]
	v_cmp_ne_u32_e64 s[6:7], 1, v51
	s_andn2_b64 vcc, exec, s[12:13]
	global_store_dwordx4 v[54:55], v[2:5], off
	s_cbranch_vccnz .LBB0_102
	v_lshl_add_u64 v[54:55], s[8:9], 1, v[54:55]
	global_store_dwordx4 v[54:55], v[2:5], off
.LBB0_102:
	ds_read2_b32 v[2:3], v38 offset0:16 offset1:49
	ds_read2_b32 v[4:5], v38 offset0:82 offset1:115
	ds_read2_b32 v[54:55], v38 offset0:148 offset1:181
	ds_read2_b32 v[58:59], v38 offset0:214 offset1:247
	s_and_b64 vcc, exec, s[6:7]
	s_waitcnt lgkmcnt(3)
	v_cvt_pk_bf16_f32 v2, v2, v3
	s_waitcnt lgkmcnt(2)
	v_cvt_pk_bf16_f32 v3, v4, v5
	s_waitcnt lgkmcnt(1)
	v_cvt_pk_bf16_f32 v4, v54, v55
	v_mad_u64_u32 v[54:55], s[12:13], s36, v44, 0
	s_waitcnt lgkmcnt(0)
	v_cvt_pk_bf16_f32 v5, v58, v59
	v_lshl_add_u64 v[54:55], v[54:55], 1, v[52:53]
	global_store_dwordx4 v[54:55], v[2:5], off
	s_cbranch_vccnz .LBB0_104
	v_lshl_add_u64 v[54:55], s[8:9], 1, v[54:55]
	global_store_dwordx4 v[54:55], v[2:5], off
.LBB0_104:
	ds_read2_b32 v[2:3], v38 offset0:24 offset1:57
	ds_read2_b32 v[4:5], v38 offset0:90 offset1:123
	ds_read2_b32 v[54:55], v38 offset0:156 offset1:189
	ds_read2_b32 v[58:59], v38 offset0:222 offset1:255
	s_and_b64 vcc, exec, s[6:7]
	s_waitcnt lgkmcnt(3)
	v_cvt_pk_bf16_f32 v2, v2, v3
	s_waitcnt lgkmcnt(2)
	v_cvt_pk_bf16_f32 v3, v4, v5
	s_waitcnt lgkmcnt(1)
	v_cvt_pk_bf16_f32 v4, v54, v55
	v_mad_u64_u32 v[54:55], s[12:13], s36, v46, 0
	s_waitcnt lgkmcnt(0)
	v_cvt_pk_bf16_f32 v5, v58, v59
	v_lshl_add_u64 v[52:53], v[54:55], 1, v[52:53]
	global_store_dwordx4 v[52:53], v[2:5], off
	s_cbranch_vccnz .LBB0_56
	v_lshl_add_u64 v[52:53], s[8:9], 1, v[52:53]
	global_store_dwordx4 v[52:53], v[2:5], off
	s_branch .LBB0_56

.LBB0_117:
	s_or_b64 exec, exec, s[12:13]
	s_waitcnt lgkmcnt(3)
	v_add_f32_e32 v105, 0, v112
	v_add_f32_e32 v105, v105, v113
	s_waitcnt lgkmcnt(2)
	v_add_f32_e32 v105, v105, v110
	v_add_f32_e32 v105, v105, v111
	s_waitcnt lgkmcnt(1)
	v_add_f32_e32 v105, v105, v108
	v_add_f32_e32 v105, v105, v109
	s_waitcnt lgkmcnt(0)
	v_add_f32_e32 v105, v105, v106
	v_add_f32_e32 v105, v105, v107
	v_fmamk_f32 v105, v105, 0x3a800000, v124
	v_mul_f32_e32 v106, 0x4b800000, v105
	v_cmp_gt_f32_e64 s[6:7], s19, v105
	s_cmp_eq_u32 s21, s17
	s_mov_b32 s12, s21
	v_cndmask_b32_e64 v105, v105, v106, s[6:7]
	v_rsq_f32_e32 v105, v105
	v_or_b32_e32 v106, s22, v1
	v_ashrrev_i32_e32 v107, 31, v106
	v_lshlrev_b64 v[106:107], 11, v[106:107]
	v_mul_f32_e32 v108, 0x45800000, v105
	v_cndmask_b32_e64 v108, v105, v108, s[6:7]
	v_pk_mul_f32 v[62:63], v[62:63], v[108:109] op_sel_hi:[1,0]
	v_pk_mul_f32 v[64:65], v[64:65], v[108:109] op_sel_hi:[1,0]
	v_pk_mul_f32 v[58:59], v[58:59], v[108:109] op_sel_hi:[1,0]
	v_pk_mul_f32 v[60:61], v[60:61], v[108:109] op_sel_hi:[1,0]
	v_pk_mul_f32 v[64:65], v[8:9], v[64:65]
	v_pk_mul_f32 v[62:63], v[6:7], v[62:63]
	v_pk_mul_f32 v[110:111], v[4:5], v[60:61]
	v_pk_mul_f32 v[60:61], v[2:3], v[58:59]
	v_lshl_add_u64 v[106:107], v[100:101], 0, v[106:107]
	v_cvt_pk_bf16_f32 v58, v62, v63
	v_cvt_pk_bf16_f32 v59, v64, v65
	v_cvt_pk_bf16_f32 v60, v60, v61
	v_cvt_pk_bf16_f32 v61, v110, v111
	v_pk_mul_f32 v[54:55], v[54:55], v[108:109] op_sel_hi:[1,0]
	v_pk_mul_f32 v[56:57], v[56:57], v[108:109] op_sel_hi:[1,0]
	v_pk_mul_f32 v[50:51], v[50:51], v[108:109] op_sel_hi:[1,0]
	v_pk_mul_f32 v[52:53], v[52:53], v[108:109] op_sel_hi:[1,0]
	global_store_dwordx4 v[106:107], v[58:61], off
	v_pk_mul_f32 v[56:57], v[16:17], v[56:57]
	v_pk_mul_f32 v[54:55], v[14:15], v[54:55]
	v_pk_mul_f32 v[58:59], v[12:13], v[52:53]
	v_pk_mul_f32 v[52:53], v[10:11], v[50:51]
	v_cvt_pk_bf16_f32 v50, v54, v55
	v_cvt_pk_bf16_f32 v51, v56, v57
	v_cvt_pk_bf16_f32 v52, v52, v53
	v_cvt_pk_bf16_f32 v53, v58, v59
	v_pk_mul_f32 v[46:47], v[46:47], v[108:109] op_sel_hi:[1,0]
	v_pk_mul_f32 v[48:49], v[48:49], v[108:109] op_sel_hi:[1,0]
	v_pk_mul_f32 v[42:43], v[42:43], v[108:109] op_sel_hi:[1,0]
	v_pk_mul_f32 v[44:45], v[44:45], v[108:109] op_sel_hi:[1,0]
	global_store_dwordx4 v[106:107], v[50:53], off offset:64
	v_pk_mul_f32 v[48:49], v[24:25], v[48:49]
	v_pk_mul_f32 v[46:47], v[22:23], v[46:47]
	v_pk_mul_f32 v[50:51], v[20:21], v[44:45]
	v_pk_mul_f32 v[44:45], v[18:19], v[42:43]
	v_cvt_pk_bf16_f32 v42, v46, v47
	v_cvt_pk_bf16_f32 v43, v48, v49
	v_cvt_pk_bf16_f32 v44, v44, v45
	v_cvt_pk_bf16_f32 v45, v50, v51
	v_pk_mul_f32 v[38:39], v[38:39], v[108:109] op_sel_hi:[1,0]
	v_pk_mul_f32 v[40:41], v[40:41], v[108:109] op_sel_hi:[1,0]
	v_pk_mul_f32 v[34:35], v[34:35], v[108:109] op_sel_hi:[1,0]
	v_pk_mul_f32 v[36:37], v[36:37], v[108:109] op_sel_hi:[1,0]
	global_store_dwordx4 v[106:107], v[42:45], off offset:128
	v_pk_mul_f32 v[40:41], v[32:33], v[40:41]
	v_pk_mul_f32 v[38:39], v[30:31], v[38:39]
	v_pk_mul_f32 v[42:43], v[28:29], v[36:37]
	v_pk_mul_f32 v[36:37], v[26:27], v[34:35]
	v_cvt_pk_bf16_f32 v34, v38, v39
	v_cvt_pk_bf16_f32 v35, v40, v41
	v_cvt_pk_bf16_f32 v36, v36, v37
	v_cvt_pk_bf16_f32 v37, v42, v43
	global_store_dwordx4 v[106:107], v[34:37], off offset:192
	s_waitcnt vmcnt(4)
	v_mov_b64_e32 v[38:39], v[94:95]
	v_mov_b64_e32 v[42:43], v[82:83]
	v_mov_b64_e32 v[34:35], v[90:91]
	v_mov_b64_e32 v[46:47], v[86:87]
	v_mov_b64_e32 v[50:51], v[74:75]
	v_mov_b64_e32 v[54:55], v[78:79]
	v_mov_b64_e32 v[58:59], v[66:67]
	v_mov_b64_e32 v[62:63], v[70:71]
	v_mov_b64_e32 v[36:37], v[92:93]
	v_mov_b64_e32 v[40:41], v[96:97]
	v_mov_b64_e32 v[44:45], v[84:85]
	v_mov_b64_e32 v[48:49], v[88:89]
	v_mov_b64_e32 v[52:53], v[76:77]
	v_mov_b64_e32 v[56:57], v[80:81]
	v_mov_b64_e32 v[60:61], v[68:69]
	v_mov_b64_e32 v[64:65], v[72:73]
	s_cbranch_scc1 .LBB0_129

.LBB0_215:
	s_waitcnt vmcnt(0)
	v_pk_mul_f32 v[86:87], v[86:87], v[94:95] op_sel_hi:[1,0]
	v_add_u32_e32 v38, 0x8000, v57
	v_pk_mul_f32 v[84:85], v[84:85], v[94:95] op_sel_hi:[1,0]
	ds_write2_b32 v38, v86, v87 offset1:1
	v_add_u32_e32 v38, 0x8008, v57
	ds_write2_b32 v38, v84, v85 offset1:1
	v_pk_mul_f32 v[80:81], v[80:81], v[92:93] op_sel_hi:[1,0]
	v_add_u32_e32 v38, 0x8000, v67
	v_pk_mul_f32 v[78:79], v[78:79], v[92:93] op_sel_hi:[1,0]
	ds_write2_b32 v38, v80, v81 offset1:1
	v_add_u32_e32 v38, 0x8008, v67
	ds_write2_b32 v38, v78, v79 offset1:1
	v_pk_mul_f32 v[76:77], v[76:77], v[90:91] op_sel_hi:[1,0]
	v_add_u32_e32 v38, 0x8420, v67
	v_pk_mul_f32 v[72:73], v[72:73], v[90:91] op_sel_hi:[1,0]
	ds_write2_b32 v38, v76, v77 offset1:1
	v_add_u32_e32 v38, 0x8428, v67
	ds_write2_b32 v38, v72, v73 offset1:1
	v_pk_mul_f32 v[70:71], v[70:71], v[88:89] op_sel_hi:[1,0]
	v_add_u32_e32 v38, 0x8840, v67
	v_pk_mul_f32 v[68:69], v[68:69], v[88:89] op_sel_hi:[1,0]
	ds_write2_b32 v38, v70, v71 offset1:1
	v_add_u32_e32 v38, 0x8848, v67
	ds_write2_b32 v38, v68, v69 offset1:1
	v_pk_mul_f32 v[64:65], v[64:65], v[82:83] op_sel_hi:[1,0]
	v_add_u32_e32 v38, 0x8c60, v67
	v_pk_mul_f32 v[62:63], v[62:63], v[82:83] op_sel_hi:[1,0]
	ds_write2_b32 v38, v64, v65 offset1:1
	v_add_u32_e32 v38, 0x8c68, v67
	ds_write2_b32 v38, v62, v63 offset1:1
	v_pk_mul_f32 v[60:61], v[60:61], v[74:75] op_sel_hi:[1,0]
	v_add_u32_e32 v38, 0x9080, v67
	v_pk_mul_f32 v[58:59], v[58:59], v[74:75] op_sel_hi:[1,0]
	ds_write2_b32 v38, v60, v61 offset1:1
	v_add_u32_e32 v38, 0x9088, v67
	ds_write2_b32 v38, v58, v59 offset1:1
	v_pk_mul_f32 v[54:55], v[54:55], v[66:67] op_sel_hi:[1,0]
	v_add_u32_e32 v38, 0x94a0, v67
	v_pk_mul_f32 v[52:53], v[52:53], v[66:67] op_sel_hi:[1,0]
	ds_write2_b32 v38, v54, v55 offset1:1
	v_add_u32_e32 v38, 0x94a8, v67
	ds_write2_b32 v38, v52, v53 offset1:1
	v_pk_mul_f32 v[2:3], v[2:3], v[56:57] op_sel_hi:[1,0]
	v_add_u32_e32 v38, 0x98c0, v67
	v_pk_mul_f32 v[4:5], v[4:5], v[56:57] op_sel_hi:[1,0]
	ds_write2_b32 v38, v2, v3 offset1:1
	v_add_u32_e32 v2, 0x98c8, v67
	ds_write2_b32 v2, v4, v5 offset1:1
	s_waitcnt lgkmcnt(0)
	v_add_u32_e32 v38, 0x8000, v47
	ds_read2_b32 v[2:3], v38 offset1:33
	ds_read2_b32 v[4:5], v38 offset0:66 offset1:99
	ds_read2_b32 v[54:55], v38 offset0:132 offset1:165
	ds_read2_b32 v[58:59], v38 offset0:198 offset1:231
	v_mov_b32_e32 v51, v39
	v_lshl_add_u64 v[52:53], s[10:11], 0, v[50:51]
	s_cmp_lg_u32 s8, 0
	s_waitcnt lgkmcnt(3)
	v_cvt_pk_bf16_f32 v2, v2, v3
	s_waitcnt lgkmcnt(2)
	v_cvt_pk_bf16_f32 v3, v4, v5
	s_waitcnt lgkmcnt(1)
	v_cvt_pk_bf16_f32 v4, v54, v55
	v_mad_u64_u32 v[54:55], s[6:7], s27, v40, 0
	s_cselect_b64 s[10:11], -1, 0
	s_cmp_eq_u32 s8, 0
	s_waitcnt lgkmcnt(0)
	v_cvt_pk_bf16_f32 v5, v58, v59
	v_lshl_add_u64 v[54:55], v[54:55], 1, v[52:53]
	global_store_dwordx4 v[54:55], v[2:5], off
	s_cbranch_scc1 .LBB0_217
	v_lshl_add_u64 v[54:55], s[8:9], 1, v[54:55]
	global_store_dwordx4 v[54:55], v[2:5], off
.LBB0_217:
	ds_read2_b32 v[2:3], v38 offset0:8 offset1:41
	ds_read2_b32 v[4:5], v38 offset0:74 offset1:107
	ds_read2_b32 v[54:55], v38 offset0:140 offset1:173
	ds_read2_b32 v[58:59], v38 offset0:206 offset1:239
	v_cndmask_b32_e64 v51, 0, 1, s[10:11]
	s_waitcnt lgkmcnt(3)
	v_cvt_pk_bf16_f32 v2, v2, v3
	s_waitcnt lgkmcnt(2)
	v_cvt_pk_bf16_f32 v3, v4, v5
	s_waitcnt lgkmcnt(1)
	v_cvt_pk_bf16_f32 v4, v54, v55
	v_mad_u64_u32 v[54:55], s[6:7], s27, v42, 0
	s_waitcnt lgkmcnt(0)
	v_cvt_pk_bf16_f32 v5, v58, v59
	v_lshl_add_u64 v[54:55], v[54:55], 1, v[52:53]
	v_cmp_ne_u32_e64 s[6:7], 1, v51
	s_andn2_b64 vcc, exec, s[10:11]
	global_store_dwordx4 v[54:55], v[2:5], off
	s_cbranch_vccnz .LBB0_219
	v_lshl_add_u64 v[54:55], s[8:9], 1, v[54:55]
	global_store_dwordx4 v[54:55], v[2:5], off
.LBB0_219:
	ds_read2_b32 v[2:3], v38 offset0:16 offset1:49
	ds_read2_b32 v[4:5], v38 offset0:82 offset1:115
	ds_read2_b32 v[54:55], v38 offset0:148 offset1:181
	ds_read2_b32 v[58:59], v38 offset0:214 offset1:247
	s_and_b64 vcc, exec, s[6:7]
	s_waitcnt lgkmcnt(3)
	v_cvt_pk_bf16_f32 v2, v2, v3
	s_waitcnt lgkmcnt(2)
	v_cvt_pk_bf16_f32 v3, v4, v5
	s_waitcnt lgkmcnt(1)
	v_cvt_pk_bf16_f32 v4, v54, v55
	v_mad_u64_u32 v[54:55], s[10:11], s27, v44, 0
	s_waitcnt lgkmcnt(0)
	v_cvt_pk_bf16_f32 v5, v58, v59
	v_lshl_add_u64 v[54:55], v[54:55], 1, v[52:53]
	global_store_dwordx4 v[54:55], v[2:5], off
	s_cbranch_vccnz .LBB0_221
	v_lshl_add_u64 v[54:55], s[8:9], 1, v[54:55]
	global_store_dwordx4 v[54:55], v[2:5], off
.LBB0_221:
	ds_read2_b32 v[2:3], v38 offset0:24 offset1:57
	ds_read2_b32 v[4:5], v38 offset0:90 offset1:123
	ds_read2_b32 v[54:55], v38 offset0:156 offset1:189
	ds_read2_b32 v[58:59], v38 offset0:222 offset1:255
	s_and_b64 vcc, exec, s[6:7]
	s_waitcnt lgkmcnt(3)
	v_cvt_pk_bf16_f32 v2, v2, v3
	s_waitcnt lgkmcnt(2)
	v_cvt_pk_bf16_f32 v3, v4, v5
	s_waitcnt lgkmcnt(1)
	v_cvt_pk_bf16_f32 v4, v54, v55
	v_mad_u64_u32 v[54:55], s[10:11], s27, v46, 0
	s_waitcnt lgkmcnt(0)
	v_cvt_pk_bf16_f32 v5, v58, v59
	v_lshl_add_u64 v[52:53], v[54:55], 1, v[52:53]
	global_store_dwordx4 v[52:53], v[2:5], off
	s_cbranch_vccnz .LBB0_173
	v_lshl_add_u64 v[52:53], s[8:9], 1, v[52:53]
	global_store_dwordx4 v[52:53], v[2:5], off
	s_branch .LBB0_173

.LBB0_247:
	s_mov_b64 s[8:9], exec
	s_lshl_b32 s6, s86, 8
	v_mbcnt_lo_u32_b32 v2, s8, 0
	s_add_u32 s6, s84, s6
	v_mbcnt_hi_u32_b32 v2, s9, v2
	s_addc_u32 s7, s85, 0
	v_cmp_eq_u32_e32 vcc, 0, v2
	s_and_saveexec_b64 s[10:11], vcc
	s_cbranch_execz .LBB0_249
	s_bcnt1_i32_b64 s8, s[8:9]
	v_mov_b32_e32 v4, 0x1000
	v_mov_b32_e32 v5, s8
	global_atomic_add v4, v4, v5, s[6:7] offset:1024 sc0
	buffer_inv sc1

.LBB0_262:
	s_or_b64 exec, exec, s[10:11]
	s_waitcnt vmcnt(0)
	s_waitcnt vmcnt(0)

.LBB0_280:
	s_or_b64 exec, exec, s[8:9]
	s_mov_b64 s[8:9], exec
	v_mbcnt_lo_u32_b32 v1, s8, 0
	v_mbcnt_hi_u32_b32 v1, s9, v1
	v_cmp_eq_u32_e32 vcc, 0, v1
	s_waitcnt vmcnt(0)
	s_and_saveexec_b64 s[10:11], vcc
	s_cbranch_execz .LBB0_282
	s_bcnt1_i32_b64 s8, s[8:9]
	v_mov_b32_e32 v1, 0x2000
	v_mov_b32_e32 v2, s8
	global_atomic_add v1, v2, s[6:7] offset:1024

.LBB0_302:
	s_lshr_b32 s15, s47, 31
	s_add_i32 s15, s47, s15
	s_ashr_i32 s22, s15, 1
	s_ashr_i32 s23, s22, 31
	s_lshl_b32 s13, s47, 8
	s_lshl_b64 s[24:25], s[22:23], 10
	s_add_u32 s24, s82, s24
	s_addc_u32 s25, s83, s25
	s_lshl_b32 s15, s22, 9
	s_sub_i32 s13, s13, s15
	s_add_i32 s15, s47, 1
	s_cmp_lt_u32 s15, 3
	v_or_b32_e32 v148, s13, v150
	s_cselect_b64 vcc, -1, 0
	v_ashrrev_i32_e32 v149, 31, v148
	v_cndmask_b32_e32 v146, 1.0, v154, vcc
	v_lshl_add_u32 v155, s20, 8, v1
	v_lshl_add_u64 v[148:149], v[148:149], 1, s[24:25]
	v_pk_add_f32 v[128:129], v[128:129], 0 op_sel_hi:[1,0]
	v_pk_add_f32 v[126:127], v[126:127], 0 op_sel_hi:[1,0]
	v_pk_add_f32 v[124:125], v[124:125], 0 op_sel_hi:[1,0]
	v_pk_add_f32 v[122:123], v[122:123], 0 op_sel_hi:[1,0]
	v_mad_i64_i32 v[156:157], s[22:23], v155, s46, v[148:149]
	v_pk_mul_f32 v[128:129], v[146:147], v[128:129] op_sel_hi:[0,1]
	v_pk_mul_f32 v[126:127], v[146:147], v[126:127] op_sel_hi:[0,1]
	v_pk_mul_f32 v[158:159], v[146:147], v[124:125] op_sel_hi:[0,1]
	v_pk_mul_f32 v[124:125], v[146:147], v[122:123] op_sel_hi:[0,1]
	v_cvt_pk_bf16_f32 v122, v126, v127
	v_cvt_pk_bf16_f32 v123, v128, v129
	v_pk_add_f32 v[112:113], v[112:113], 0 op_sel_hi:[1,0]
	v_pk_add_f32 v[110:111], v[110:111], 0 op_sel_hi:[1,0]
	v_cvt_pk_bf16_f32 v124, v124, v125
	v_cvt_pk_bf16_f32 v125, v158, v159
	global_store_dwordx4 v[156:157], v[122:125], off
	v_pk_add_f32 v[120:121], v[120:121], 0 op_sel_hi:[1,0]
	v_pk_add_f32 v[118:119], v[118:119], 0 op_sel_hi:[1,0]
	v_pk_mul_f32 v[122:123], v[146:147], v[112:113] op_sel_hi:[0,1]
	v_pk_mul_f32 v[112:113], v[146:147], v[110:111] op_sel_hi:[0,1]
	v_pk_mul_f32 v[120:121], v[146:147], v[120:121] op_sel_hi:[0,1]
	v_pk_mul_f32 v[118:119], v[146:147], v[118:119] op_sel_hi:[0,1]
	v_cvt_pk_bf16_f32 v110, v118, v119
	v_cvt_pk_bf16_f32 v111, v120, v121
	v_cvt_pk_bf16_f32 v112, v112, v113
	v_cvt_pk_bf16_f32 v113, v122, v123
	global_store_dwordx4 v[156:157], v[110:113], off offset:256
	v_pk_add_f32 v[114:115], v[114:115], 0 op_sel_hi:[1,0]
	v_pk_add_f32 v[108:109], v[108:109], 0 op_sel_hi:[1,0]
	v_or_b32_e32 v110, 16, v155
	v_pk_add_f32 v[112:113], v[116:117], 0 op_sel_hi:[1,0]
	v_pk_add_f32 v[106:107], v[106:107], 0 op_sel_hi:[1,0]
	v_mad_i64_i32 v[110:111], s[22:23], v110, s46, v[148:149]
	v_pk_mul_f32 v[112:113], v[146:147], v[112:113] op_sel_hi:[0,1]
	v_pk_mul_f32 v[114:115], v[146:147], v[114:115] op_sel_hi:[0,1]
	v_pk_mul_f32 v[116:117], v[146:147], v[108:109] op_sel_hi:[0,1]
	v_pk_mul_f32 v[108:109], v[146:147], v[106:107] op_sel_hi:[0,1]
	v_cvt_pk_bf16_f32 v106, v114, v115
	v_cvt_pk_bf16_f32 v107, v112, v113
	v_pk_add_f32 v[96:97], v[96:97], 0 op_sel_hi:[1,0]
	v_pk_add_f32 v[94:95], v[94:95], 0 op_sel_hi:[1,0]
	v_cvt_pk_bf16_f32 v108, v108, v109
	v_cvt_pk_bf16_f32 v109, v116, v117
	global_store_dwordx4 v[110:111], v[106:109], off
	v_pk_add_f32 v[104:105], v[104:105], 0 op_sel_hi:[1,0]
	v_pk_add_f32 v[102:103], v[102:103], 0 op_sel_hi:[1,0]
	v_pk_mul_f32 v[106:107], v[146:147], v[96:97] op_sel_hi:[0,1]
	v_pk_mul_f32 v[96:97], v[146:147], v[94:95] op_sel_hi:[0,1]
	v_pk_mul_f32 v[104:105], v[146:147], v[104:105] op_sel_hi:[0,1]
	v_pk_mul_f32 v[102:103], v[146:147], v[102:103] op_sel_hi:[0,1]
	v_cvt_pk_bf16_f32 v94, v102, v103
	v_cvt_pk_bf16_f32 v95, v104, v105
	v_cvt_pk_bf16_f32 v96, v96, v97
	v_cvt_pk_bf16_f32 v97, v106, v107
	global_store_dwordx4 v[110:111], v[94:97], off offset:256
	v_pk_add_f32 v[98:99], v[98:99], 0 op_sel_hi:[1,0]
	v_pk_add_f32 v[92:93], v[92:93], 0 op_sel_hi:[1,0]
	v_or_b32_e32 v94, 32, v155
	v_pk_add_f32 v[96:97], v[100:101], 0 op_sel_hi:[1,0]
	v_pk_add_f32 v[90:91], v[90:91], 0 op_sel_hi:[1,0]
	v_mad_i64_i32 v[94:95], s[22:23], v94, s46, v[148:149]
	v_pk_mul_f32 v[96:97], v[146:147], v[96:97] op_sel_hi:[0,1]
	v_pk_mul_f32 v[98:99], v[146:147], v[98:99] op_sel_hi:[0,1]
	v_pk_mul_f32 v[100:101], v[146:147], v[92:93] op_sel_hi:[0,1]
	v_pk_mul_f32 v[92:93], v[146:147], v[90:91] op_sel_hi:[0,1]
	v_cvt_pk_bf16_f32 v90, v98, v99
	v_cvt_pk_bf16_f32 v91, v96, v97
	v_pk_add_f32 v[80:81], v[80:81], 0 op_sel_hi:[1,0]
	v_pk_add_f32 v[78:79], v[78:79], 0 op_sel_hi:[1,0]
	v_cvt_pk_bf16_f32 v92, v92, v93
	v_cvt_pk_bf16_f32 v93, v100, v101
	global_store_dwordx4 v[94:95], v[90:93], off
	v_pk_add_f32 v[88:89], v[88:89], 0 op_sel_hi:[1,0]
	v_pk_add_f32 v[86:87], v[86:87], 0 op_sel_hi:[1,0]
	v_pk_mul_f32 v[90:91], v[146:147], v[80:81] op_sel_hi:[0,1]
	v_pk_mul_f32 v[80:81], v[146:147], v[78:79] op_sel_hi:[0,1]
	v_pk_mul_f32 v[88:89], v[146:147], v[88:89] op_sel_hi:[0,1]
	v_pk_mul_f32 v[86:87], v[146:147], v[86:87] op_sel_hi:[0,1]
	v_cvt_pk_bf16_f32 v78, v86, v87
	v_cvt_pk_bf16_f32 v79, v88, v89
	v_cvt_pk_bf16_f32 v80, v80, v81
	v_cvt_pk_bf16_f32 v81, v90, v91
	global_store_dwordx4 v[94:95], v[78:81], off offset:256
	v_pk_add_f32 v[82:83], v[82:83], 0 op_sel_hi:[1,0]
	v_pk_add_f32 v[76:77], v[76:77], 0 op_sel_hi:[1,0]
	v_or_b32_e32 v78, 48, v155
	v_pk_add_f32 v[80:81], v[84:85], 0 op_sel_hi:[1,0]
	v_pk_add_f32 v[74:75], v[74:75], 0 op_sel_hi:[1,0]
	v_mad_i64_i32 v[78:79], s[22:23], v78, s46, v[148:149]
	v_pk_mul_f32 v[80:81], v[146:147], v[80:81] op_sel_hi:[0,1]
	v_pk_mul_f32 v[82:83], v[146:147], v[82:83] op_sel_hi:[0,1]
	v_pk_mul_f32 v[84:85], v[146:147], v[76:77] op_sel_hi:[0,1]
	v_pk_mul_f32 v[76:77], v[146:147], v[74:75] op_sel_hi:[0,1]
	v_cvt_pk_bf16_f32 v74, v82, v83
	v_cvt_pk_bf16_f32 v75, v80, v81
	v_pk_add_f32 v[70:71], v[70:71], 0 op_sel_hi:[1,0]
	v_pk_add_f32 v[68:69], v[68:69], 0 op_sel_hi:[1,0]
	v_pk_add_f32 v[66:67], v[66:67], 0 op_sel_hi:[1,0]
	v_cvt_pk_bf16_f32 v76, v76, v77
	v_cvt_pk_bf16_f32 v77, v84, v85
	global_store_dwordx4 v[78:79], v[74:77], off
	v_pk_add_f32 v[72:73], v[72:73], 0 op_sel_hi:[1,0]
	v_pk_mul_f32 v[70:71], v[146:147], v[70:71] op_sel_hi:[0,1]
	v_pk_mul_f32 v[74:75], v[146:147], v[68:69] op_sel_hi:[0,1]
	v_pk_mul_f32 v[68:69], v[146:147], v[66:67] op_sel_hi:[0,1]
	v_cvt_pk_bf16_f32 v66, v70, v71
	v_pk_mul_f32 v[72:73], v[146:147], v[72:73] op_sel_hi:[0,1]
	v_cvt_pk_bf16_f32 v67, v72, v73
	v_cvt_pk_bf16_f32 v68, v68, v69
	v_cvt_pk_bf16_f32 v69, v74, v75
	global_store_dwordx4 v[78:79], v[66:69], off offset:256
	v_pk_add_f32 v[64:65], v[64:65], 0 op_sel_hi:[1,0]
	v_pk_add_f32 v[62:63], v[62:63], 0 op_sel_hi:[1,0]
	v_add_u32_e32 v66, 0x80, v155
	v_pk_add_f32 v[60:61], v[60:61], 0 op_sel_hi:[1,0]
	v_pk_add_f32 v[58:59], v[58:59], 0 op_sel_hi:[1,0]
	v_mad_i64_i32 v[66:67], s[22:23], v66, s46, v[148:149]
	v_pk_mul_f32 v[64:65], v[146:147], v[64:65] op_sel_hi:[0,1]
	v_pk_mul_f32 v[62:63], v[146:147], v[62:63] op_sel_hi:[0,1]
	v_pk_mul_f32 v[68:69], v[146:147], v[60:61] op_sel_hi:[0,1]
	v_pk_mul_f32 v[60:61], v[146:147], v[58:59] op_sel_hi:[0,1]
	v_cvt_pk_bf16_f32 v58, v62, v63
	v_cvt_pk_bf16_f32 v59, v64, v65
	v_pk_add_f32 v[48:49], v[48:49], 0 op_sel_hi:[1,0]
	v_pk_add_f32 v[46:47], v[46:47], 0 op_sel_hi:[1,0]
	v_cvt_pk_bf16_f32 v60, v60, v61
	v_cvt_pk_bf16_f32 v61, v68, v69
	global_store_dwordx4 v[66:67], v[58:61], off
	v_pk_add_f32 v[56:57], v[56:57], 0 op_sel_hi:[1,0]
	v_pk_add_f32 v[54:55], v[54:55], 0 op_sel_hi:[1,0]
	v_pk_mul_f32 v[58:59], v[146:147], v[48:49] op_sel_hi:[0,1]
	v_pk_mul_f32 v[48:49], v[146:147], v[46:47] op_sel_hi:[0,1]
	v_pk_mul_f32 v[56:57], v[146:147], v[56:57] op_sel_hi:[0,1]
	v_pk_mul_f32 v[54:55], v[146:147], v[54:55] op_sel_hi:[0,1]
	v_cvt_pk_bf16_f32 v46, v54, v55
	v_cvt_pk_bf16_f32 v47, v56, v57
	v_cvt_pk_bf16_f32 v48, v48, v49
	v_cvt_pk_bf16_f32 v49, v58, v59
	global_store_dwordx4 v[66:67], v[46:49], off offset:256
	v_pk_add_f32 v[50:51], v[50:51], 0 op_sel_hi:[1,0]
	v_pk_add_f32 v[44:45], v[44:45], 0 op_sel_hi:[1,0]
	v_add_u32_e32 v46, 0x90, v155
	v_pk_add_f32 v[48:49], v[52:53], 0 op_sel_hi:[1,0]
	v_pk_add_f32 v[42:43], v[42:43], 0 op_sel_hi:[1,0]
	v_mad_i64_i32 v[46:47], s[22:23], v46, s46, v[148:149]
	v_pk_mul_f32 v[48:49], v[146:147], v[48:49] op_sel_hi:[0,1]
	v_pk_mul_f32 v[50:51], v[146:147], v[50:51] op_sel_hi:[0,1]
	v_pk_mul_f32 v[52:53], v[146:147], v[44:45] op_sel_hi:[0,1]
	v_pk_mul_f32 v[44:45], v[146:147], v[42:43] op_sel_hi:[0,1]
	v_cvt_pk_bf16_f32 v42, v50, v51
	v_cvt_pk_bf16_f32 v43, v48, v49
	v_pk_add_f32 v[32:33], v[32:33], 0 op_sel_hi:[1,0]
	v_pk_add_f32 v[30:31], v[30:31], 0 op_sel_hi:[1,0]
	v_cvt_pk_bf16_f32 v44, v44, v45
	v_cvt_pk_bf16_f32 v45, v52, v53
	global_store_dwordx4 v[46:47], v[42:45], off
	v_pk_add_f32 v[40:41], v[40:41], 0 op_sel_hi:[1,0]
	v_pk_add_f32 v[38:39], v[38:39], 0 op_sel_hi:[1,0]
	v_pk_mul_f32 v[42:43], v[146:147], v[32:33] op_sel_hi:[0,1]
	v_pk_mul_f32 v[32:33], v[146:147], v[30:31] op_sel_hi:[0,1]
	v_pk_mul_f32 v[40:41], v[146:147], v[40:41] op_sel_hi:[0,1]
	v_pk_mul_f32 v[38:39], v[146:147], v[38:39] op_sel_hi:[0,1]
	v_cvt_pk_bf16_f32 v30, v38, v39
	v_cvt_pk_bf16_f32 v31, v40, v41
	v_cvt_pk_bf16_f32 v32, v32, v33
	v_cvt_pk_bf16_f32 v33, v42, v43
	global_store_dwordx4 v[46:47], v[30:33], off offset:256
	v_pk_add_f32 v[34:35], v[34:35], 0 op_sel_hi:[1,0]
	v_pk_add_f32 v[28:29], v[28:29], 0 op_sel_hi:[1,0]
	v_add_u32_e32 v30, 0xa0, v155
	v_pk_add_f32 v[32:33], v[36:37], 0 op_sel_hi:[1,0]
	v_pk_add_f32 v[26:27], v[26:27], 0 op_sel_hi:[1,0]
	v_mad_i64_i32 v[30:31], s[22:23], v30, s46, v[148:149]
	v_pk_mul_f32 v[32:33], v[146:147], v[32:33] op_sel_hi:[0,1]
	v_pk_mul_f32 v[34:35], v[146:147], v[34:35] op_sel_hi:[0,1]
	v_pk_mul_f32 v[36:37], v[146:147], v[28:29] op_sel_hi:[0,1]
	v_pk_mul_f32 v[28:29], v[146:147], v[26:27] op_sel_hi:[0,1]
	v_cvt_pk_bf16_f32 v26, v34, v35
	v_cvt_pk_bf16_f32 v27, v32, v33
	v_pk_add_f32 v[16:17], v[16:17], 0 op_sel_hi:[1,0]
	v_pk_add_f32 v[14:15], v[14:15], 0 op_sel_hi:[1,0]
	v_cvt_pk_bf16_f32 v28, v28, v29
	v_cvt_pk_bf16_f32 v29, v36, v37
	global_store_dwordx4 v[30:31], v[26:29], off
	v_pk_add_f32 v[24:25], v[24:25], 0 op_sel_hi:[1,0]
	v_pk_add_f32 v[22:23], v[22:23], 0 op_sel_hi:[1,0]
	v_pk_mul_f32 v[26:27], v[146:147], v[16:17] op_sel_hi:[0,1]
	v_pk_mul_f32 v[16:17], v[146:147], v[14:15] op_sel_hi:[0,1]
	v_pk_mul_f32 v[24:25], v[146:147], v[24:25] op_sel_hi:[0,1]
	v_pk_mul_f32 v[22:23], v[146:147], v[22:23] op_sel_hi:[0,1]
	v_cvt_pk_bf16_f32 v14, v22, v23
	v_cvt_pk_bf16_f32 v15, v24, v25
	v_cvt_pk_bf16_f32 v16, v16, v17
	v_cvt_pk_bf16_f32 v17, v26, v27
	global_store_dwordx4 v[30:31], v[14:17], off offset:256
	v_pk_add_f32 v[18:19], v[18:19], 0 op_sel_hi:[1,0]
	v_pk_add_f32 v[12:13], v[12:13], 0 op_sel_hi:[1,0]
	v_add_u32_e32 v14, 0xb0, v155
	v_pk_add_f32 v[16:17], v[20:21], 0 op_sel_hi:[1,0]
	v_pk_add_f32 v[10:11], v[10:11], 0 op_sel_hi:[1,0]
	v_mad_i64_i32 v[14:15], s[22:23], v14, s46, v[148:149]
	v_pk_mul_f32 v[16:17], v[146:147], v[16:17] op_sel_hi:[0,1]
	v_pk_mul_f32 v[18:19], v[146:147], v[18:19] op_sel_hi:[0,1]
	v_pk_mul_f32 v[20:21], v[146:147], v[12:13] op_sel_hi:[0,1]
	v_pk_mul_f32 v[12:13], v[146:147], v[10:11] op_sel_hi:[0,1]
	v_cvt_pk_bf16_f32 v10, v18, v19
	v_cvt_pk_bf16_f32 v11, v16, v17
	v_pk_add_f32 v[4:5], v[4:5], 0 op_sel_hi:[1,0]
	v_pk_add_f32 v[2:3], v[2:3], 0 op_sel_hi:[1,0]
	v_cvt_pk_bf16_f32 v12, v12, v13
	v_cvt_pk_bf16_f32 v13, v20, v21
	global_store_dwordx4 v[14:15], v[10:13], off
	v_pk_add_f32 v[8:9], v[8:9], 0 op_sel_hi:[1,0]
	v_pk_add_f32 v[6:7], v[6:7], 0 op_sel_hi:[1,0]
	v_pk_mul_f32 v[10:11], v[146:147], v[4:5] op_sel_hi:[0,1]
	v_pk_mul_f32 v[4:5], v[146:147], v[2:3] op_sel_hi:[0,1]
	s_andn2_b64 vcc, exec, s[4:5]
	s_mov_b64 s[4:5], -1
	v_and_b32_e32 v208, 63, v0
	v_pk_mul_f32 v[8:9], v[146:147], v[8:9] op_sel_hi:[0,1]
	v_pk_mul_f32 v[6:7], v[146:147], v[6:7] op_sel_hi:[0,1]
	v_cvt_pk_bf16_f32 v2, v6, v7
	v_cvt_pk_bf16_f32 v3, v8, v9
	v_cvt_pk_bf16_f32 v4, v4, v5
	v_cvt_pk_bf16_f32 v5, v10, v11
	global_store_dwordx4 v[14:15], v[2:5], off offset:256
	s_cbranch_vccnz .LBB0_295
	s_andn2_b64 vcc, exec, s[6:7]
	s_cbranch_vccnz .LBB0_294
	s_barrier
	s_branch .LBB0_294

.LBB0_444:
	s_mov_b64 s[10:11], exec
	s_lshl_b32 s8, s86, 8
	v_mbcnt_lo_u32_b32 v2, s10, 0
	s_add_u32 s8, s84, s8
	v_mbcnt_hi_u32_b32 v2, s11, v2
	s_addc_u32 s9, s85, 0
	v_cmp_eq_u32_e32 vcc, 0, v2
	s_and_saveexec_b64 s[12:13], vcc
	s_cbranch_execz .LBB0_446
	s_bcnt1_i32_b64 s10, s[10:11]
	v_mov_b32_e32 v4, 0x1000
	v_mov_b32_e32 v5, s10
	global_atomic_add v4, v4, v5, s[8:9] offset:1024 sc0
	buffer_inv sc1

.LBB0_459:
	s_or_b64 exec, exec, s[12:13]
	s_waitcnt vmcnt(0)
	s_waitcnt vmcnt(0)

.LBB0_477:
	s_or_b64 exec, exec, s[10:11]
	s_mov_b64 s[10:11], exec
	v_mbcnt_lo_u32_b32 v1, s10, 0
	v_mbcnt_hi_u32_b32 v1, s11, v1
	v_cmp_eq_u32_e32 vcc, 0, v1
	s_waitcnt vmcnt(0)
	s_and_saveexec_b64 s[12:13], vcc
	s_cbranch_execz .LBB0_479
	s_bcnt1_i32_b64 s10, s[10:11]
	v_mov_b32_e32 v1, 0x2000
	v_mov_b32_e32 v2, s10
	global_atomic_add v1, v2, s[8:9] offset:1024

.LBB0_584:
	s_waitcnt vmcnt(0)
	v_pk_mul_f32 v[86:87], v[86:87], v[94:95] op_sel_hi:[1,0]
	v_add_u32_e32 v38, 0x8000, v57
	v_pk_mul_f32 v[84:85], v[84:85], v[94:95] op_sel_hi:[1,0]
	ds_write2_b32 v38, v86, v87 offset1:1
	v_add_u32_e32 v38, 0x8008, v57
	ds_write2_b32 v38, v84, v85 offset1:1
	v_pk_mul_f32 v[80:81], v[80:81], v[92:93] op_sel_hi:[1,0]
	v_add_u32_e32 v38, 0x8000, v67
	v_pk_mul_f32 v[78:79], v[78:79], v[92:93] op_sel_hi:[1,0]
	ds_write2_b32 v38, v80, v81 offset1:1
	v_add_u32_e32 v38, 0x8008, v67
	ds_write2_b32 v38, v78, v79 offset1:1
	v_pk_mul_f32 v[76:77], v[76:77], v[90:91] op_sel_hi:[1,0]
	v_add_u32_e32 v38, 0x8420, v67
	v_pk_mul_f32 v[74:75], v[74:75], v[90:91] op_sel_hi:[1,0]
	ds_write2_b32 v38, v76, v77 offset1:1
	v_add_u32_e32 v38, 0x8428, v67
	ds_write2_b32 v38, v74, v75 offset1:1
	v_pk_mul_f32 v[70:71], v[70:71], v[88:89] op_sel_hi:[1,0]
	v_add_u32_e32 v38, 0x8840, v67
	v_pk_mul_f32 v[68:69], v[68:69], v[88:89] op_sel_hi:[1,0]
	ds_write2_b32 v38, v70, v71 offset1:1
	v_add_u32_e32 v38, 0x8848, v67
	ds_write2_b32 v38, v68, v69 offset1:1
	v_pk_mul_f32 v[64:65], v[64:65], v[82:83] op_sel_hi:[1,0]
	v_add_u32_e32 v38, 0x8c60, v67
	v_pk_mul_f32 v[62:63], v[62:63], v[82:83] op_sel_hi:[1,0]
	ds_write2_b32 v38, v64, v65 offset1:1
	v_add_u32_e32 v38, 0x8c68, v67
	ds_write2_b32 v38, v62, v63 offset1:1
	v_pk_mul_f32 v[60:61], v[60:61], v[72:73] op_sel_hi:[1,0]
	v_add_u32_e32 v38, 0x9080, v67
	v_pk_mul_f32 v[58:59], v[58:59], v[72:73] op_sel_hi:[1,0]
	ds_write2_b32 v38, v60, v61 offset1:1
	v_add_u32_e32 v38, 0x9088, v67
	ds_write2_b32 v38, v58, v59 offset1:1
	v_pk_mul_f32 v[54:55], v[54:55], v[66:67] op_sel_hi:[1,0]
	v_add_u32_e32 v38, 0x94a0, v67
	v_pk_mul_f32 v[52:53], v[52:53], v[66:67] op_sel_hi:[1,0]
	ds_write2_b32 v38, v54, v55 offset1:1
	v_add_u32_e32 v38, 0x94a8, v67
	ds_write2_b32 v38, v52, v53 offset1:1
	v_pk_mul_f32 v[2:3], v[2:3], v[56:57] op_sel_hi:[1,0]
	v_add_u32_e32 v38, 0x98c0, v67
	v_pk_mul_f32 v[4:5], v[4:5], v[56:57] op_sel_hi:[1,0]
	ds_write2_b32 v38, v2, v3 offset1:1
	v_add_u32_e32 v2, 0x98c8, v67
	ds_write2_b32 v2, v4, v5 offset1:1
	s_waitcnt lgkmcnt(0)
	v_add_u32_e32 v38, 0x8000, v47
	ds_read2_b32 v[2:3], v38 offset1:33
	ds_read2_b32 v[4:5], v38 offset0:66 offset1:99
	ds_read2_b32 v[54:55], v38 offset0:132 offset1:165
	ds_read2_b32 v[58:59], v38 offset0:198 offset1:231
	v_mov_b32_e32 v51, v39
	v_lshl_add_u64 v[52:53], s[8:9], 0, v[50:51]
	s_cmp_lg_u32 s6, 0
	s_waitcnt lgkmcnt(3)
	v_cvt_pk_bf16_f32 v2, v2, v3
	s_waitcnt lgkmcnt(2)
	v_cvt_pk_bf16_f32 v3, v4, v5
	s_waitcnt lgkmcnt(1)
	v_cvt_pk_bf16_f32 v4, v54, v55
	v_mad_u64_u32 v[54:55], s[4:5], s35, v40, 0
	s_cselect_b64 s[8:9], -1, 0
	s_cmp_eq_u32 s6, 0
	s_waitcnt lgkmcnt(0)
	v_cvt_pk_bf16_f32 v5, v58, v59
	v_lshl_add_u64 v[54:55], v[54:55], 1, v[52:53]
	global_store_dwordx4 v[54:55], v[2:5], off
	s_cbranch_scc1 .LBB0_586
	v_lshl_add_u64 v[54:55], s[6:7], 1, v[54:55]
	global_store_dwordx4 v[54:55], v[2:5], off
.LBB0_586:
	ds_read2_b32 v[2:3], v38 offset0:8 offset1:41
	ds_read2_b32 v[4:5], v38 offset0:74 offset1:107
	ds_read2_b32 v[54:55], v38 offset0:206 offset1:239
	v_cndmask_b32_e64 v51, 0, 1, s[8:9]
	s_andn2_b64 vcc, exec, s[8:9]
	s_waitcnt lgkmcnt(2)
	v_cvt_pk_bf16_f32 v2, v2, v3
	s_waitcnt lgkmcnt(1)
	v_cvt_pk_bf16_f32 v3, v4, v5
	ds_read2_b32 v[4:5], v38 offset0:140 offset1:173
	s_waitcnt lgkmcnt(0)
	v_cvt_pk_bf16_f32 v4, v4, v5
	v_cvt_pk_bf16_f32 v5, v54, v55
	v_mad_u64_u32 v[54:55], s[4:5], s35, v42, 0
	v_lshl_add_u64 v[54:55], v[54:55], 1, v[52:53]
	v_cmp_ne_u32_e64 s[4:5], 1, v51
	global_store_dwordx4 v[54:55], v[2:5], off
	s_cbranch_vccnz .LBB0_588
	v_lshl_add_u64 v[54:55], s[6:7], 1, v[54:55]
	global_store_dwordx4 v[54:55], v[2:5], off
.LBB0_588:
	ds_read2_b32 v[2:3], v38 offset0:16 offset1:49
	ds_read2_b32 v[4:5], v38 offset0:82 offset1:115
	ds_read2_b32 v[54:55], v38 offset0:214 offset1:247
	s_and_b64 vcc, exec, s[4:5]
	s_waitcnt lgkmcnt(2)
	v_cvt_pk_bf16_f32 v2, v2, v3
	s_waitcnt lgkmcnt(1)
	v_cvt_pk_bf16_f32 v3, v4, v5
	ds_read2_b32 v[4:5], v38 offset0:148 offset1:181
	s_waitcnt lgkmcnt(0)
	v_cvt_pk_bf16_f32 v4, v4, v5
	v_cvt_pk_bf16_f32 v5, v54, v55
	v_mad_u64_u32 v[54:55], s[8:9], s35, v44, 0
	v_lshl_add_u64 v[54:55], v[54:55], 1, v[52:53]
	global_store_dwordx4 v[54:55], v[2:5], off
	s_cbranch_vccnz .LBB0_590
	v_lshl_add_u64 v[54:55], s[6:7], 1, v[54:55]
	global_store_dwordx4 v[54:55], v[2:5], off
.LBB0_590:
	ds_read2_b32 v[2:3], v38 offset0:24 offset1:57
	ds_read2_b32 v[4:5], v38 offset0:90 offset1:123
	ds_read2_b32 v[54:55], v38 offset0:222 offset1:255
	s_and_b64 vcc, exec, s[4:5]
	s_waitcnt lgkmcnt(2)
	v_cvt_pk_bf16_f32 v2, v2, v3
	s_waitcnt lgkmcnt(1)
	v_cvt_pk_bf16_f32 v3, v4, v5
	ds_read2_b32 v[4:5], v38 offset0:156 offset1:189
	s_waitcnt lgkmcnt(0)
	v_cvt_pk_bf16_f32 v4, v4, v5
	v_cvt_pk_bf16_f32 v5, v54, v55
	v_mad_u64_u32 v[54:55], s[8:9], s35, v46, 0
	v_lshl_add_u64 v[52:53], v[54:55], 1, v[52:53]
	global_store_dwordx4 v[52:53], v[2:5], off
	s_cbranch_vccnz .LBB0_542
	v_lshl_add_u64 v[52:53], s[6:7], 1, v[52:53]
	global_store_dwordx4 v[52:53], v[2:5], off
	s_branch .LBB0_542

.LBB0_618:
	s_mov_b64 s[58:59], exec
	v_mbcnt_lo_u32_b32 v7, s58, 0
	v_mbcnt_hi_u32_b32 v7, s59, v7
	v_cmp_eq_u32_e32 vcc, 0, v7
	s_and_saveexec_b64 s[56:57], vcc
	s_cbranch_execz .LBB0_620
	s_bcnt1_i32_b64 s6, s[58:59]
	v_readlane_b32 s44, v255, 3
	v_mov_b32_e32 v10, s6
	v_readlane_b32 s45, v255, 4
	s_nop 4
	global_atomic_add v10, v6, v10, s[44:45] sc0
	buffer_inv sc1

.LBB0_633:
	s_or_b64 exec, exec, s[58:59]
	s_waitcnt vmcnt(0)
	s_waitcnt vmcnt(0)

.LBB0_651:
	s_or_b64 exec, exec, s[56:57]
	s_mov_b64 s[56:57], exec
	v_mbcnt_lo_u32_b32 v7, s56, 0
	v_mbcnt_hi_u32_b32 v7, s57, v7
	v_cmp_eq_u32_e32 vcc, 0, v7
	s_waitcnt vmcnt(0)
	s_and_saveexec_b64 s[58:59], vcc
	s_cbranch_execz .LBB0_653
	s_bcnt1_i32_b64 s6, s[56:57]
	v_mov_b32_e32 v7, s6
	global_atomic_add v6, v7, s[38:39]

.LBB0_742:
	s_or_b64 exec, exec, s[80:81]
	ds_bpermute_b32 v41, v241, v120
	ds_bpermute_b32 v40, v241, v119
	ds_bpermute_b32 v7, v241, v118
	v_mov_b32_e32 v42, v114
	v_mov_b32_e32 v43, v94
	s_waitcnt lgkmcnt(2)
	v_max_f32_e64 v41, |v41|, |v41|
	v_max_f32_e32 v45, 1.0, v41
	ds_bpermute_b32 v41, v241, v121
	s_waitcnt lgkmcnt(2)
	v_max_f32_e64 v40, |v40|, |v40|
	v_max_f32_e32 v40, 1.0, v40
	s_waitcnt lgkmcnt(1)
	v_max_f32_e64 v7, |v7|, |v7|
	v_max_f32_e32 v7, 1.0, v7
	s_waitcnt lgkmcnt(0)
	v_max_f32_e64 v41, |v41|, |v41|
	v_max_f32_e32 v47, 1.0, v41
	v_div_scale_f32 v41, s[80:81], v40, v40, 1.0
	v_rcp_f32_e32 v49, v41
	v_mov_b32_e32 v94, v115
	s_waitcnt lgkmcnt(0)
	s_barrier
	v_fma_f32 v51, -v41, v49, 1.0
	v_fmac_f32_e32 v49, v51, v49
	v_div_scale_f32 v51, vcc, 1.0, v40, 1.0
	v_mul_f32_e32 v52, v51, v49
	v_fma_f32 v53, -v41, v52, v51
	v_fmac_f32_e32 v52, v53, v49
	v_fma_f32 v41, -v41, v52, v51
	v_div_fmas_f32 v41, v41, v49, v52
	v_div_fixup_f32 v53, v41, v40, 1.0
	v_div_scale_f32 v40, s[80:81], v7, v7, 1.0
	v_rcp_f32_e32 v41, v40
	s_nop 0
	v_fma_f32 v49, -v40, v41, 1.0
	v_fmac_f32_e32 v41, v49, v41
	v_div_scale_f32 v49, vcc, 1.0, v7, 1.0
	v_mul_f32_e32 v51, v49, v41
	v_fma_f32 v52, -v40, v51, v49
	v_fmac_f32_e32 v51, v52, v41
	v_fma_f32 v40, -v40, v51, v49
	v_div_fmas_f32 v40, v40, v41, v51
	v_div_fixup_f32 v52, v40, v7, 1.0
	v_div_scale_f32 v7, s[80:81], v47, v47, 1.0
	v_pk_mul_f32 v[122:123], v[74:75], v[52:53]
	v_pk_mul_f32 v[74:75], v[42:43], v[52:53] op_sel_hi:[1,0]
	v_rcp_f32_e32 v42, v7
	v_pk_mul_f32 v[128:129], v[62:63], v[52:53]
	v_pk_mul_f32 v[132:133], v[54:55], v[52:53]
	v_pk_mul_f32 v[40:41], v[128:129], v[128:129]
	v_fma_f32 v43, -v7, v42, 1.0
	v_fmac_f32_e32 v42, v43, v42
	v_div_scale_f32 v43, vcc, 1.0, v47, 1.0
	v_mul_f32_e32 v49, v43, v42
	v_fma_f32 v51, -v7, v49, v43
	v_fmac_f32_e32 v49, v51, v42
	v_fma_f32 v7, -v7, v49, v43
	v_div_fmas_f32 v7, v7, v42, v49
	v_div_fixup_f32 v143, v7, v47, 1.0
	v_div_scale_f32 v7, s[80:81], v45, v45, 1.0
	v_rcp_f32_e32 v42, v7
	v_pk_fma_f32 v[40:41], v[132:133], v[132:133], v[40:41]
	v_pk_mul_f32 v[124:125], v[58:59], v[52:53]
	v_pk_mul_f32 v[120:121], v[70:71], v[52:53]
	v_fma_f32 v43, -v7, v42, 1.0
	v_fmac_f32_e32 v42, v43, v42
	v_div_scale_f32 v43, vcc, 1.0, v45, 1.0
	v_mul_f32_e32 v47, v43, v42
	v_fma_f32 v49, -v7, v47, v43
	v_pk_fma_f32 v[40:41], v[124:125], v[124:125], v[40:41]
	v_fmac_f32_e32 v47, v49, v42
	v_pk_fma_f32 v[40:41], v[122:123], v[122:123], v[40:41]
	v_fma_f32 v7, -v7, v47, v43
	v_pk_fma_f32 v[40:41], v[120:121], v[120:121], v[40:41]
	v_pk_mul_f32 v[118:119], v[66:67], v[52:53]
	v_div_fmas_f32 v7, v7, v42, v47
	v_pk_fma_f32 v[40:41], v[118:119], v[118:119], v[40:41]
	v_pk_mul_f32 v[114:115], v[78:79], v[52:53]
	v_div_fixup_f32 v142, v7, v45, 1.0
	v_pk_fma_f32 v[54:55], v[114:115], v[114:115], v[40:41]
	v_pk_mul_f32 v[40:41], v[90:91], v[52:53]
	v_pk_mul_f32 v[130:131], v[64:65], v[142:143]
	v_pk_fma_f32 v[54:55], v[40:41], v[40:41], v[54:55]
	v_pk_mul_f32 v[86:87], v[86:87], v[52:53]
	v_pk_mul_f32 v[134:135], v[56:57], v[142:143]
	v_pk_mul_f32 v[42:43], v[130:131], v[130:131]
	v_pk_fma_f32 v[54:55], v[86:87], v[86:87], v[54:55]
	v_pk_mul_f32 v[78:79], v[82:83], v[52:53]
	v_pk_fma_f32 v[42:43], v[134:135], v[134:135], v[42:43]
	v_pk_mul_f32 v[126:127], v[60:61], v[142:143]
	v_pk_fma_f32 v[136:137], v[78:79], v[78:79], v[54:55]
	v_mov_b32_e32 v54, v53
	v_mov_b32_e32 v58, v116
	v_mov_b32_e32 v59, v96
	v_mov_b32_e32 v96, v117
	v_pk_fma_f32 v[42:43], v[126:127], v[126:127], v[42:43]
	v_pk_mul_f32 v[116:117], v[76:77], v[142:143]
	v_pk_mul_f32 v[70:71], v[94:95], v[54:55] op_sel_hi:[1,0]
	v_pk_fma_f32 v[42:43], v[116:117], v[116:117], v[42:43]
	v_pk_mul_f32 v[94:95], v[72:73], v[142:143]
	v_pk_mul_f32 v[90:91], v[68:69], v[142:143]
	v_pk_fma_f32 v[42:43], v[94:95], v[94:95], v[42:43]
	v_pk_mul_f32 v[82:83], v[80:81], v[142:143]
	v_pk_fma_f32 v[42:43], v[90:91], v[90:91], v[42:43]
	v_pk_mul_f32 v[80:81], v[88:89], v[142:143]
	v_pk_fma_f32 v[56:57], v[82:83], v[82:83], v[42:43]
	v_pk_mul_f32 v[42:43], v[92:93], v[142:143]
	v_pk_mul_f32 v[76:77], v[84:85], v[142:143]
	v_pk_fma_f32 v[56:57], v[42:43], v[42:43], v[56:57]
	v_pk_mul_f32 v[138:139], v[74:75], v[74:75]
	v_pk_fma_f32 v[56:57], v[80:81], v[80:81], v[56:57]
	v_pk_mul_f32 v[140:141], v[70:71], v[70:71]
	v_pk_fma_f32 v[88:89], v[76:77], v[76:77], v[56:57]
	v_mov_b32_e32 v56, v106
	v_mov_b32_e32 v57, v102
	v_pk_mul_f32 v[62:63], v[56:57], v[52:53] op_sel_hi:[1,0]
	v_mov_b32_e32 v56, v108
	v_mov_b32_e32 v57, v104
	v_pk_mul_f32 v[66:67], v[56:57], v[142:143] op_sel_hi:[1,0]
	v_mov_b32_e32 v56, v110
	v_mov_b32_e32 v57, v98
	v_mov_b32_e32 v84, v143
	v_mov_b32_e32 v102, v107
	v_mov_b32_e32 v104, v109
	v_pk_mul_f32 v[56:57], v[56:57], v[52:53] op_sel_hi:[1,0]
	v_mov_b32_e32 v98, v111
	v_mov_b32_e32 v52, v112
	v_mov_b32_e32 v53, v100
	v_mov_b32_e32 v100, v113
	v_pk_mul_f32 v[72:73], v[58:59], v[142:143] op_sel_hi:[1,0]
	v_pk_mul_f32 v[68:69], v[96:97], v[84:85] op_sel_hi:[1,0]
	v_pk_mul_f32 v[64:65], v[102:103], v[54:55] op_sel_hi:[1,0]
	v_pk_mul_f32 v[60:61], v[104:105], v[84:85] op_sel_hi:[1,0]
	v_pk_mul_f32 v[58:59], v[98:99], v[54:55] op_sel_hi:[1,0]
	v_pk_mul_f32 v[54:55], v[52:53], v[142:143] op_sel_hi:[1,0]
	v_pk_mul_f32 v[52:53], v[100:101], v[84:85] op_sel_hi:[1,0]
	v_mov_b32_e32 v85, v138
	v_mov_b32_e32 v138, v141
	v_pk_mul_f32 v[144:145], v[62:63], v[62:63]
	v_pk_mul_f32 v[102:103], v[64:65], v[64:65]
	v_mov_b32_e32 v84, v140
	v_pk_add_f32 v[112:113], v[138:139], v[136:137] op_sel:[0,1] op_sel_hi:[1,0]
	v_pk_mul_f32 v[108:109], v[56:57], v[56:57]
	v_pk_add_f32 v[84:85], v[84:85], v[112:113]
	v_mov_b32_e32 v112, v103
	v_mov_b32_e32 v113, v145
	v_pk_mul_f32 v[98:99], v[58:59], v[58:59]
	v_pk_add_f32 v[84:85], v[112:113], v[84:85]
	v_mov_b32_e32 v103, v144
	v_pk_add_f32 v[84:85], v[102:103], v[84:85]
	v_mov_b32_e32 v102, v99
	v_mov_b32_e32 v103, v109
	v_pk_add_f32 v[84:85], v[102:103], v[84:85]
	v_mov_b32_e32 v99, v108
	v_pk_add_f32 v[84:85], v[98:99], v[84:85]
	ds_bpermute_b32 v99, v242, v85
	ds_bpermute_b32 v98, v242, v84
	v_pk_mul_f32 v[92:93], v[72:73], v[72:73]
	v_pk_mul_f32 v[96:97], v[68:69], v[68:69]
	v_mov_b32_e32 v103, v92
	v_mov_b32_e32 v92, v97
	s_waitcnt lgkmcnt(0)
	v_pk_add_f32 v[84:85], v[84:85], v[98:99]
	ds_bpermute_b32 v99, v243, v85
	ds_bpermute_b32 v98, v243, v84
	v_pk_mul_f32 v[106:107], v[66:67], v[66:67]
	v_pk_mul_f32 v[104:105], v[60:61], v[60:61]
	v_mov_b32_e32 v102, v96
	v_pk_add_f32 v[88:89], v[92:93], v[88:89] op_sel:[0,1] op_sel_hi:[1,0]
	v_mov_b32_e32 v92, v105
	v_pk_add_f32 v[88:89], v[102:103], v[88:89]
	v_mov_b32_e32 v93, v107
	v_pk_mul_f32 v[110:111], v[54:55], v[54:55]
	v_pk_mul_f32 v[100:101], v[52:53], v[52:53]
	v_pk_add_f32 v[88:89], v[92:93], v[88:89]
	v_mov_b32_e32 v105, v106
	s_waitcnt lgkmcnt(0)
	v_pk_add_f32 v[84:85], v[84:85], v[98:99]
	v_pk_add_f32 v[88:89], v[104:105], v[88:89]
	v_mov_b32_e32 v92, v101
	v_mov_b32_e32 v93, v111
	ds_bpermute_b32 v99, v244, v85
	ds_bpermute_b32 v98, v244, v84
	v_pk_add_f32 v[88:89], v[92:93], v[88:89]
	v_mov_b32_e32 v101, v110
	v_pk_add_f32 v[88:89], v[100:101], v[88:89]
	ds_bpermute_b32 v93, v242, v89
	ds_bpermute_b32 v92, v242, v88
	s_waitcnt lgkmcnt(2)
	v_pk_add_f32 v[84:85], v[84:85], v[98:99]
	ds_bpermute_b32 v99, v245, v85
	ds_bpermute_b32 v98, v245, v84
	s_mov_b32 s80, 0x358637bd
	s_waitcnt lgkmcnt(2)
	v_pk_add_f32 v[88:89], v[88:89], v[92:93]
	ds_bpermute_b32 v93, v243, v89
	ds_bpermute_b32 v92, v243, v88
	s_waitcnt lgkmcnt(2)
	v_pk_add_f32 v[84:85], v[84:85], v[98:99]
	v_mov_b64_e32 v[98:99], s[80:81]
	v_pk_fma_f32 v[84:85], v[84:85], s[8:9], v[98:99] op_sel_hi:[1,0,0]
	s_waitcnt lgkmcnt(0)
	v_pk_add_f32 v[88:89], v[88:89], v[92:93]
	v_mul_f32_e32 v7, 0x4b800000, v85
	v_cmp_gt_f32_e64 s[80:81], s42, v85
	ds_bpermute_b32 v93, v244, v89
	ds_bpermute_b32 v92, v244, v88
	v_cndmask_b32_e64 v7, v85, v7, s[80:81]
	v_rsq_f32_e32 v7, v7
	v_cmp_gt_f32_e32 vcc, s42, v84
	s_waitcnt lgkmcnt(0)
	v_pk_add_f32 v[88:89], v[88:89], v[92:93]
	v_mul_f32_e32 v45, 0x45800000, v7
	v_cndmask_b32_e64 v7, v7, v45, s[80:81]
	v_mul_f32_e32 v45, 0x4b800000, v84
	ds_bpermute_b32 v93, v245, v89
	ds_bpermute_b32 v92, v245, v88
	v_cndmask_b32_e32 v45, v84, v45, vcc
	v_rsq_f32_e32 v45, v45
	v_mul_f32_e32 v40, v40, v7
	s_waitcnt lgkmcnt(0)
	v_pk_add_f32 v[88:89], v[88:89], v[92:93]
	v_mul_f32_e32 v47, 0x45800000, v45
	v_pk_fma_f32 v[88:89], v[88:89], s[8:9], v[98:99] op_sel_hi:[1,0,0]
	v_cndmask_b32_e32 v84, v45, v47, vcc
	v_mul_f32_e32 v45, 0x4b800000, v89
	v_cmp_gt_f32_e64 s[80:81], s42, v89
	v_cmp_gt_f32_e32 vcc, s42, v88
	s_nop 0
	v_cndmask_b32_e64 v45, v89, v45, s[80:81]
	v_rsq_f32_e32 v45, v45
	s_nop 0
	v_mul_f32_e32 v47, 0x45800000, v45
	v_cndmask_b32_e64 v85, v45, v47, s[80:81]
	v_mul_f32_e32 v45, 0x4b800000, v88
	v_cndmask_b32_e32 v45, v88, v45, vcc
	v_rsq_f32_e32 v45, v45
	s_nop 0
	v_mul_f32_e32 v47, 0x45800000, v45
	v_cndmask_b32_e32 v88, v45, v47, vcc
	global_load_dword v45, v[194:195], off
	v_mul_f32_e32 v47, v132, v7
	s_waitcnt vmcnt(0)
	v_mul_f32_e32 v47, v45, v47
	v_bfe_u32 v49, v47, 16, 1
	v_add3_u32 v47, v47, v49, s14
	ds_write_b16_d16_hi v238, v47
	v_mul_f32_e32 v47, v133, v84
	v_mul_f32_e32 v47, v45, v47
	v_bfe_u32 v49, v47, 16, 1
	v_add3_u32 v47, v47, v49, s14
	ds_write_b16_d16_hi v238, v47 offset:272
	v_mul_f32_e32 v47, v134, v85
	v_mul_f32_e32 v47, v45, v47
	v_bfe_u32 v49, v47, 16, 1
	v_add3_u32 v47, v47, v49, s14
	ds_write_b16_d16_hi v238, v47 offset:544
	v_mul_f32_e32 v47, v135, v88
	v_mul_f32_e32 v45, v45, v47
	v_bfe_u32 v47, v45, 16, 1
	v_add3_u32 v45, v45, v47, s14
	ds_write_b16_d16_hi v238, v45 offset:816
	global_load_dword v45, v[194:195], off offset:64
	v_mul_f32_e32 v47, v128, v7
	s_waitcnt vmcnt(0)
	v_mul_f32_e32 v47, v45, v47
	v_bfe_u32 v49, v47, 16, 1
	v_add3_u32 v47, v47, v49, s14
	ds_write_b16_d16_hi v238, v47 offset:32
	v_mul_f32_e32 v47, v129, v84
	v_mul_f32_e32 v47, v45, v47
	v_bfe_u32 v49, v47, 16, 1
	v_add3_u32 v47, v47, v49, s14
	ds_write_b16_d16_hi v238, v47 offset:304
	v_mul_f32_e32 v47, v130, v85
	v_mul_f32_e32 v47, v45, v47
	v_bfe_u32 v49, v47, 16, 1
	v_add3_u32 v47, v47, v49, s14
	ds_write_b16_d16_hi v238, v47 offset:576
	v_mul_f32_e32 v47, v131, v88
	v_mul_f32_e32 v45, v45, v47
	v_bfe_u32 v47, v45, 16, 1
	v_add3_u32 v45, v45, v47, s14
	ds_write_b16_d16_hi v238, v45 offset:848
	global_load_dword v45, v[194:195], off offset:128
	v_mul_f32_e32 v47, v124, v7
	s_waitcnt vmcnt(0)
	v_mul_f32_e32 v47, v45, v47
	v_bfe_u32 v49, v47, 16, 1
	v_add3_u32 v47, v47, v49, s14
	ds_write_b16_d16_hi v238, v47 offset:64
	v_mul_f32_e32 v47, v125, v84
	v_mul_f32_e32 v47, v45, v47
	v_bfe_u32 v49, v47, 16, 1
	v_add3_u32 v47, v47, v49, s14
	ds_write_b16_d16_hi v238, v47 offset:336
	v_mul_f32_e32 v47, v126, v85
	v_mul_f32_e32 v47, v45, v47
	v_bfe_u32 v49, v47, 16, 1
	v_add3_u32 v47, v47, v49, s14
	ds_write_b16_d16_hi v238, v47 offset:608
	v_mul_f32_e32 v47, v127, v88
	v_mul_f32_e32 v45, v45, v47
	v_bfe_u32 v47, v45, 16, 1
	v_add3_u32 v45, v45, v47, s14
	ds_write_b16_d16_hi v238, v45 offset:880
	global_load_dword v45, v[194:195], off offset:192
	v_mul_f32_e32 v47, v122, v7
	s_waitcnt vmcnt(0)
	v_mul_f32_e32 v47, v47, v45
	v_bfe_u32 v49, v47, 16, 1
	v_add3_u32 v47, v47, v49, s14
	ds_write_b16_d16_hi v238, v47 offset:96
	v_mul_f32_e32 v47, v123, v84
	v_mul_f32_e32 v47, v47, v45
	v_bfe_u32 v49, v47, 16, 1
	v_add3_u32 v47, v47, v49, s14
	ds_write_b16_d16_hi v238, v47 offset:368
	v_mul_f32_e32 v47, v116, v85
	v_mul_f32_e32 v47, v45, v47
	v_bfe_u32 v49, v47, 16, 1
	v_add3_u32 v47, v47, v49, s14
	ds_write_b16_d16_hi v238, v47 offset:640
	v_mul_f32_e32 v47, v117, v88
	v_mul_f32_e32 v45, v45, v47
	v_bfe_u32 v47, v45, 16, 1
	v_add3_u32 v45, v45, v47, s14
	ds_write_b16_d16_hi v238, v45 offset:912
	global_load_dword v45, v[194:195], off offset:256
	v_mul_f32_e32 v47, v120, v7
	s_waitcnt vmcnt(0)
	v_mul_f32_e32 v47, v47, v45
	v_bfe_u32 v49, v47, 16, 1
	v_add3_u32 v47, v47, v49, s14
	ds_write_b16_d16_hi v238, v47 offset:128
	v_mul_f32_e32 v47, v121, v84
	v_mul_f32_e32 v47, v47, v45
	v_bfe_u32 v49, v47, 16, 1
	v_add3_u32 v47, v47, v49, s14
	ds_write_b16_d16_hi v238, v47 offset:400
	v_mul_f32_e32 v47, v94, v85
	v_mul_f32_e32 v47, v47, v45
	v_bfe_u32 v49, v47, 16, 1
	v_add3_u32 v47, v47, v49, s14
	ds_write_b16_d16_hi v238, v47 offset:672
	v_mul_f32_e32 v47, v95, v88
	v_mul_f32_e32 v45, v47, v45
	v_bfe_u32 v47, v45, 16, 1
	v_add3_u32 v45, v45, v47, s14
	ds_write_b16_d16_hi v238, v45 offset:944
	global_load_dword v45, v[194:195], off offset:320
	v_mul_f32_e32 v47, v118, v7
	s_waitcnt vmcnt(0)
	v_mul_f32_e32 v47, v47, v45
	v_bfe_u32 v49, v47, 16, 1
	v_add3_u32 v47, v47, v49, s14
	ds_write_b16_d16_hi v238, v47 offset:160
	v_mul_f32_e32 v47, v119, v84
	v_mul_f32_e32 v47, v47, v45
	v_bfe_u32 v49, v47, 16, 1
	v_add3_u32 v47, v47, v49, s14
	ds_write_b16_d16_hi v238, v47 offset:432
	v_mul_f32_e32 v47, v90, v85
	v_mul_f32_e32 v47, v47, v45
	v_bfe_u32 v49, v47, 16, 1
	v_add3_u32 v47, v47, v49, s14
	ds_write_b16_d16_hi v238, v47 offset:704
	v_mul_f32_e32 v47, v91, v88
	v_mul_f32_e32 v45, v47, v45
	v_bfe_u32 v47, v45, 16, 1
	v_add3_u32 v45, v45, v47, s14
	ds_write_b16_d16_hi v238, v45 offset:976
	global_load_dword v45, v[194:195], off offset:384
	v_mul_f32_e32 v47, v114, v7
	s_waitcnt vmcnt(0)
	v_mul_f32_e32 v47, v47, v45
	v_bfe_u32 v49, v47, 16, 1
	v_add3_u32 v47, v47, v49, s14
	ds_write_b16_d16_hi v238, v47 offset:192
	v_mul_f32_e32 v47, v115, v84
	v_mul_f32_e32 v47, v47, v45
	v_bfe_u32 v49, v47, 16, 1
	v_add3_u32 v47, v47, v49, s14
	ds_write_b16_d16_hi v238, v47 offset:464
	v_mul_f32_e32 v47, v82, v85
	v_mul_f32_e32 v47, v47, v45
	v_bfe_u32 v49, v47, 16, 1
	v_add3_u32 v47, v47, v49, s14
	ds_write_b16_d16_hi v238, v47 offset:736
	v_mul_f32_e32 v47, v83, v88
	v_mul_f32_e32 v45, v47, v45
	v_bfe_u32 v47, v45, 16, 1
	v_add3_u32 v45, v45, v47, s14
	ds_write_b16_d16_hi v238, v45 offset:1008
	global_load_dword v45, v[194:195], off offset:448
	s_waitcnt vmcnt(0)
	v_mul_f32_e32 v40, v40, v45
	v_bfe_u32 v47, v40, 16, 1
	v_add3_u32 v40, v40, v47, s14
	ds_write_b16_d16_hi v238, v40 offset:224
	v_mul_f32_e32 v40, v41, v84
	v_mul_f32_e32 v40, v40, v45
	v_bfe_u32 v41, v40, 16, 1
	v_add3_u32 v40, v40, v41, s14
	ds_write_b16_d16_hi v238, v40 offset:496
	v_mul_f32_e32 v40, v42, v85
	v_mul_f32_e32 v40, v40, v45
	v_bfe_u32 v41, v40, 16, 1
	v_add3_u32 v40, v40, v41, s14
	ds_write_b16_d16_hi v238, v40 offset:768
	v_mul_f32_e32 v40, v43, v88
	v_mul_f32_e32 v40, v40, v45
	v_bfe_u32 v41, v40, 16, 1
	v_add3_u32 v40, v40, v41, s14
	ds_write_b16_d16_hi v238, v40 offset:1040
	v_ashrrev_i32_e32 v51, 31, v50
	s_and_saveexec_b64 s[80:81], s[76:77]
	s_cbranch_execz .LBB0_746
	v_lshlrev_b32_e32 v45, 16, v36
	v_mul_f32_e32 v45, 0xbfb8aa3b, v45
	v_exp_f32_e32 v82, v45
	v_lshlrev_b32_e32 v45, 16, v37
	ds_read_b128 v[40:43], v239
	v_mul_f32_e32 v45, 0xbfb8aa3b, v45
	v_exp_f32_e32 v83, v45
	v_and_b32_e32 v36, 0xffff0000, v36
	v_and_b32_e32 v37, 0xffff0000, v37
	s_waitcnt lgkmcnt(0)
	v_lshlrev_b32_e32 v47, 16, v41
	v_pk_add_f32 v[82:83], v[82:83], 1.0 op_sel_hi:[1,0]
	v_lshlrev_b32_e32 v45, 16, v40
	v_div_scale_f32 v49, vcc, v83, v83, v47
	v_rcp_f32_e32 v89, v49
	v_mul_f32_e32 v36, 0xbfb8aa3b, v36
	v_mul_f32_e32 v37, 0xbfb8aa3b, v37
	v_exp_f32_e32 v36, v36
	v_fma_f32 v90, -v49, v89, 1.0
	v_fmac_f32_e32 v89, v90, v89
	v_div_scale_f32 v90, vcc, v47, v83, v47
	v_mul_f32_e32 v91, v90, v89
	v_fma_f32 v92, -v49, v91, v90
	v_fmac_f32_e32 v91, v92, v89
	v_fma_f32 v49, -v49, v91, v90
	v_div_fmas_f32 v49, v49, v89, v91
	v_div_fixup_f32 v47, v49, v83, v47
	v_div_scale_f32 v49, vcc, v82, v82, v45
	v_rcp_f32_e32 v83, v49
	v_exp_f32_e32 v37, v37
	v_and_b32_e32 v40, 0xffff0000, v40
	v_and_b32_e32 v41, 0xffff0000, v41
	v_fma_f32 v89, -v49, v83, 1.0
	v_fmac_f32_e32 v83, v89, v83
	v_div_scale_f32 v89, vcc, v45, v82, v45
	v_mul_f32_e32 v90, v89, v83
	v_fma_f32 v91, -v49, v90, v89
	v_fmac_f32_e32 v90, v91, v83
	v_fma_f32 v49, -v49, v90, v89
	v_div_fmas_f32 v49, v49, v83, v90
	v_pk_add_f32 v[36:37], v[36:37], 1.0 op_sel_hi:[1,0]
	v_div_fixup_f32 v45, v49, v82, v45
	v_div_scale_f32 v49, vcc, v36, v36, v40
	v_rcp_f32_e32 v82, v49
	s_nop 0
	v_fma_f32 v83, -v49, v82, 1.0
	v_fmac_f32_e32 v82, v83, v82
	v_div_scale_f32 v83, vcc, v40, v36, v40
	v_mul_f32_e32 v89, v83, v82
	v_fma_f32 v90, -v49, v89, v83
	v_fmac_f32_e32 v89, v90, v82
	v_fma_f32 v49, -v49, v89, v83
	v_div_fmas_f32 v49, v49, v82, v89
	v_div_fixup_f32 v40, v49, v36, v40
	v_div_scale_f32 v36, vcc, v37, v37, v41
	v_rcp_f32_e32 v49, v36
	s_nop 0
	v_fma_f32 v82, -v36, v49, 1.0
	v_fmac_f32_e32 v49, v82, v49
	v_div_scale_f32 v82, vcc, v41, v37, v41
	v_mul_f32_e32 v83, v82, v49
	v_fma_f32 v89, -v36, v83, v82
	v_fmac_f32_e32 v83, v89, v49
	v_fma_f32 v36, -v36, v83, v82
	v_div_fmas_f32 v36, v36, v49, v83
	v_div_fixup_f32 v41, v36, v37, v41
	v_and_b32_e32 v37, 0xffff0000, v38
	v_mul_f32_e32 v37, 0xbfb8aa3b, v37
	v_lshlrev_b32_e32 v36, 16, v38
	v_exp_f32_e32 v38, v37
	v_lshlrev_b32_e32 v37, 16, v39
	v_mul_f32_e32 v36, 0xbfb8aa3b, v36
	v_mul_f32_e32 v37, 0xbfb8aa3b, v37
	v_exp_f32_e32 v36, v36
	v_exp_f32_e32 v37, v37
	v_lshlrev_b32_e32 v82, 16, v43
	v_lshlrev_b32_e32 v49, 16, v42
	v_and_b32_e32 v39, 0xffff0000, v39
	v_pk_add_f32 v[36:37], v[36:37], 1.0 op_sel_hi:[1,0]
	v_mul_f32_e32 v39, 0xbfb8aa3b, v39
	v_div_scale_f32 v83, vcc, v37, v37, v82
	v_rcp_f32_e32 v89, v83
	v_exp_f32_e32 v39, v39
	v_and_b32_e32 v42, 0xffff0000, v42
	v_and_b32_e32 v43, 0xffff0000, v43
	v_fma_f32 v90, -v83, v89, 1.0
	v_fmac_f32_e32 v89, v90, v89
	v_div_scale_f32 v90, vcc, v82, v37, v82
	v_mul_f32_e32 v91, v90, v89
	v_fma_f32 v92, -v83, v91, v90
	v_fmac_f32_e32 v91, v92, v89
	v_fma_f32 v83, -v83, v91, v90
	v_div_fmas_f32 v83, v83, v89, v91
	v_div_fixup_f32 v82, v83, v37, v82
	v_div_scale_f32 v37, vcc, v36, v36, v49
	v_rcp_f32_e32 v83, v37
	s_nop 0
	v_fma_f32 v89, -v37, v83, 1.0
	v_fmac_f32_e32 v83, v89, v83
	v_div_scale_f32 v89, vcc, v49, v36, v49
	v_mul_f32_e32 v90, v89, v83
	v_fma_f32 v91, -v37, v90, v89
	v_fmac_f32_e32 v90, v91, v83
	v_fma_f32 v37, -v37, v90, v89
	v_div_fmas_f32 v37, v37, v83, v90
	v_div_fixup_f32 v49, v37, v36, v49
	v_pk_add_f32 v[36:37], v[38:39], 1.0 op_sel_hi:[1,0]
	s_nop 0
	v_div_scale_f32 v38, vcc, v36, v36, v42
	v_rcp_f32_e32 v39, v38
	s_nop 0
	v_fma_f32 v83, -v38, v39, 1.0
	v_fmac_f32_e32 v39, v83, v39
	v_div_scale_f32 v83, vcc, v42, v36, v42
	v_mul_f32_e32 v89, v83, v39
	v_fma_f32 v90, -v38, v89, v83
	v_fmac_f32_e32 v89, v90, v39
	v_fma_f32 v38, -v38, v89, v83
	v_div_fmas_f32 v38, v38, v39, v89
	v_div_fixup_f32 v36, v38, v36, v42
	v_div_scale_f32 v38, vcc, v37, v37, v43
	v_rcp_f32_e32 v39, v38
	s_nop 0
	v_fma_f32 v42, -v38, v39, 1.0
	v_fmac_f32_e32 v39, v42, v39
	v_div_scale_f32 v42, vcc, v43, v37, v43
	v_mul_f32_e32 v83, v42, v39
	v_fma_f32 v89, -v38, v83, v42
	v_fmac_f32_e32 v83, v89, v39
	v_fma_f32 v38, -v38, v83, v42
	v_div_fmas_f32 v38, v38, v39, v83
	v_div_fixup_f32 v37, v38, v37, v43
	v_bfe_u32 v38, v37, 16, 1
	v_bfe_u32 v39, v36, 16, 1
	v_bfe_u32 v42, v41, 16, 1
	v_bfe_u32 v43, v40, 16, 1
	v_add3_u32 v40, v40, v43, s14
	v_add3_u32 v41, v41, v42, s14
	v_add3_u32 v36, v36, v39, s14
	v_add3_u32 v37, v37, v38, s14
	v_bfe_u32 v38, v45, 16, 1
	v_bfe_u32 v39, v47, 16, 1
	v_bfe_u32 v42, v49, 16, 1
	v_bfe_u32 v43, v82, 16, 1
	v_add3_u32 v43, v82, v43, s14
	v_add3_u32 v42, v49, v42, s14
	v_add3_u32 v39, v47, v39, s14
	v_add3_u32 v38, v45, v38, s14
	v_lshrrev_b32_e32 v45, 16, v38
	v_lshrrev_b32_e32 v47, 16, v39
	v_lshrrev_b32_e32 v38, 16, v42
	v_lshrrev_b32_e32 v39, 16, v43
	v_and_or_b32 v39, v37, s17, v39
	v_and_or_b32 v38, v36, s17, v38
	v_and_or_b32 v37, v41, s17, v47
	v_and_or_b32 v36, v40, s17, v45
	v_lshlrev_b64 v[40:41], 11, v[50:51]
	v_lshl_add_u64 v[40:41], v[176:177], 0, v[40:41]
	global_store_dwordx4 v[40:41], v[36:39], off
	s_or_b64 exec, exec, s[80:81]
	v_ashrrev_i32_e32 v49, 31, v48
	s_and_saveexec_b64 s[80:81], s[74:75]
	s_cbranch_execnz .LBB0_747

.LBB0_745:
	v_lshlrev_b32_e32 v36, 16, v28
	v_lshlrev_b32_e32 v37, 16, v29
	ds_read_b128 v[32:35], v239 offset:2176
	v_mul_f32_e32 v36, 0xbfb8aa3b, v36
	v_mul_f32_e32 v37, 0xbfb8aa3b, v37
	v_exp_f32_e32 v36, v36
	v_exp_f32_e32 v37, v37
	s_waitcnt lgkmcnt(0)
	v_lshlrev_b32_e32 v39, 16, v33
	v_lshlrev_b32_e32 v38, 16, v32
	v_and_b32_e32 v28, 0xffff0000, v28
	v_pk_add_f32 v[36:37], v[36:37], 1.0 op_sel_hi:[1,0]
	v_and_b32_e32 v29, 0xffff0000, v29
	v_div_scale_f32 v40, vcc, v37, v37, v39
	v_rcp_f32_e32 v41, v40
	v_mul_f32_e32 v28, 0xbfb8aa3b, v28
	v_mul_f32_e32 v29, 0xbfb8aa3b, v29
	v_exp_f32_e32 v28, v28
	v_fma_f32 v42, -v40, v41, 1.0
	v_fmac_f32_e32 v41, v42, v41
	v_div_scale_f32 v42, vcc, v39, v37, v39
	v_mul_f32_e32 v43, v42, v41
	v_fma_f32 v45, -v40, v43, v42
	v_fmac_f32_e32 v43, v45, v41
	v_fma_f32 v40, -v40, v43, v42
	v_div_fmas_f32 v40, v40, v41, v43
	v_div_fixup_f32 v37, v40, v37, v39
	v_div_scale_f32 v39, vcc, v36, v36, v38
	v_rcp_f32_e32 v40, v39
	v_exp_f32_e32 v29, v29
	v_and_b32_e32 v32, 0xffff0000, v32
	v_and_b32_e32 v33, 0xffff0000, v33
	v_fma_f32 v41, -v39, v40, 1.0
	v_fmac_f32_e32 v40, v41, v40
	v_div_scale_f32 v41, vcc, v38, v36, v38
	v_mul_f32_e32 v42, v41, v40
	v_fma_f32 v43, -v39, v42, v41
	v_fmac_f32_e32 v42, v43, v40
	v_fma_f32 v39, -v39, v42, v41
	v_div_fmas_f32 v39, v39, v40, v42
	v_pk_add_f32 v[28:29], v[28:29], 1.0 op_sel_hi:[1,0]
	v_div_fixup_f32 v36, v39, v36, v38
	v_div_scale_f32 v38, vcc, v28, v28, v32
	v_rcp_f32_e32 v39, v38
	s_nop 0
	v_fma_f32 v40, -v38, v39, 1.0
	v_fmac_f32_e32 v39, v40, v39
	v_div_scale_f32 v40, vcc, v32, v28, v32
	v_mul_f32_e32 v41, v40, v39
	v_fma_f32 v42, -v38, v41, v40
	v_fmac_f32_e32 v41, v42, v39
	v_fma_f32 v38, -v38, v41, v40
	v_div_fmas_f32 v38, v38, v39, v41
	v_div_fixup_f32 v32, v38, v28, v32
	v_div_scale_f32 v28, vcc, v29, v29, v33
	v_rcp_f32_e32 v38, v28
	s_nop 0
	v_fma_f32 v39, -v28, v38, 1.0
	v_fmac_f32_e32 v38, v39, v38
	v_div_scale_f32 v39, vcc, v33, v29, v33
	v_mul_f32_e32 v40, v39, v38
	v_fma_f32 v41, -v28, v40, v39
	v_fmac_f32_e32 v40, v41, v38
	v_fma_f32 v28, -v28, v40, v39
	v_div_fmas_f32 v28, v28, v38, v40
	v_div_fixup_f32 v33, v28, v29, v33
	v_and_b32_e32 v29, 0xffff0000, v30
	v_mul_f32_e32 v29, 0xbfb8aa3b, v29
	v_lshlrev_b32_e32 v28, 16, v30
	v_exp_f32_e32 v30, v29
	v_lshlrev_b32_e32 v29, 16, v31
	v_mul_f32_e32 v28, 0xbfb8aa3b, v28
	v_mul_f32_e32 v29, 0xbfb8aa3b, v29
	v_exp_f32_e32 v28, v28
	v_exp_f32_e32 v29, v29
	v_lshlrev_b32_e32 v39, 16, v35
	v_lshlrev_b32_e32 v38, 16, v34
	v_and_b32_e32 v31, 0xffff0000, v31
	v_pk_add_f32 v[28:29], v[28:29], 1.0 op_sel_hi:[1,0]
	v_mul_f32_e32 v31, 0xbfb8aa3b, v31
	v_div_scale_f32 v40, vcc, v29, v29, v39
	v_rcp_f32_e32 v41, v40
	v_exp_f32_e32 v31, v31
	v_and_b32_e32 v34, 0xffff0000, v34
	v_and_b32_e32 v35, 0xffff0000, v35
	v_fma_f32 v42, -v40, v41, 1.0
	v_fmac_f32_e32 v41, v42, v41
	v_div_scale_f32 v42, vcc, v39, v29, v39
	v_mul_f32_e32 v43, v42, v41
	v_fma_f32 v45, -v40, v43, v42
	v_fmac_f32_e32 v43, v45, v41
	v_fma_f32 v40, -v40, v43, v42
	v_div_fmas_f32 v40, v40, v41, v43
	v_div_fixup_f32 v39, v40, v29, v39
	v_div_scale_f32 v29, vcc, v28, v28, v38
	v_rcp_f32_e32 v40, v29
	s_nop 0
	v_fma_f32 v41, -v29, v40, 1.0
	v_fmac_f32_e32 v40, v41, v40
	v_div_scale_f32 v41, vcc, v38, v28, v38
	v_mul_f32_e32 v42, v41, v40
	v_fma_f32 v43, -v29, v42, v41
	v_fmac_f32_e32 v42, v43, v40
	v_fma_f32 v29, -v29, v42, v41
	v_div_fmas_f32 v29, v29, v40, v42
	v_div_fixup_f32 v38, v29, v28, v38
	v_pk_add_f32 v[28:29], v[30:31], 1.0 op_sel_hi:[1,0]
	s_nop 0
	v_div_scale_f32 v30, vcc, v28, v28, v34
	v_rcp_f32_e32 v31, v30
	s_nop 0
	v_fma_f32 v40, -v30, v31, 1.0
	v_fmac_f32_e32 v31, v40, v31
	v_div_scale_f32 v40, vcc, v34, v28, v34
	v_mul_f32_e32 v41, v40, v31
	v_fma_f32 v42, -v30, v41, v40
	v_fmac_f32_e32 v41, v42, v31
	v_fma_f32 v30, -v30, v41, v40
	v_div_fmas_f32 v30, v30, v31, v41
	v_div_fixup_f32 v28, v30, v28, v34
	v_div_scale_f32 v30, vcc, v29, v29, v35
	v_rcp_f32_e32 v31, v30
	s_nop 0
	v_fma_f32 v34, -v30, v31, 1.0
	v_fmac_f32_e32 v31, v34, v31
	v_div_scale_f32 v34, vcc, v35, v29, v35
	v_mul_f32_e32 v40, v34, v31
	v_fma_f32 v41, -v30, v40, v34
	v_fmac_f32_e32 v40, v41, v31
	v_fma_f32 v30, -v30, v40, v34
	v_div_fmas_f32 v30, v30, v31, v40
	v_div_fixup_f32 v29, v30, v29, v35
	v_bfe_u32 v30, v29, 16, 1
	v_bfe_u32 v31, v28, 16, 1
	v_bfe_u32 v34, v33, 16, 1
	v_bfe_u32 v35, v32, 16, 1
	v_add3_u32 v32, v32, v35, s14
	v_add3_u32 v33, v33, v34, s14
	v_add3_u32 v28, v28, v31, s14
	v_add3_u32 v29, v29, v30, s14
	v_bfe_u32 v30, v36, 16, 1
	v_bfe_u32 v31, v37, 16, 1
	v_bfe_u32 v34, v38, 16, 1
	v_bfe_u32 v35, v39, 16, 1
	v_add3_u32 v35, v39, v35, s14
	v_add3_u32 v34, v38, v34, s14
	v_add3_u32 v31, v37, v31, s14
	v_add3_u32 v30, v36, v30, s14
	v_lshrrev_b32_e32 v36, 16, v30
	v_lshrrev_b32_e32 v37, 16, v31
	v_lshrrev_b32_e32 v30, 16, v34
	v_lshrrev_b32_e32 v31, 16, v35
	v_and_or_b32 v31, v29, s17, v31
	v_and_or_b32 v30, v28, s17, v30
	v_and_or_b32 v29, v33, s17, v37
	v_and_or_b32 v28, v32, s17, v36
	v_lshlrev_b64 v[32:33], 11, v[46:47]
	v_lshl_add_u64 v[32:33], v[176:177], 0, v[32:33]
	global_store_dwordx4 v[32:33], v[28:31], off
	s_or_b64 exec, exec, s[80:81]
	v_ashrrev_i32_e32 v45, 31, v44
	s_and_saveexec_b64 s[80:81], s[70:71]
	s_cbranch_execnz .LBB0_749
	s_branch .LBB0_750

.LBB0_747:
	v_lshlrev_b32_e32 v40, 16, v32
	v_lshlrev_b32_e32 v41, 16, v33
	ds_read_b128 v[36:39], v239 offset:1088
	v_mul_f32_e32 v40, 0xbfb8aa3b, v40
	v_mul_f32_e32 v41, 0xbfb8aa3b, v41
	v_exp_f32_e32 v40, v40
	v_exp_f32_e32 v41, v41
	s_waitcnt lgkmcnt(0)
	v_lshlrev_b32_e32 v43, 16, v37
	v_lshlrev_b32_e32 v42, 16, v36
	v_and_b32_e32 v32, 0xffff0000, v32
	v_pk_add_f32 v[40:41], v[40:41], 1.0 op_sel_hi:[1,0]
	v_and_b32_e32 v33, 0xffff0000, v33
	v_div_scale_f32 v45, vcc, v41, v41, v43
	v_rcp_f32_e32 v47, v45
	v_mul_f32_e32 v32, 0xbfb8aa3b, v32
	v_mul_f32_e32 v33, 0xbfb8aa3b, v33
	v_exp_f32_e32 v32, v32
	v_fma_f32 v82, -v45, v47, 1.0
	v_fmac_f32_e32 v47, v82, v47
	v_div_scale_f32 v82, vcc, v43, v41, v43
	v_mul_f32_e32 v83, v82, v47
	v_fma_f32 v89, -v45, v83, v82
	v_fmac_f32_e32 v83, v89, v47
	v_fma_f32 v45, -v45, v83, v82
	v_div_fmas_f32 v45, v45, v47, v83
	v_div_fixup_f32 v41, v45, v41, v43
	v_div_scale_f32 v43, vcc, v40, v40, v42
	v_rcp_f32_e32 v45, v43
	v_exp_f32_e32 v33, v33
	v_and_b32_e32 v36, 0xffff0000, v36
	v_and_b32_e32 v37, 0xffff0000, v37
	v_fma_f32 v47, -v43, v45, 1.0
	v_fmac_f32_e32 v45, v47, v45
	v_div_scale_f32 v47, vcc, v42, v40, v42
	v_mul_f32_e32 v82, v47, v45
	v_fma_f32 v83, -v43, v82, v47
	v_fmac_f32_e32 v82, v83, v45
	v_fma_f32 v43, -v43, v82, v47
	v_div_fmas_f32 v43, v43, v45, v82
	v_pk_add_f32 v[32:33], v[32:33], 1.0 op_sel_hi:[1,0]
	v_div_fixup_f32 v40, v43, v40, v42
	v_div_scale_f32 v42, vcc, v32, v32, v36
	v_rcp_f32_e32 v43, v42
	s_nop 0
	v_fma_f32 v45, -v42, v43, 1.0
	v_fmac_f32_e32 v43, v45, v43
	v_div_scale_f32 v45, vcc, v36, v32, v36
	v_mul_f32_e32 v47, v45, v43
	v_fma_f32 v82, -v42, v47, v45
	v_fmac_f32_e32 v47, v82, v43
	v_fma_f32 v42, -v42, v47, v45
	v_div_fmas_f32 v42, v42, v43, v47
	v_div_fixup_f32 v36, v42, v32, v36
	v_div_scale_f32 v32, vcc, v33, v33, v37
	v_rcp_f32_e32 v42, v32
	s_nop 0
	v_fma_f32 v43, -v32, v42, 1.0
	v_fmac_f32_e32 v42, v43, v42
	v_div_scale_f32 v43, vcc, v37, v33, v37
	v_mul_f32_e32 v45, v43, v42
	v_fma_f32 v47, -v32, v45, v43
	v_fmac_f32_e32 v45, v47, v42
	v_fma_f32 v32, -v32, v45, v43
	v_div_fmas_f32 v32, v32, v42, v45
	v_div_fixup_f32 v37, v32, v33, v37
	v_and_b32_e32 v33, 0xffff0000, v34
	v_mul_f32_e32 v33, 0xbfb8aa3b, v33
	v_lshlrev_b32_e32 v32, 16, v34
	v_exp_f32_e32 v34, v33
	v_lshlrev_b32_e32 v33, 16, v35
	v_mul_f32_e32 v32, 0xbfb8aa3b, v32
	v_mul_f32_e32 v33, 0xbfb8aa3b, v33
	v_exp_f32_e32 v32, v32
	v_exp_f32_e32 v33, v33
	v_lshlrev_b32_e32 v43, 16, v39
	v_lshlrev_b32_e32 v42, 16, v38
	v_and_b32_e32 v35, 0xffff0000, v35
	v_pk_add_f32 v[32:33], v[32:33], 1.0 op_sel_hi:[1,0]
	v_mul_f32_e32 v35, 0xbfb8aa3b, v35
	v_div_scale_f32 v45, vcc, v33, v33, v43
	v_rcp_f32_e32 v47, v45
	v_exp_f32_e32 v35, v35
	v_and_b32_e32 v38, 0xffff0000, v38
	v_and_b32_e32 v39, 0xffff0000, v39
	v_fma_f32 v82, -v45, v47, 1.0
	v_fmac_f32_e32 v47, v82, v47
	v_div_scale_f32 v82, vcc, v43, v33, v43
	v_mul_f32_e32 v83, v82, v47
	v_fma_f32 v89, -v45, v83, v82
	v_fmac_f32_e32 v83, v89, v47
	v_fma_f32 v45, -v45, v83, v82
	v_div_fmas_f32 v45, v45, v47, v83
	v_div_fixup_f32 v43, v45, v33, v43
	v_div_scale_f32 v33, vcc, v32, v32, v42
	v_rcp_f32_e32 v45, v33
	s_nop 0
	v_fma_f32 v47, -v33, v45, 1.0
	v_fmac_f32_e32 v45, v47, v45
	v_div_scale_f32 v47, vcc, v42, v32, v42
	v_mul_f32_e32 v82, v47, v45
	v_fma_f32 v83, -v33, v82, v47
	v_fmac_f32_e32 v82, v83, v45
	v_fma_f32 v33, -v33, v82, v47
	v_div_fmas_f32 v33, v33, v45, v82
	v_div_fixup_f32 v42, v33, v32, v42
	v_pk_add_f32 v[32:33], v[34:35], 1.0 op_sel_hi:[1,0]
	s_nop 0
	v_div_scale_f32 v34, vcc, v32, v32, v38
	v_rcp_f32_e32 v35, v34
	s_nop 0
	v_fma_f32 v45, -v34, v35, 1.0
	v_fmac_f32_e32 v35, v45, v35
	v_div_scale_f32 v45, vcc, v38, v32, v38
	v_mul_f32_e32 v47, v45, v35
	v_fma_f32 v82, -v34, v47, v45
	v_fmac_f32_e32 v47, v82, v35
	v_fma_f32 v34, -v34, v47, v45
	v_div_fmas_f32 v34, v34, v35, v47
	v_div_fixup_f32 v32, v34, v32, v38
	v_div_scale_f32 v34, vcc, v33, v33, v39
	v_rcp_f32_e32 v35, v34
	s_nop 0
	v_fma_f32 v38, -v34, v35, 1.0
	v_fmac_f32_e32 v35, v38, v35
	v_div_scale_f32 v38, vcc, v39, v33, v39
	v_mul_f32_e32 v45, v38, v35
	v_fma_f32 v47, -v34, v45, v38
	v_fmac_f32_e32 v45, v47, v35
	v_fma_f32 v34, -v34, v45, v38
	v_div_fmas_f32 v34, v34, v35, v45
	v_div_fixup_f32 v33, v34, v33, v39
	v_bfe_u32 v34, v33, 16, 1
	v_bfe_u32 v35, v32, 16, 1
	v_bfe_u32 v38, v37, 16, 1
	v_bfe_u32 v39, v36, 16, 1
	v_add3_u32 v36, v36, v39, s14
	v_add3_u32 v37, v37, v38, s14
	v_add3_u32 v32, v32, v35, s14
	v_add3_u32 v33, v33, v34, s14
	v_bfe_u32 v34, v40, 16, 1
	v_bfe_u32 v35, v41, 16, 1
	v_bfe_u32 v38, v42, 16, 1
	v_bfe_u32 v39, v43, 16, 1
	v_add3_u32 v39, v43, v39, s14
	v_add3_u32 v38, v42, v38, s14
	v_add3_u32 v35, v41, v35, s14
	v_add3_u32 v34, v40, v34, s14
	v_lshrrev_b32_e32 v40, 16, v34
	v_lshrrev_b32_e32 v41, 16, v35
	v_lshrrev_b32_e32 v34, 16, v38
	v_lshrrev_b32_e32 v35, 16, v39
	v_and_or_b32 v35, v33, s17, v35
	v_and_or_b32 v34, v32, s17, v34
	v_and_or_b32 v33, v37, s17, v41
	v_and_or_b32 v32, v36, s17, v40
	v_lshlrev_b64 v[36:37], 11, v[48:49]
	v_lshl_add_u64 v[36:37], v[176:177], 0, v[36:37]
	global_store_dwordx4 v[36:37], v[32:35], off
	s_or_b64 exec, exec, s[80:81]
	v_ashrrev_i32_e32 v47, 31, v46
	s_and_saveexec_b64 s[80:81], s[72:73]
	s_cbranch_execnz .LBB0_745

.LBB0_749:
	v_lshlrev_b32_e32 v32, 16, v24
	v_lshlrev_b32_e32 v33, 16, v25
	ds_read_b128 v[28:31], v239 offset:3264
	v_mul_f32_e32 v32, 0xbfb8aa3b, v32
	v_mul_f32_e32 v33, 0xbfb8aa3b, v33
	v_exp_f32_e32 v32, v32
	v_exp_f32_e32 v33, v33
	s_waitcnt lgkmcnt(0)
	v_lshlrev_b32_e32 v35, 16, v29
	v_lshlrev_b32_e32 v34, 16, v28
	v_and_b32_e32 v24, 0xffff0000, v24
	v_pk_add_f32 v[32:33], v[32:33], 1.0 op_sel_hi:[1,0]
	v_and_b32_e32 v25, 0xffff0000, v25
	v_div_scale_f32 v36, vcc, v33, v33, v35
	v_rcp_f32_e32 v37, v36
	v_mul_f32_e32 v24, 0xbfb8aa3b, v24
	v_mul_f32_e32 v25, 0xbfb8aa3b, v25
	v_exp_f32_e32 v24, v24
	v_fma_f32 v38, -v36, v37, 1.0
	v_fmac_f32_e32 v37, v38, v37
	v_div_scale_f32 v38, vcc, v35, v33, v35
	v_mul_f32_e32 v39, v38, v37
	v_fma_f32 v40, -v36, v39, v38
	v_fmac_f32_e32 v39, v40, v37
	v_fma_f32 v36, -v36, v39, v38
	v_div_fmas_f32 v36, v36, v37, v39
	v_div_fixup_f32 v33, v36, v33, v35
	v_div_scale_f32 v35, vcc, v32, v32, v34
	v_rcp_f32_e32 v36, v35
	v_exp_f32_e32 v25, v25
	v_and_b32_e32 v28, 0xffff0000, v28
	v_and_b32_e32 v29, 0xffff0000, v29
	v_fma_f32 v37, -v35, v36, 1.0
	v_fmac_f32_e32 v36, v37, v36
	v_div_scale_f32 v37, vcc, v34, v32, v34
	v_mul_f32_e32 v38, v37, v36
	v_fma_f32 v39, -v35, v38, v37
	v_fmac_f32_e32 v38, v39, v36
	v_fma_f32 v35, -v35, v38, v37
	v_div_fmas_f32 v35, v35, v36, v38
	v_pk_add_f32 v[24:25], v[24:25], 1.0 op_sel_hi:[1,0]
	v_div_fixup_f32 v32, v35, v32, v34
	v_div_scale_f32 v34, vcc, v24, v24, v28
	v_rcp_f32_e32 v35, v34
	s_nop 0
	v_fma_f32 v36, -v34, v35, 1.0
	v_fmac_f32_e32 v35, v36, v35
	v_div_scale_f32 v36, vcc, v28, v24, v28
	v_mul_f32_e32 v37, v36, v35
	v_fma_f32 v38, -v34, v37, v36
	v_fmac_f32_e32 v37, v38, v35
	v_fma_f32 v34, -v34, v37, v36
	v_div_fmas_f32 v34, v34, v35, v37
	v_div_fixup_f32 v28, v34, v24, v28
	v_div_scale_f32 v24, vcc, v25, v25, v29
	v_rcp_f32_e32 v34, v24
	s_nop 0
	v_fma_f32 v35, -v24, v34, 1.0
	v_fmac_f32_e32 v34, v35, v34
	v_div_scale_f32 v35, vcc, v29, v25, v29
	v_mul_f32_e32 v36, v35, v34
	v_fma_f32 v37, -v24, v36, v35
	v_fmac_f32_e32 v36, v37, v34
	v_fma_f32 v24, -v24, v36, v35
	v_div_fmas_f32 v24, v24, v34, v36
	v_div_fixup_f32 v29, v24, v25, v29
	v_and_b32_e32 v25, 0xffff0000, v26
	v_mul_f32_e32 v25, 0xbfb8aa3b, v25
	v_lshlrev_b32_e32 v24, 16, v26
	v_exp_f32_e32 v26, v25
	v_lshlrev_b32_e32 v25, 16, v27
	v_mul_f32_e32 v24, 0xbfb8aa3b, v24
	v_mul_f32_e32 v25, 0xbfb8aa3b, v25
	v_exp_f32_e32 v24, v24
	v_exp_f32_e32 v25, v25
	v_lshlrev_b32_e32 v35, 16, v31
	v_lshlrev_b32_e32 v34, 16, v30
	v_and_b32_e32 v27, 0xffff0000, v27
	v_pk_add_f32 v[24:25], v[24:25], 1.0 op_sel_hi:[1,0]
	v_mul_f32_e32 v27, 0xbfb8aa3b, v27
	v_div_scale_f32 v36, vcc, v25, v25, v35
	v_rcp_f32_e32 v37, v36
	v_exp_f32_e32 v27, v27
	v_and_b32_e32 v30, 0xffff0000, v30
	v_and_b32_e32 v31, 0xffff0000, v31
	v_fma_f32 v38, -v36, v37, 1.0
	v_fmac_f32_e32 v37, v38, v37
	v_div_scale_f32 v38, vcc, v35, v25, v35
	v_mul_f32_e32 v39, v38, v37
	v_fma_f32 v40, -v36, v39, v38
	v_fmac_f32_e32 v39, v40, v37
	v_fma_f32 v36, -v36, v39, v38
	v_div_fmas_f32 v36, v36, v37, v39
	v_div_fixup_f32 v35, v36, v25, v35
	v_div_scale_f32 v25, vcc, v24, v24, v34
	v_rcp_f32_e32 v36, v25
	s_nop 0
	v_fma_f32 v37, -v25, v36, 1.0
	v_fmac_f32_e32 v36, v37, v36
	v_div_scale_f32 v37, vcc, v34, v24, v34
	v_mul_f32_e32 v38, v37, v36
	v_fma_f32 v39, -v25, v38, v37
	v_fmac_f32_e32 v38, v39, v36
	v_fma_f32 v25, -v25, v38, v37
	v_div_fmas_f32 v25, v25, v36, v38
	v_div_fixup_f32 v34, v25, v24, v34
	v_pk_add_f32 v[24:25], v[26:27], 1.0 op_sel_hi:[1,0]
	s_nop 0
	v_div_scale_f32 v26, vcc, v24, v24, v30
	v_rcp_f32_e32 v27, v26
	s_nop 0
	v_fma_f32 v36, -v26, v27, 1.0
	v_fmac_f32_e32 v27, v36, v27
	v_div_scale_f32 v36, vcc, v30, v24, v30
	v_mul_f32_e32 v37, v36, v27
	v_fma_f32 v38, -v26, v37, v36
	v_fmac_f32_e32 v37, v38, v27
	v_fma_f32 v26, -v26, v37, v36
	v_div_fmas_f32 v26, v26, v27, v37
	v_div_fixup_f32 v24, v26, v24, v30
	v_div_scale_f32 v26, vcc, v25, v25, v31
	v_rcp_f32_e32 v27, v26
	s_nop 0
	v_fma_f32 v30, -v26, v27, 1.0
	v_fmac_f32_e32 v27, v30, v27
	v_div_scale_f32 v30, vcc, v31, v25, v31
	v_mul_f32_e32 v36, v30, v27
	v_fma_f32 v37, -v26, v36, v30
	v_fmac_f32_e32 v36, v37, v27
	v_fma_f32 v26, -v26, v36, v30
	v_div_fmas_f32 v26, v26, v27, v36
	v_div_fixup_f32 v25, v26, v25, v31
	v_bfe_u32 v26, v25, 16, 1
	v_bfe_u32 v27, v24, 16, 1
	v_bfe_u32 v30, v29, 16, 1
	v_bfe_u32 v31, v28, 16, 1
	v_add3_u32 v28, v28, v31, s14
	v_add3_u32 v29, v29, v30, s14
	v_add3_u32 v24, v24, v27, s14
	v_add3_u32 v25, v25, v26, s14
	v_bfe_u32 v26, v32, 16, 1
	v_bfe_u32 v27, v33, 16, 1
	v_bfe_u32 v30, v34, 16, 1
	v_bfe_u32 v31, v35, 16, 1
	v_add3_u32 v31, v35, v31, s14
	v_add3_u32 v30, v34, v30, s14
	v_add3_u32 v27, v33, v27, s14
	v_add3_u32 v26, v32, v26, s14
	v_lshrrev_b32_e32 v32, 16, v26
	v_lshrrev_b32_e32 v33, 16, v27
	v_lshrrev_b32_e32 v26, 16, v30
	v_lshrrev_b32_e32 v27, 16, v31
	v_and_or_b32 v27, v25, s17, v27
	v_and_or_b32 v26, v24, s17, v26
	v_and_or_b32 v25, v29, s17, v33
	v_and_or_b32 v24, v28, s17, v32
	v_lshlrev_b64 v[28:29], 11, v[44:45]
	v_lshl_add_u64 v[28:29], v[176:177], 0, v[28:29]
	global_store_dwordx4 v[28:29], v[24:27], off
.LBB0_750:
	s_or_b64 exec, exec, s[80:81]
	global_load_dword v24, v[194:195], off offset:512
	v_mul_f32_e32 v25, v86, v7
	s_waitcnt vmcnt(0)
	v_mul_f32_e32 v25, v25, v24
	v_bfe_u32 v26, v25, 16, 1
	v_add3_u32 v25, v25, v26, s14
	ds_write_b16_d16_hi v238, v25
	v_mul_f32_e32 v25, v87, v84
	v_mul_f32_e32 v25, v25, v24
	v_bfe_u32 v26, v25, 16, 1
	v_add3_u32 v25, v25, v26, s14
	ds_write_b16_d16_hi v238, v25 offset:272
	v_mul_f32_e32 v25, v80, v85
	v_mul_f32_e32 v25, v25, v24
	v_bfe_u32 v26, v25, 16, 1
	v_add3_u32 v25, v25, v26, s14
	ds_write_b16_d16_hi v238, v25 offset:544
	v_mul_f32_e32 v25, v81, v88
	v_mul_f32_e32 v24, v25, v24
	v_bfe_u32 v25, v24, 16, 1
	v_add3_u32 v24, v24, v25, s14
	ds_write_b16_d16_hi v238, v24 offset:816
	global_load_dword v24, v[194:195], off offset:576
	v_mul_f32_e32 v25, v78, v7
	s_waitcnt vmcnt(0)
	v_mul_f32_e32 v25, v25, v24
	v_bfe_u32 v26, v25, 16, 1
	v_add3_u32 v25, v25, v26, s14
	ds_write_b16_d16_hi v238, v25 offset:32
	v_mul_f32_e32 v25, v79, v84
	v_mul_f32_e32 v25, v25, v24
	v_bfe_u32 v26, v25, 16, 1
	v_add3_u32 v25, v25, v26, s14
	ds_write_b16_d16_hi v238, v25 offset:304
	v_mul_f32_e32 v25, v76, v85
	v_mul_f32_e32 v25, v25, v24
	v_bfe_u32 v26, v25, 16, 1
	v_add3_u32 v25, v25, v26, s14
	ds_write_b16_d16_hi v238, v25 offset:576
	v_mul_f32_e32 v25, v77, v88
	v_mul_f32_e32 v24, v25, v24
	v_bfe_u32 v25, v24, 16, 1
	v_add3_u32 v24, v24, v25, s14
	ds_write_b16_d16_hi v238, v24 offset:848
	global_load_dword v24, v[194:195], off offset:640
	v_mul_f32_e32 v25, v75, v7
	s_waitcnt vmcnt(0)
	v_mul_f32_e32 v25, v25, v24
	v_bfe_u32 v26, v25, 16, 1
	v_add3_u32 v25, v25, v26, s14
	ds_write_b16_d16_hi v238, v25 offset:64
	v_mul_f32_e32 v25, v71, v84
	v_mul_f32_e32 v25, v25, v24
	v_bfe_u32 v26, v25, 16, 1
	v_add3_u32 v25, v25, v26, s14
	ds_write_b16_d16_hi v238, v25 offset:336
	v_mul_f32_e32 v25, v73, v85
	v_mul_f32_e32 v25, v25, v24
	v_bfe_u32 v26, v25, 16, 1
	v_add3_u32 v25, v25, v26, s14
	ds_write_b16_d16_hi v238, v25 offset:608
	v_mul_f32_e32 v25, v69, v88
	v_mul_f32_e32 v24, v25, v24
	v_bfe_u32 v25, v24, 16, 1
	v_add3_u32 v24, v24, v25, s14
	ds_write_b16_d16_hi v238, v24 offset:880
	global_load_dword v24, v[194:195], off offset:704
	v_mul_f32_e32 v25, v74, v7
	s_waitcnt vmcnt(0)
	v_mul_f32_e32 v25, v25, v24
	v_bfe_u32 v26, v25, 16, 1
	v_add3_u32 v25, v25, v26, s14
	ds_write_b16_d16_hi v238, v25 offset:96
	v_mul_f32_e32 v25, v70, v84
	v_mul_f32_e32 v25, v25, v24
	v_bfe_u32 v26, v25, 16, 1
	v_add3_u32 v25, v25, v26, s14
	ds_write_b16_d16_hi v238, v25 offset:368
	v_mul_f32_e32 v25, v72, v85
	v_mul_f32_e32 v25, v25, v24
	v_bfe_u32 v26, v25, 16, 1
	v_add3_u32 v25, v25, v26, s14
	ds_write_b16_d16_hi v238, v25 offset:640
	v_mul_f32_e32 v25, v68, v88
	v_mul_f32_e32 v24, v25, v24
	v_bfe_u32 v25, v24, 16, 1
	v_add3_u32 v24, v24, v25, s14
	ds_write_b16_d16_hi v238, v24 offset:912
	global_load_dword v24, v[194:195], off offset:768
	v_mul_f32_e32 v25, v63, v7
	s_waitcnt vmcnt(0)
	v_mul_f32_e32 v25, v25, v24
	v_bfe_u32 v26, v25, 16, 1
	v_add3_u32 v25, v25, v26, s14
	ds_write_b16_d16_hi v238, v25 offset:128
	v_mul_f32_e32 v25, v65, v84
	v_mul_f32_e32 v25, v25, v24
	v_bfe_u32 v26, v25, 16, 1
	v_add3_u32 v25, v25, v26, s14
	ds_write_b16_d16_hi v238, v25 offset:400
	v_mul_f32_e32 v25, v67, v85
	v_mul_f32_e32 v25, v25, v24
	v_bfe_u32 v26, v25, 16, 1
	v_add3_u32 v25, v25, v26, s14
	ds_write_b16_d16_hi v238, v25 offset:672
	v_mul_f32_e32 v25, v61, v88
	v_mul_f32_e32 v24, v25, v24
	v_bfe_u32 v25, v24, 16, 1
	v_add3_u32 v24, v24, v25, s14
	ds_write_b16_d16_hi v238, v24 offset:944
	global_load_dword v24, v[194:195], off offset:832
	v_mul_f32_e32 v25, v62, v7
	s_waitcnt vmcnt(0)
	v_mul_f32_e32 v25, v25, v24
	v_bfe_u32 v26, v25, 16, 1
	v_add3_u32 v25, v25, v26, s14
	ds_write_b16_d16_hi v238, v25 offset:160
	v_mul_f32_e32 v25, v64, v84
	v_mul_f32_e32 v25, v25, v24
	v_bfe_u32 v26, v25, 16, 1
	v_add3_u32 v25, v25, v26, s14
	ds_write_b16_d16_hi v238, v25 offset:432
	v_mul_f32_e32 v25, v66, v85
	v_mul_f32_e32 v25, v25, v24
	v_bfe_u32 v26, v25, 16, 1
	v_add3_u32 v25, v25, v26, s14
	ds_write_b16_d16_hi v238, v25 offset:704
	v_mul_f32_e32 v25, v60, v88
	v_mul_f32_e32 v24, v25, v24
	v_bfe_u32 v25, v24, 16, 1
	v_add3_u32 v24, v24, v25, s14
	ds_write_b16_d16_hi v238, v24 offset:976
	global_load_dword v24, v[194:195], off offset:896
	v_mul_f32_e32 v25, v57, v7
	v_mul_f32_e32 v7, v56, v7
	s_waitcnt vmcnt(0)
	v_mul_f32_e32 v25, v25, v24
	v_bfe_u32 v26, v25, 16, 1
	v_add3_u32 v25, v25, v26, s14
	ds_write_b16_d16_hi v238, v25 offset:192
	v_mul_f32_e32 v25, v59, v84
	v_mul_f32_e32 v25, v25, v24
	v_bfe_u32 v26, v25, 16, 1
	v_add3_u32 v25, v25, v26, s14
	ds_write_b16_d16_hi v238, v25 offset:464
	v_mul_f32_e32 v25, v55, v85
	v_mul_f32_e32 v25, v25, v24
	v_bfe_u32 v26, v25, 16, 1
	v_add3_u32 v25, v25, v26, s14
	ds_write_b16_d16_hi v238, v25 offset:736
	v_mul_f32_e32 v25, v53, v88
	v_mul_f32_e32 v24, v25, v24
	v_bfe_u32 v25, v24, 16, 1
	v_add3_u32 v24, v24, v25, s14
	ds_write_b16_d16_hi v238, v24 offset:1008
	global_load_dword v24, v[194:195], off offset:960
	s_waitcnt vmcnt(0)
	v_mul_f32_e32 v7, v7, v24
	v_bfe_u32 v25, v7, 16, 1
	v_add3_u32 v7, v7, v25, s14
	ds_write_b16_d16_hi v238, v7 offset:224
	v_mul_f32_e32 v7, v58, v84
	v_mul_f32_e32 v7, v7, v24
	v_bfe_u32 v25, v7, 16, 1
	v_add3_u32 v7, v7, v25, s14
	ds_write_b16_d16_hi v238, v7 offset:496
	v_mul_f32_e32 v7, v54, v85
	v_mul_f32_e32 v7, v7, v24
	v_bfe_u32 v25, v7, 16, 1
	v_add3_u32 v7, v7, v25, s14
	ds_write_b16_d16_hi v238, v7 offset:768
	v_mul_f32_e32 v7, v52, v88
	v_mul_f32_e32 v7, v7, v24
	v_bfe_u32 v24, v7, 16, 1
	v_add3_u32 v7, v7, v24, s14
	ds_write_b16_d16_hi v238, v7 offset:1040
	s_and_saveexec_b64 s[80:81], s[76:77]
	s_cbranch_execz .LBB0_754
	v_lshlrev_b32_e32 v7, 16, v20
	v_mul_f32_e32 v7, 0xbfb8aa3b, v7
	v_exp_f32_e32 v28, v7
	v_and_b32_e32 v7, 0xffff0000, v20
	v_mul_f32_e32 v7, 0xbfb8aa3b, v7
	v_exp_f32_e32 v20, v7
	v_lshlrev_b32_e32 v7, 16, v21
	ds_read_b128 v[24:27], v239
	v_mul_f32_e32 v7, 0xbfb8aa3b, v7
	v_exp_f32_e32 v29, v7
	v_and_b32_e32 v7, 0xffff0000, v21
	v_mul_f32_e32 v7, 0xbfb8aa3b, v7
	s_waitcnt lgkmcnt(0)
	v_lshlrev_b32_e32 v30, 16, v25
	v_pk_add_f32 v[28:29], v[28:29], 1.0 op_sel_hi:[1,0]
	v_exp_f32_e32 v21, v7
	v_div_scale_f32 v31, s[76:77], v29, v29, v30
	v_rcp_f32_e32 v32, v31
	v_lshlrev_b32_e32 v7, 16, v24
	v_and_b32_e32 v24, 0xffff0000, v24
	v_pk_add_f32 v[20:21], v[20:21], 1.0 op_sel_hi:[1,0]
	v_fma_f32 v33, -v31, v32, 1.0
	v_fmac_f32_e32 v32, v33, v32
	v_div_scale_f32 v33, vcc, v30, v29, v30
	v_mul_f32_e32 v34, v33, v32
	v_fma_f32 v35, -v31, v34, v33
	v_fmac_f32_e32 v34, v35, v32
	v_fma_f32 v31, -v31, v34, v33
	v_div_fmas_f32 v31, v31, v32, v34
	v_div_fixup_f32 v29, v31, v29, v30
	v_div_scale_f32 v30, s[76:77], v28, v28, v7
	v_rcp_f32_e32 v31, v30
	v_and_b32_e32 v25, 0xffff0000, v25
	v_fma_f32 v32, -v30, v31, 1.0
	v_fmac_f32_e32 v31, v32, v31
	v_div_scale_f32 v32, vcc, v7, v28, v7
	v_mul_f32_e32 v33, v32, v31
	v_fma_f32 v34, -v30, v33, v32
	v_fmac_f32_e32 v33, v34, v31
	v_fma_f32 v30, -v30, v33, v32
	v_div_fmas_f32 v30, v30, v31, v33
	v_div_fixup_f32 v7, v30, v28, v7
	v_div_scale_f32 v28, s[76:77], v20, v20, v24
	v_rcp_f32_e32 v30, v28
	s_nop 0
	v_fma_f32 v31, -v28, v30, 1.0
	v_fmac_f32_e32 v30, v31, v30
	v_div_scale_f32 v31, vcc, v24, v20, v24
	v_mul_f32_e32 v32, v31, v30
	v_fma_f32 v33, -v28, v32, v31
	v_fmac_f32_e32 v32, v33, v30
	v_fma_f32 v28, -v28, v32, v31
	v_div_fmas_f32 v28, v28, v30, v32
	v_div_fixup_f32 v24, v28, v20, v24
	v_div_scale_f32 v20, s[76:77], v21, v21, v25
	v_rcp_f32_e32 v28, v20
	s_nop 0
	v_fma_f32 v30, -v20, v28, 1.0
	v_fmac_f32_e32 v28, v30, v28
	v_div_scale_f32 v30, vcc, v25, v21, v25
	v_mul_f32_e32 v31, v30, v28
	v_fma_f32 v32, -v20, v31, v30
	v_fmac_f32_e32 v31, v32, v28
	v_fma_f32 v20, -v20, v31, v30
	v_div_fmas_f32 v20, v20, v28, v31
	v_div_fixup_f32 v25, v20, v21, v25
	v_and_b32_e32 v21, 0xffff0000, v22
	v_mul_f32_e32 v21, 0xbfb8aa3b, v21
	v_lshlrev_b32_e32 v20, 16, v22
	v_exp_f32_e32 v22, v21
	v_lshlrev_b32_e32 v21, 16, v23
	v_mul_f32_e32 v20, 0xbfb8aa3b, v20
	v_mul_f32_e32 v21, 0xbfb8aa3b, v21
	v_exp_f32_e32 v20, v20
	v_exp_f32_e32 v21, v21
	v_lshlrev_b32_e32 v30, 16, v27
	v_lshlrev_b32_e32 v28, 16, v26
	v_and_b32_e32 v23, 0xffff0000, v23
	v_pk_add_f32 v[20:21], v[20:21], 1.0 op_sel_hi:[1,0]
	v_mul_f32_e32 v23, 0xbfb8aa3b, v23
	v_div_scale_f32 v31, s[76:77], v21, v21, v30
	v_rcp_f32_e32 v32, v31
	v_exp_f32_e32 v23, v23
	v_and_b32_e32 v26, 0xffff0000, v26
	v_and_b32_e32 v27, 0xffff0000, v27
	v_fma_f32 v33, -v31, v32, 1.0
	v_fmac_f32_e32 v32, v33, v32
	v_div_scale_f32 v33, vcc, v30, v21, v30
	v_mul_f32_e32 v34, v33, v32
	v_fma_f32 v35, -v31, v34, v33
	v_fmac_f32_e32 v34, v35, v32
	v_fma_f32 v31, -v31, v34, v33
	v_div_fmas_f32 v31, v31, v32, v34
	v_div_fixup_f32 v30, v31, v21, v30
	v_div_scale_f32 v21, s[76:77], v20, v20, v28
	v_rcp_f32_e32 v31, v21
	s_nop 0
	v_fma_f32 v32, -v21, v31, 1.0
	v_fmac_f32_e32 v31, v32, v31
	v_div_scale_f32 v32, vcc, v28, v20, v28
	v_mul_f32_e32 v33, v32, v31
	v_fma_f32 v34, -v21, v33, v32
	v_fmac_f32_e32 v33, v34, v31
	v_fma_f32 v21, -v21, v33, v32
	v_div_fmas_f32 v21, v21, v31, v33
	v_div_fixup_f32 v28, v21, v20, v28
	v_pk_add_f32 v[20:21], v[22:23], 1.0 op_sel_hi:[1,0]
	s_nop 0
	v_div_scale_f32 v22, s[76:77], v20, v20, v26
	v_rcp_f32_e32 v23, v22
	s_nop 0
	v_fma_f32 v31, -v22, v23, 1.0
	v_fmac_f32_e32 v23, v31, v23
	v_div_scale_f32 v31, vcc, v26, v20, v26
	v_mul_f32_e32 v32, v31, v23
	v_fma_f32 v33, -v22, v32, v31
	v_fmac_f32_e32 v32, v33, v23
	v_fma_f32 v22, -v22, v32, v31
	v_div_fmas_f32 v22, v22, v23, v32
	v_div_fixup_f32 v20, v22, v20, v26
	v_div_scale_f32 v22, s[76:77], v21, v21, v27
	v_rcp_f32_e32 v23, v22
	s_nop 0
	v_fma_f32 v26, -v22, v23, 1.0
	v_fmac_f32_e32 v23, v26, v23
	v_div_scale_f32 v26, vcc, v27, v21, v27
	v_mul_f32_e32 v31, v26, v23
	v_fma_f32 v32, -v22, v31, v26
	v_fmac_f32_e32 v31, v32, v23
	v_fma_f32 v22, -v22, v31, v26
	v_div_fmas_f32 v22, v22, v23, v31
	v_div_fixup_f32 v21, v22, v21, v27
	v_bfe_u32 v22, v21, 16, 1
	v_bfe_u32 v23, v20, 16, 1
	v_bfe_u32 v26, v25, 16, 1
	v_bfe_u32 v27, v24, 16, 1
	v_add3_u32 v24, v24, v27, s14
	v_add3_u32 v25, v25, v26, s14
	v_add3_u32 v20, v20, v23, s14
	v_add3_u32 v21, v21, v22, s14
	v_bfe_u32 v22, v7, 16, 1
	v_bfe_u32 v23, v29, 16, 1
	v_bfe_u32 v26, v28, 16, 1
	v_bfe_u32 v27, v30, 16, 1
	v_add3_u32 v27, v30, v27, s14
	v_add3_u32 v26, v28, v26, s14
	v_add3_u32 v23, v29, v23, s14
	v_add3_u32 v7, v7, v22, s14
	v_lshrrev_b32_e32 v7, 16, v7
	v_lshrrev_b32_e32 v28, 16, v23
	v_lshrrev_b32_e32 v22, 16, v26
	v_lshrrev_b32_e32 v23, 16, v27
	v_and_or_b32 v23, v21, s17, v23
	v_and_or_b32 v22, v20, s17, v22
	v_and_or_b32 v21, v25, s17, v28
	v_and_or_b32 v20, v24, s17, v7
	v_lshlrev_b64 v[24:25], 11, v[50:51]
	v_lshl_add_u64 v[24:25], v[176:177], 0, v[24:25]
	global_store_dwordx4 v[24:25], v[20:23], off offset:256
	s_or_b64 exec, exec, s[80:81]
	s_and_saveexec_b64 s[76:77], s[74:75]
	s_cbranch_execnz .LBB0_755

.LBB0_753:
	v_lshlrev_b32_e32 v7, 16, v12
	v_mul_f32_e32 v7, 0xbfb8aa3b, v7
	v_exp_f32_e32 v20, v7
	v_and_b32_e32 v7, 0xffff0000, v12
	v_mul_f32_e32 v7, 0xbfb8aa3b, v7
	v_exp_f32_e32 v12, v7
	v_lshlrev_b32_e32 v7, 16, v13
	ds_read_b128 v[16:19], v239 offset:2176
	v_mul_f32_e32 v7, 0xbfb8aa3b, v7
	v_exp_f32_e32 v21, v7
	v_and_b32_e32 v7, 0xffff0000, v13
	v_mul_f32_e32 v7, 0xbfb8aa3b, v7
	s_waitcnt lgkmcnt(0)
	v_lshlrev_b32_e32 v22, 16, v17
	v_pk_add_f32 v[20:21], v[20:21], 1.0 op_sel_hi:[1,0]
	v_exp_f32_e32 v13, v7
	v_div_scale_f32 v23, s[72:73], v21, v21, v22
	v_rcp_f32_e32 v24, v23
	v_lshlrev_b32_e32 v7, 16, v16
	v_and_b32_e32 v16, 0xffff0000, v16
	v_pk_add_f32 v[12:13], v[12:13], 1.0 op_sel_hi:[1,0]
	v_fma_f32 v25, -v23, v24, 1.0
	v_fmac_f32_e32 v24, v25, v24
	v_div_scale_f32 v25, vcc, v22, v21, v22
	v_mul_f32_e32 v26, v25, v24
	v_fma_f32 v27, -v23, v26, v25
	v_fmac_f32_e32 v26, v27, v24
	v_fma_f32 v23, -v23, v26, v25
	v_div_fmas_f32 v23, v23, v24, v26
	v_div_fixup_f32 v21, v23, v21, v22
	v_div_scale_f32 v22, s[72:73], v20, v20, v7
	v_rcp_f32_e32 v23, v22
	v_and_b32_e32 v17, 0xffff0000, v17
	v_fma_f32 v24, -v22, v23, 1.0
	v_fmac_f32_e32 v23, v24, v23
	v_div_scale_f32 v24, vcc, v7, v20, v7
	v_mul_f32_e32 v25, v24, v23
	v_fma_f32 v26, -v22, v25, v24
	v_fmac_f32_e32 v25, v26, v23
	v_fma_f32 v22, -v22, v25, v24
	v_div_fmas_f32 v22, v22, v23, v25
	v_div_fixup_f32 v7, v22, v20, v7
	v_div_scale_f32 v20, s[72:73], v12, v12, v16
	v_rcp_f32_e32 v22, v20
	s_nop 0
	v_fma_f32 v23, -v20, v22, 1.0
	v_fmac_f32_e32 v22, v23, v22
	v_div_scale_f32 v23, vcc, v16, v12, v16
	v_mul_f32_e32 v24, v23, v22
	v_fma_f32 v25, -v20, v24, v23
	v_fmac_f32_e32 v24, v25, v22
	v_fma_f32 v20, -v20, v24, v23
	v_div_fmas_f32 v20, v20, v22, v24
	v_div_fixup_f32 v16, v20, v12, v16
	v_div_scale_f32 v12, s[72:73], v13, v13, v17
	v_rcp_f32_e32 v20, v12
	s_nop 0
	v_fma_f32 v22, -v12, v20, 1.0
	v_fmac_f32_e32 v20, v22, v20
	v_div_scale_f32 v22, vcc, v17, v13, v17
	v_mul_f32_e32 v23, v22, v20
	v_fma_f32 v24, -v12, v23, v22
	v_fmac_f32_e32 v23, v24, v20
	v_fma_f32 v12, -v12, v23, v22
	v_div_fmas_f32 v12, v12, v20, v23
	v_div_fixup_f32 v17, v12, v13, v17
	v_and_b32_e32 v13, 0xffff0000, v14
	v_mul_f32_e32 v13, 0xbfb8aa3b, v13
	v_lshlrev_b32_e32 v12, 16, v14
	v_exp_f32_e32 v14, v13
	v_lshlrev_b32_e32 v13, 16, v15
	v_mul_f32_e32 v12, 0xbfb8aa3b, v12
	v_mul_f32_e32 v13, 0xbfb8aa3b, v13
	v_exp_f32_e32 v12, v12
	v_exp_f32_e32 v13, v13
	v_lshlrev_b32_e32 v22, 16, v19
	v_lshlrev_b32_e32 v20, 16, v18
	v_and_b32_e32 v15, 0xffff0000, v15
	v_pk_add_f32 v[12:13], v[12:13], 1.0 op_sel_hi:[1,0]
	v_mul_f32_e32 v15, 0xbfb8aa3b, v15
	v_div_scale_f32 v23, s[72:73], v13, v13, v22
	v_rcp_f32_e32 v24, v23
	v_exp_f32_e32 v15, v15
	v_and_b32_e32 v18, 0xffff0000, v18
	v_and_b32_e32 v19, 0xffff0000, v19
	v_fma_f32 v25, -v23, v24, 1.0
	v_fmac_f32_e32 v24, v25, v24
	v_div_scale_f32 v25, vcc, v22, v13, v22
	v_mul_f32_e32 v26, v25, v24
	v_fma_f32 v27, -v23, v26, v25
	v_fmac_f32_e32 v26, v27, v24
	v_fma_f32 v23, -v23, v26, v25
	v_div_fmas_f32 v23, v23, v24, v26
	v_div_fixup_f32 v22, v23, v13, v22
	v_div_scale_f32 v13, s[72:73], v12, v12, v20
	v_rcp_f32_e32 v23, v13
	s_nop 0
	v_fma_f32 v24, -v13, v23, 1.0
	v_fmac_f32_e32 v23, v24, v23
	v_div_scale_f32 v24, vcc, v20, v12, v20
	v_mul_f32_e32 v25, v24, v23
	v_fma_f32 v26, -v13, v25, v24
	v_fmac_f32_e32 v25, v26, v23
	v_fma_f32 v13, -v13, v25, v24
	v_div_fmas_f32 v13, v13, v23, v25
	v_div_fixup_f32 v20, v13, v12, v20
	v_pk_add_f32 v[12:13], v[14:15], 1.0 op_sel_hi:[1,0]
	s_nop 0
	v_div_scale_f32 v14, s[72:73], v12, v12, v18
	v_rcp_f32_e32 v15, v14
	s_nop 0
	v_fma_f32 v23, -v14, v15, 1.0
	v_fmac_f32_e32 v15, v23, v15
	v_div_scale_f32 v23, vcc, v18, v12, v18
	v_mul_f32_e32 v24, v23, v15
	v_fma_f32 v25, -v14, v24, v23
	v_fmac_f32_e32 v24, v25, v15
	v_fma_f32 v14, -v14, v24, v23
	v_div_fmas_f32 v14, v14, v15, v24
	v_div_fixup_f32 v12, v14, v12, v18
	v_div_scale_f32 v14, s[72:73], v13, v13, v19
	v_rcp_f32_e32 v15, v14
	s_nop 0
	v_fma_f32 v18, -v14, v15, 1.0
	v_fmac_f32_e32 v15, v18, v15
	v_div_scale_f32 v18, vcc, v19, v13, v19
	v_mul_f32_e32 v23, v18, v15
	v_fma_f32 v24, -v14, v23, v18
	v_fmac_f32_e32 v23, v24, v15
	v_fma_f32 v14, -v14, v23, v18
	v_div_fmas_f32 v14, v14, v15, v23
	v_div_fixup_f32 v13, v14, v13, v19
	v_bfe_u32 v14, v13, 16, 1
	v_bfe_u32 v15, v12, 16, 1
	v_bfe_u32 v18, v17, 16, 1
	v_bfe_u32 v19, v16, 16, 1
	v_add3_u32 v16, v16, v19, s14
	v_add3_u32 v17, v17, v18, s14
	v_add3_u32 v12, v12, v15, s14
	v_add3_u32 v13, v13, v14, s14
	v_bfe_u32 v14, v7, 16, 1
	v_bfe_u32 v15, v21, 16, 1
	v_bfe_u32 v18, v20, 16, 1
	v_bfe_u32 v19, v22, 16, 1
	v_add3_u32 v19, v22, v19, s14
	v_add3_u32 v18, v20, v18, s14
	v_add3_u32 v15, v21, v15, s14
	v_add3_u32 v7, v7, v14, s14
	v_lshrrev_b32_e32 v7, 16, v7
	v_lshrrev_b32_e32 v20, 16, v15
	v_lshrrev_b32_e32 v14, 16, v18
	v_lshrrev_b32_e32 v15, 16, v19
	v_and_or_b32 v15, v13, s17, v15
	v_and_or_b32 v14, v12, s17, v14
	v_and_or_b32 v13, v17, s17, v20
	v_and_or_b32 v12, v16, s17, v7
	v_lshlrev_b64 v[16:17], 11, v[46:47]
	v_lshl_add_u64 v[16:17], v[176:177], 0, v[16:17]
	global_store_dwordx4 v[16:17], v[12:15], off offset:256
	s_or_b64 exec, exec, s[74:75]
	s_and_saveexec_b64 s[72:73], s[70:71]
	s_cbranch_execz .LBB0_688
	s_branch .LBB0_757

.LBB0_755:
	v_lshlrev_b32_e32 v7, 16, v16
	v_mul_f32_e32 v7, 0xbfb8aa3b, v7
	v_exp_f32_e32 v24, v7
	v_and_b32_e32 v7, 0xffff0000, v16
	v_mul_f32_e32 v7, 0xbfb8aa3b, v7
	v_exp_f32_e32 v16, v7
	v_lshlrev_b32_e32 v7, 16, v17
	ds_read_b128 v[20:23], v239 offset:1088
	v_mul_f32_e32 v7, 0xbfb8aa3b, v7
	v_exp_f32_e32 v25, v7
	v_and_b32_e32 v7, 0xffff0000, v17
	v_mul_f32_e32 v7, 0xbfb8aa3b, v7
	s_waitcnt lgkmcnt(0)
	v_lshlrev_b32_e32 v26, 16, v21
	v_pk_add_f32 v[24:25], v[24:25], 1.0 op_sel_hi:[1,0]
	v_exp_f32_e32 v17, v7
	v_div_scale_f32 v27, s[74:75], v25, v25, v26
	v_rcp_f32_e32 v28, v27
	v_lshlrev_b32_e32 v7, 16, v20
	v_and_b32_e32 v20, 0xffff0000, v20
	v_pk_add_f32 v[16:17], v[16:17], 1.0 op_sel_hi:[1,0]
	v_fma_f32 v29, -v27, v28, 1.0
	v_fmac_f32_e32 v28, v29, v28
	v_div_scale_f32 v29, vcc, v26, v25, v26
	v_mul_f32_e32 v30, v29, v28
	v_fma_f32 v31, -v27, v30, v29
	v_fmac_f32_e32 v30, v31, v28
	v_fma_f32 v27, -v27, v30, v29
	v_div_fmas_f32 v27, v27, v28, v30
	v_div_fixup_f32 v25, v27, v25, v26
	v_div_scale_f32 v26, s[74:75], v24, v24, v7
	v_rcp_f32_e32 v27, v26
	v_and_b32_e32 v21, 0xffff0000, v21
	v_fma_f32 v28, -v26, v27, 1.0
	v_fmac_f32_e32 v27, v28, v27
	v_div_scale_f32 v28, vcc, v7, v24, v7
	v_mul_f32_e32 v29, v28, v27
	v_fma_f32 v30, -v26, v29, v28
	v_fmac_f32_e32 v29, v30, v27
	v_fma_f32 v26, -v26, v29, v28
	v_div_fmas_f32 v26, v26, v27, v29
	v_div_fixup_f32 v7, v26, v24, v7
	v_div_scale_f32 v24, s[74:75], v16, v16, v20
	v_rcp_f32_e32 v26, v24
	s_nop 0
	v_fma_f32 v27, -v24, v26, 1.0
	v_fmac_f32_e32 v26, v27, v26
	v_div_scale_f32 v27, vcc, v20, v16, v20
	v_mul_f32_e32 v28, v27, v26
	v_fma_f32 v29, -v24, v28, v27
	v_fmac_f32_e32 v28, v29, v26
	v_fma_f32 v24, -v24, v28, v27
	v_div_fmas_f32 v24, v24, v26, v28
	v_div_fixup_f32 v20, v24, v16, v20
	v_div_scale_f32 v16, s[74:75], v17, v17, v21
	v_rcp_f32_e32 v24, v16
	s_nop 0
	v_fma_f32 v26, -v16, v24, 1.0
	v_fmac_f32_e32 v24, v26, v24
	v_div_scale_f32 v26, vcc, v21, v17, v21
	v_mul_f32_e32 v27, v26, v24
	v_fma_f32 v28, -v16, v27, v26
	v_fmac_f32_e32 v27, v28, v24
	v_fma_f32 v16, -v16, v27, v26
	v_div_fmas_f32 v16, v16, v24, v27
	v_div_fixup_f32 v21, v16, v17, v21
	v_and_b32_e32 v17, 0xffff0000, v18
	v_mul_f32_e32 v17, 0xbfb8aa3b, v17
	v_lshlrev_b32_e32 v16, 16, v18
	v_exp_f32_e32 v18, v17
	v_lshlrev_b32_e32 v17, 16, v19
	v_mul_f32_e32 v16, 0xbfb8aa3b, v16
	v_mul_f32_e32 v17, 0xbfb8aa3b, v17
	v_exp_f32_e32 v16, v16
	v_exp_f32_e32 v17, v17
	v_lshlrev_b32_e32 v26, 16, v23
	v_lshlrev_b32_e32 v24, 16, v22
	v_and_b32_e32 v19, 0xffff0000, v19
	v_pk_add_f32 v[16:17], v[16:17], 1.0 op_sel_hi:[1,0]
	v_mul_f32_e32 v19, 0xbfb8aa3b, v19
	v_div_scale_f32 v27, s[74:75], v17, v17, v26
	v_rcp_f32_e32 v28, v27
	v_exp_f32_e32 v19, v19
	v_and_b32_e32 v22, 0xffff0000, v22
	v_and_b32_e32 v23, 0xffff0000, v23
	v_fma_f32 v29, -v27, v28, 1.0
	v_fmac_f32_e32 v28, v29, v28
	v_div_scale_f32 v29, vcc, v26, v17, v26
	v_mul_f32_e32 v30, v29, v28
	v_fma_f32 v31, -v27, v30, v29
	v_fmac_f32_e32 v30, v31, v28
	v_fma_f32 v27, -v27, v30, v29
	v_div_fmas_f32 v27, v27, v28, v30
	v_div_fixup_f32 v26, v27, v17, v26
	v_div_scale_f32 v17, s[74:75], v16, v16, v24
	v_rcp_f32_e32 v27, v17
	s_nop 0
	v_fma_f32 v28, -v17, v27, 1.0
	v_fmac_f32_e32 v27, v28, v27
	v_div_scale_f32 v28, vcc, v24, v16, v24
	v_mul_f32_e32 v29, v28, v27
	v_fma_f32 v30, -v17, v29, v28
	v_fmac_f32_e32 v29, v30, v27
	v_fma_f32 v17, -v17, v29, v28
	v_div_fmas_f32 v17, v17, v27, v29
	v_div_fixup_f32 v24, v17, v16, v24
	v_pk_add_f32 v[16:17], v[18:19], 1.0 op_sel_hi:[1,0]
	s_nop 0
	v_div_scale_f32 v18, s[74:75], v16, v16, v22
	v_rcp_f32_e32 v19, v18
	s_nop 0
	v_fma_f32 v27, -v18, v19, 1.0
	v_fmac_f32_e32 v19, v27, v19
	v_div_scale_f32 v27, vcc, v22, v16, v22
	v_mul_f32_e32 v28, v27, v19
	v_fma_f32 v29, -v18, v28, v27
	v_fmac_f32_e32 v28, v29, v19
	v_fma_f32 v18, -v18, v28, v27
	v_div_fmas_f32 v18, v18, v19, v28
	v_div_fixup_f32 v16, v18, v16, v22
	v_div_scale_f32 v18, s[74:75], v17, v17, v23
	v_rcp_f32_e32 v19, v18
	s_nop 0
	v_fma_f32 v22, -v18, v19, 1.0
	v_fmac_f32_e32 v19, v22, v19
	v_div_scale_f32 v22, vcc, v23, v17, v23
	v_mul_f32_e32 v27, v22, v19
	v_fma_f32 v28, -v18, v27, v22
	v_fmac_f32_e32 v27, v28, v19
	v_fma_f32 v18, -v18, v27, v22
	v_div_fmas_f32 v18, v18, v19, v27
	v_div_fixup_f32 v17, v18, v17, v23
	v_bfe_u32 v18, v17, 16, 1
	v_bfe_u32 v19, v16, 16, 1
	v_bfe_u32 v22, v21, 16, 1
	v_bfe_u32 v23, v20, 16, 1
	v_add3_u32 v20, v20, v23, s14
	v_add3_u32 v21, v21, v22, s14
	v_add3_u32 v16, v16, v19, s14
	v_add3_u32 v17, v17, v18, s14
	v_bfe_u32 v18, v7, 16, 1
	v_bfe_u32 v19, v25, 16, 1
	v_bfe_u32 v22, v24, 16, 1
	v_bfe_u32 v23, v26, 16, 1
	v_add3_u32 v23, v26, v23, s14
	v_add3_u32 v22, v24, v22, s14
	v_add3_u32 v19, v25, v19, s14
	v_add3_u32 v7, v7, v18, s14
	v_lshrrev_b32_e32 v7, 16, v7
	v_lshrrev_b32_e32 v24, 16, v19
	v_lshrrev_b32_e32 v18, 16, v22
	v_lshrrev_b32_e32 v19, 16, v23
	v_and_or_b32 v19, v17, s17, v19
	v_and_or_b32 v18, v16, s17, v18
	v_and_or_b32 v17, v21, s17, v24
	v_and_or_b32 v16, v20, s17, v7
	v_lshlrev_b64 v[20:21], 11, v[48:49]
	v_lshl_add_u64 v[20:21], v[176:177], 0, v[20:21]
	global_store_dwordx4 v[20:21], v[16:19], off offset:256
	s_or_b64 exec, exec, s[76:77]
	s_and_saveexec_b64 s[74:75], s[72:73]
	s_cbranch_execnz .LBB0_753

.LBB0_757:
	v_lshlrev_b32_e32 v7, 16, v8
	v_mul_f32_e32 v7, 0xbfb8aa3b, v7
	v_exp_f32_e32 v16, v7
	v_and_b32_e32 v7, 0xffff0000, v8
	v_mul_f32_e32 v7, 0xbfb8aa3b, v7
	v_exp_f32_e32 v8, v7
	v_lshlrev_b32_e32 v7, 16, v9
	ds_read_b128 v[12:15], v239 offset:3264
	v_mul_f32_e32 v7, 0xbfb8aa3b, v7
	v_exp_f32_e32 v17, v7
	v_and_b32_e32 v7, 0xffff0000, v9
	v_mul_f32_e32 v7, 0xbfb8aa3b, v7
	s_waitcnt lgkmcnt(0)
	v_lshlrev_b32_e32 v18, 16, v13
	v_pk_add_f32 v[16:17], v[16:17], 1.0 op_sel_hi:[1,0]
	v_exp_f32_e32 v9, v7
	v_div_scale_f32 v19, s[70:71], v17, v17, v18
	v_rcp_f32_e32 v20, v19
	v_lshlrev_b32_e32 v7, 16, v12
	v_and_b32_e32 v12, 0xffff0000, v12
	v_pk_add_f32 v[8:9], v[8:9], 1.0 op_sel_hi:[1,0]
	v_fma_f32 v21, -v19, v20, 1.0
	v_fmac_f32_e32 v20, v21, v20
	v_div_scale_f32 v21, vcc, v18, v17, v18
	v_mul_f32_e32 v22, v21, v20
	v_fma_f32 v23, -v19, v22, v21
	v_fmac_f32_e32 v22, v23, v20
	v_fma_f32 v19, -v19, v22, v21
	v_div_fmas_f32 v19, v19, v20, v22
	v_div_fixup_f32 v17, v19, v17, v18
	v_div_scale_f32 v18, s[70:71], v16, v16, v7
	v_rcp_f32_e32 v19, v18
	v_and_b32_e32 v13, 0xffff0000, v13
	v_fma_f32 v20, -v18, v19, 1.0
	v_fmac_f32_e32 v19, v20, v19
	v_div_scale_f32 v20, vcc, v7, v16, v7
	v_mul_f32_e32 v21, v20, v19
	v_fma_f32 v22, -v18, v21, v20
	v_fmac_f32_e32 v21, v22, v19
	v_fma_f32 v18, -v18, v21, v20
	v_div_fmas_f32 v18, v18, v19, v21
	v_div_fixup_f32 v7, v18, v16, v7
	v_div_scale_f32 v16, s[70:71], v8, v8, v12
	v_rcp_f32_e32 v18, v16
	s_nop 0
	v_fma_f32 v19, -v16, v18, 1.0
	v_fmac_f32_e32 v18, v19, v18
	v_div_scale_f32 v19, vcc, v12, v8, v12
	v_mul_f32_e32 v20, v19, v18
	v_fma_f32 v21, -v16, v20, v19
	v_fmac_f32_e32 v20, v21, v18
	v_fma_f32 v16, -v16, v20, v19
	v_div_fmas_f32 v16, v16, v18, v20
	v_div_fixup_f32 v12, v16, v8, v12
	v_div_scale_f32 v8, s[70:71], v9, v9, v13
	v_rcp_f32_e32 v16, v8
	s_nop 0
	v_fma_f32 v18, -v8, v16, 1.0
	v_fmac_f32_e32 v16, v18, v16
	v_div_scale_f32 v18, vcc, v13, v9, v13
	v_mul_f32_e32 v19, v18, v16
	v_fma_f32 v20, -v8, v19, v18
	v_fmac_f32_e32 v19, v20, v16
	v_fma_f32 v8, -v8, v19, v18
	v_div_fmas_f32 v8, v8, v16, v19
	v_div_fixup_f32 v13, v8, v9, v13
	v_and_b32_e32 v9, 0xffff0000, v10
	v_mul_f32_e32 v9, 0xbfb8aa3b, v9
	v_lshlrev_b32_e32 v8, 16, v10
	v_exp_f32_e32 v10, v9
	v_lshlrev_b32_e32 v9, 16, v11
	v_mul_f32_e32 v8, 0xbfb8aa3b, v8
	v_mul_f32_e32 v9, 0xbfb8aa3b, v9
	v_exp_f32_e32 v8, v8
	v_exp_f32_e32 v9, v9
	v_lshlrev_b32_e32 v18, 16, v15
	v_lshlrev_b32_e32 v16, 16, v14
	v_and_b32_e32 v11, 0xffff0000, v11
	v_pk_add_f32 v[8:9], v[8:9], 1.0 op_sel_hi:[1,0]
	v_mul_f32_e32 v11, 0xbfb8aa3b, v11
	v_div_scale_f32 v19, s[70:71], v9, v9, v18
	v_rcp_f32_e32 v20, v19
	v_exp_f32_e32 v11, v11
	v_and_b32_e32 v14, 0xffff0000, v14
	v_and_b32_e32 v15, 0xffff0000, v15
	v_fma_f32 v21, -v19, v20, 1.0
	v_fmac_f32_e32 v20, v21, v20
	v_div_scale_f32 v21, vcc, v18, v9, v18
	v_mul_f32_e32 v22, v21, v20
	v_fma_f32 v23, -v19, v22, v21
	v_fmac_f32_e32 v22, v23, v20
	v_fma_f32 v19, -v19, v22, v21
	v_div_fmas_f32 v19, v19, v20, v22
	v_div_fixup_f32 v18, v19, v9, v18
	v_div_scale_f32 v9, s[70:71], v8, v8, v16
	v_rcp_f32_e32 v19, v9
	s_nop 0
	v_fma_f32 v20, -v9, v19, 1.0
	v_fmac_f32_e32 v19, v20, v19
	v_div_scale_f32 v20, vcc, v16, v8, v16
	v_mul_f32_e32 v21, v20, v19
	v_fma_f32 v22, -v9, v21, v20
	v_fmac_f32_e32 v21, v22, v19
	v_fma_f32 v9, -v9, v21, v20
	v_div_fmas_f32 v9, v9, v19, v21
	v_div_fixup_f32 v16, v9, v8, v16
	v_pk_add_f32 v[8:9], v[10:11], 1.0 op_sel_hi:[1,0]
	s_nop 0
	v_div_scale_f32 v10, s[70:71], v8, v8, v14
	v_rcp_f32_e32 v11, v10
	s_nop 0
	v_fma_f32 v19, -v10, v11, 1.0
	v_fmac_f32_e32 v11, v19, v11
	v_div_scale_f32 v19, vcc, v14, v8, v14
	v_mul_f32_e32 v20, v19, v11
	v_fma_f32 v21, -v10, v20, v19
	v_fmac_f32_e32 v20, v21, v11
	v_fma_f32 v10, -v10, v20, v19
	v_div_fmas_f32 v10, v10, v11, v20
	v_div_fixup_f32 v8, v10, v8, v14
	v_div_scale_f32 v10, s[70:71], v9, v9, v15
	v_rcp_f32_e32 v11, v10
	s_nop 0
	v_fma_f32 v14, -v10, v11, 1.0
	v_fmac_f32_e32 v11, v14, v11
	v_div_scale_f32 v14, vcc, v15, v9, v15
	v_mul_f32_e32 v19, v14, v11
	v_fma_f32 v20, -v10, v19, v14
	v_fmac_f32_e32 v19, v20, v11
	v_fma_f32 v10, -v10, v19, v14
	v_div_fmas_f32 v10, v10, v11, v19
	v_div_fixup_f32 v9, v10, v9, v15
	v_bfe_u32 v10, v9, 16, 1
	v_bfe_u32 v11, v8, 16, 1
	v_bfe_u32 v14, v13, 16, 1
	v_bfe_u32 v15, v12, 16, 1
	v_add3_u32 v12, v12, v15, s14
	v_add3_u32 v13, v13, v14, s14
	v_add3_u32 v8, v8, v11, s14
	v_add3_u32 v9, v9, v10, s14
	v_bfe_u32 v10, v7, 16, 1
	v_bfe_u32 v11, v17, 16, 1
	v_bfe_u32 v14, v16, 16, 1
	v_bfe_u32 v15, v18, 16, 1
	v_add3_u32 v15, v18, v15, s14
	v_add3_u32 v14, v16, v14, s14
	v_add3_u32 v11, v17, v11, s14
	v_add3_u32 v7, v7, v10, s14
	v_lshrrev_b32_e32 v7, 16, v7
	v_lshrrev_b32_e32 v16, 16, v11
	v_lshrrev_b32_e32 v10, 16, v14
	v_lshrrev_b32_e32 v11, 16, v15
	v_and_or_b32 v11, v9, s17, v11
	v_and_or_b32 v10, v8, s17, v10
	v_and_or_b32 v9, v13, s17, v16
	v_and_or_b32 v8, v12, s17, v7
	v_lshlrev_b64 v[12:13], 11, v[44:45]
	v_lshl_add_u64 v[12:13], v[176:177], 0, v[12:13]
	global_store_dwordx4 v[12:13], v[8:11], off offset:256
	s_branch .LBB0_688

.LBB0_839:
	v_lshl_or_b32 v150, s41, 8, v153
	v_lshl_add_u32 v146, s20, 8, v1
	v_readlane_b32 s44, v253, 2
	v_ashrrev_i32_e32 v151, 31, v150
	v_readlane_b32 s45, v253, 3
	v_ashrrev_i32_e32 v147, 31, v146
	v_or_b32_e32 v188, 16, v146
	v_lshl_add_u64 v[148:149], v[150:151], 2, s[44:45]
	v_lshlrev_b64 v[160:161], 12, v[146:147]
	v_ashrrev_i32_e32 v189, 31, v188
	v_lshl_add_u64 v[172:173], v[148:149], 0, v[160:161]
	v_lshlrev_b64 v[176:177], 12, v[188:189]
	global_load_dwordx4 v[160:163], v[172:173], off nt
	global_load_dwordx4 v[164:167], v[172:173], off offset:16 nt
	global_load_dwordx4 v[168:171], v[172:173], off offset:512 nt
	s_nop 0
	global_load_dwordx4 v[172:175], v[172:173], off offset:528 nt
	v_lshl_add_u64 v[190:191], v[148:149], 0, v[176:177]
	global_load_dwordx4 v[176:179], v[190:191], off nt
	global_load_dwordx4 v[180:183], v[190:191], off offset:16 nt
	global_load_dwordx4 v[184:187], v[190:191], off offset:512 nt
	global_load_dwordx4 v[194:197], v[190:191], off offset:528 nt
	v_lshlrev_b64 v[198:199], 11, v[146:147]
	v_lshlrev_b64 v[150:151], 1, v[150:151]
	v_lshl_add_u64 v[198:199], s[82:83], 0, v[198:199]
	v_lshl_add_u64 v[198:199], v[198:199], 0, v[150:151]
	v_or_b32_e32 v190, 32, v146
	v_lshlrev_b64 v[188:189], 11, v[188:189]
	v_ashrrev_i32_e32 v191, 31, v190
	v_lshl_add_u64 v[188:189], s[82:83], 0, v[188:189]
	v_lshlrev_b64 v[200:201], 12, v[190:191]
	v_lshl_add_u64 v[188:189], v[188:189], 0, v[150:151]
	v_lshl_add_u64 v[200:201], v[148:149], 0, v[200:201]
	s_andn2_b64 vcc, exec, s[4:5]
	s_mov_b64 s[4:5], -1
	v_readlane_b32 s46, v253, 4
	v_readlane_b32 s47, v253, 5
	v_readlane_b32 s48, v253, 6
	v_readlane_b32 s49, v253, 7
	v_readlane_b32 s50, v253, 8
	v_readlane_b32 s51, v253, 9
	v_readlane_b32 s52, v253, 10
	v_readlane_b32 s53, v253, 11
	v_readlane_b32 s54, v253, 12
	v_readlane_b32 s55, v253, 13
	v_readlane_b32 s56, v253, 14
	v_readlane_b32 s57, v253, 15
	v_readlane_b32 s58, v253, 16
	v_readlane_b32 s59, v253, 17
	s_waitcnt vmcnt(0)
	v_pk_add_f32 v[126:127], v[126:127], v[160:161]
	v_pk_add_f32 v[124:125], v[124:125], v[166:167]
	v_pk_add_f32 v[122:123], v[122:123], v[164:165]
	v_pk_add_f32 v[160:161], v[108:109], v[174:175]
	v_pk_add_f32 v[128:129], v[128:129], v[162:163]
	v_pk_add_f32 v[112:113], v[112:113], v[170:171]
	v_pk_add_f32 v[110:111], v[110:111], v[168:169]
	v_pk_add_f32 v[162:163], v[106:107], v[172:173]
	v_cvt_pk_bf16_f32 v106, v126, v127
	v_cvt_pk_bf16_f32 v107, v128, v129
	v_cvt_pk_bf16_f32 v108, v122, v123
	v_cvt_pk_bf16_f32 v109, v124, v125
	v_pk_add_f32 v[122:123], v[100:101], v[196:197]
	v_pk_add_f32 v[124:125], v[98:99], v[194:195]
	global_store_dwordx4 v[198:199], v[106:109], off
	v_cvt_pk_bf16_f32 v98, v110, v111
	v_cvt_pk_bf16_f32 v99, v112, v113
	v_cvt_pk_bf16_f32 v100, v162, v163
	v_cvt_pk_bf16_f32 v101, v160, v161
	v_or_b32_e32 v160, 48, v146
	v_pk_add_f32 v[114:115], v[114:115], v[180:181]
	v_ashrrev_i32_e32 v161, 31, v160
	v_pk_add_f32 v[120:121], v[120:121], v[178:179]
	v_pk_add_f32 v[118:119], v[118:119], v[176:177]
	v_pk_add_f32 v[116:117], v[116:117], v[182:183]
	global_store_dwordx4 v[198:199], v[98:101], off offset:256
	v_pk_add_f32 v[104:105], v[104:105], v[186:187]
	v_pk_add_f32 v[102:103], v[102:103], v[184:185]
	v_cvt_pk_bf16_f32 v98, v118, v119
	v_cvt_pk_bf16_f32 v99, v120, v121
	v_cvt_pk_bf16_f32 v100, v114, v115
	v_cvt_pk_bf16_f32 v101, v116, v117
	v_lshlrev_b64 v[114:115], 12, v[160:161]
	global_store_dwordx4 v[188:189], v[98:101], off
	v_lshl_add_u64 v[126:127], v[148:149], 0, v[114:115]
	v_lshlrev_b64 v[164:165], 11, v[190:191]
	v_cvt_pk_bf16_f32 v98, v102, v103
	v_cvt_pk_bf16_f32 v99, v104, v105
	v_cvt_pk_bf16_f32 v100, v124, v125
	v_cvt_pk_bf16_f32 v101, v122, v123
	global_store_dwordx4 v[188:189], v[98:101], off offset:256
	global_load_dwordx4 v[98:101], v[200:201], off nt
	s_nop 0
	global_load_dwordx4 v[102:105], v[200:201], off offset:16 nt
	global_load_dwordx4 v[106:109], v[200:201], off offset:528 nt
	global_load_dwordx4 v[110:113], v[200:201], off offset:512 nt
	global_load_dwordx4 v[114:117], v[126:127], off nt
	global_load_dwordx4 v[118:121], v[126:127], off offset:16 nt
	global_load_dwordx4 v[122:125], v[126:127], off offset:512 nt
	s_nop 0
	global_load_dwordx4 v[126:129], v[126:127], off offset:528 nt
	v_lshl_add_u64 v[164:165], s[82:83], 0, v[164:165]
	v_lshlrev_b64 v[160:161], 11, v[160:161]
	v_lshl_add_u64 v[164:165], v[164:165], 0, v[150:151]
	v_lshl_add_u64 v[160:161], s[82:83], 0, v[160:161]
	v_lshl_add_u64 v[160:161], v[160:161], 0, v[150:151]
	v_add_u32_e32 v162, 0x80, v146
	v_ashrrev_i32_e32 v163, 31, v162
	v_lshlrev_b64 v[166:167], 12, v[162:163]
	v_lshl_add_u64 v[166:167], v[148:149], 0, v[166:167]
	s_waitcnt vmcnt(3)
	v_pk_add_f32 v[88:89], v[88:89], v[116:117]
	v_pk_add_f32 v[96:97], v[96:97], v[100:101]
	v_pk_add_f32 v[94:95], v[94:95], v[98:99]
	v_pk_add_f32 v[92:93], v[92:93], v[104:105]
	v_pk_add_f32 v[90:91], v[90:91], v[102:103]
	s_waitcnt vmcnt(0)
	v_pk_add_f32 v[98:99], v[68:69], v[128:129]
	v_pk_add_f32 v[100:101], v[66:67], v[126:127]
	v_cvt_pk_bf16_f32 v66, v94, v95
	v_cvt_pk_bf16_f32 v67, v96, v97
	v_cvt_pk_bf16_f32 v68, v90, v91
	v_cvt_pk_bf16_f32 v69, v92, v93
	v_pk_add_f32 v[80:81], v[80:81], v[112:113]
	v_pk_add_f32 v[78:79], v[78:79], v[110:111]
	v_pk_add_f32 v[76:77], v[76:77], v[108:109]
	v_pk_add_f32 v[74:75], v[74:75], v[106:107]
	global_store_dwordx4 v[164:165], v[66:69], off
	v_pk_add_f32 v[86:87], v[86:87], v[114:115]
	v_pk_add_f32 v[84:85], v[84:85], v[120:121]
	v_cvt_pk_bf16_f32 v66, v78, v79
	v_cvt_pk_bf16_f32 v67, v80, v81
	v_cvt_pk_bf16_f32 v68, v74, v75
	v_cvt_pk_bf16_f32 v69, v76, v77
	v_pk_add_f32 v[82:83], v[82:83], v[118:119]
	global_store_dwordx4 v[164:165], v[66:69], off offset:256
	v_pk_add_f32 v[72:73], v[72:73], v[124:125]
	v_pk_add_f32 v[70:71], v[70:71], v[122:123]
	v_cvt_pk_bf16_f32 v66, v86, v87
	v_cvt_pk_bf16_f32 v67, v88, v89
	v_cvt_pk_bf16_f32 v68, v82, v83
	v_cvt_pk_bf16_f32 v69, v84, v85
	global_store_dwordx4 v[160:161], v[66:69], off
	v_lshlrev_b64 v[102:103], 11, v[162:163]
	v_lshl_add_u64 v[102:103], s[82:83], 0, v[102:103]
	v_cvt_pk_bf16_f32 v66, v70, v71
	v_cvt_pk_bf16_f32 v67, v72, v73
	v_cvt_pk_bf16_f32 v68, v100, v101
	v_cvt_pk_bf16_f32 v69, v98, v99
	v_add_u32_e32 v98, 0x90, v146
	v_ashrrev_i32_e32 v99, 31, v98
	v_lshlrev_b64 v[82:83], 12, v[98:99]
	global_store_dwordx4 v[160:161], v[66:69], off offset:256
	v_lshl_add_u64 v[94:95], v[148:149], 0, v[82:83]
	global_load_dwordx4 v[66:69], v[166:167], off nt
	global_load_dwordx4 v[70:73], v[166:167], off offset:16 nt
	global_load_dwordx4 v[74:77], v[166:167], off offset:528 nt
	global_load_dwordx4 v[78:81], v[166:167], off offset:512 nt
	global_load_dwordx4 v[82:85], v[94:95], off nt
	global_load_dwordx4 v[86:89], v[94:95], off offset:16 nt
	global_load_dwordx4 v[90:93], v[94:95], off offset:512 nt
	s_nop 0
	global_load_dwordx4 v[94:97], v[94:95], off offset:528 nt
	v_lshlrev_b64 v[98:99], 11, v[98:99]
	v_lshl_add_u64 v[102:103], v[102:103], 0, v[150:151]
	v_lshl_add_u64 v[98:99], s[82:83], 0, v[98:99]
	v_lshl_add_u64 v[98:99], v[98:99], 0, v[150:151]
	v_add_u32_e32 v100, 0xa0, v146
	v_ashrrev_i32_e32 v101, 31, v100
	v_lshlrev_b64 v[104:105], 12, v[100:101]
	v_lshl_add_u64 v[104:105], v[148:149], 0, v[104:105]
	s_waitcnt vmcnt(7)
	v_pk_add_f32 v[64:65], v[64:65], v[68:69]
	v_pk_add_f32 v[62:63], v[62:63], v[66:67]
	s_waitcnt vmcnt(6)
	v_pk_add_f32 v[60:61], v[60:61], v[72:73]
	v_pk_add_f32 v[58:59], v[58:59], v[70:71]
	s_waitcnt vmcnt(0)
	v_pk_add_f32 v[66:67], v[36:37], v[96:97]
	v_pk_add_f32 v[68:69], v[34:35], v[94:95]
	v_cvt_pk_bf16_f32 v34, v62, v63
	v_cvt_pk_bf16_f32 v35, v64, v65
	v_cvt_pk_bf16_f32 v36, v58, v59
	v_cvt_pk_bf16_f32 v37, v60, v61
	v_pk_add_f32 v[48:49], v[48:49], v[80:81]
	v_pk_add_f32 v[46:47], v[46:47], v[78:79]
	v_pk_add_f32 v[44:45], v[44:45], v[76:77]
	v_pk_add_f32 v[42:43], v[42:43], v[74:75]
	global_store_dwordx4 v[102:103], v[34:37], off
	v_pk_add_f32 v[56:57], v[56:57], v[84:85]
	v_pk_add_f32 v[54:55], v[54:55], v[82:83]
	v_cvt_pk_bf16_f32 v34, v46, v47
	v_cvt_pk_bf16_f32 v35, v48, v49
	v_cvt_pk_bf16_f32 v36, v42, v43
	v_cvt_pk_bf16_f32 v37, v44, v45
	v_pk_add_f32 v[52:53], v[52:53], v[88:89]
	v_pk_add_f32 v[50:51], v[50:51], v[86:87]
	global_store_dwordx4 v[102:103], v[34:37], off offset:256
	v_pk_add_f32 v[40:41], v[40:41], v[92:93]
	v_pk_add_f32 v[38:39], v[38:39], v[90:91]
	v_cvt_pk_bf16_f32 v34, v54, v55
	v_cvt_pk_bf16_f32 v35, v56, v57
	v_cvt_pk_bf16_f32 v36, v50, v51
	v_cvt_pk_bf16_f32 v37, v52, v53
	global_store_dwordx4 v[98:99], v[34:37], off
	s_nop 1
	v_cvt_pk_bf16_f32 v34, v38, v39
	v_cvt_pk_bf16_f32 v35, v40, v41
	v_cvt_pk_bf16_f32 v36, v68, v69
	v_cvt_pk_bf16_f32 v37, v66, v67
	v_add_u32_e32 v66, 0xb0, v146
	v_ashrrev_i32_e32 v67, 31, v66
	v_lshlrev_b64 v[50:51], 12, v[66:67]
	global_store_dwordx4 v[98:99], v[34:37], off offset:256
	v_lshl_add_u64 v[62:63], v[148:149], 0, v[50:51]
	global_load_dwordx4 v[34:37], v[104:105], off nt
	global_load_dwordx4 v[38:41], v[104:105], off offset:16 nt
	global_load_dwordx4 v[42:45], v[104:105], off offset:528 nt
	global_load_dwordx4 v[46:49], v[104:105], off offset:512 nt
	global_load_dwordx4 v[50:53], v[62:63], off nt
	global_load_dwordx4 v[54:57], v[62:63], off offset:16 nt
	global_load_dwordx4 v[58:61], v[62:63], off offset:512 nt
	s_nop 0
	global_load_dwordx4 v[62:65], v[62:63], off offset:528 nt
	v_lshlrev_b64 v[68:69], 11, v[100:101]
	v_lshl_add_u64 v[68:69], s[82:83], 0, v[68:69]
	v_lshlrev_b64 v[66:67], 11, v[66:67]
	v_lshl_add_u64 v[68:69], v[68:69], 0, v[150:151]
	v_lshl_add_u64 v[66:67], s[82:83], 0, v[66:67]
	v_lshl_add_u64 v[66:67], v[66:67], 0, v[150:151]
	s_waitcnt vmcnt(7)
	v_pk_add_f32 v[32:33], v[32:33], v[36:37]
	v_pk_add_f32 v[30:31], v[30:31], v[34:35]
	s_waitcnt vmcnt(6)
	v_pk_add_f32 v[28:29], v[28:29], v[40:41]
	v_pk_add_f32 v[26:27], v[26:27], v[38:39]
	s_waitcnt vmcnt(0)
	v_pk_add_f32 v[34:35], v[4:5], v[64:65]
	v_pk_add_f32 v[36:37], v[2:3], v[62:63]
	v_cvt_pk_bf16_f32 v2, v30, v31
	v_cvt_pk_bf16_f32 v3, v32, v33
	v_cvt_pk_bf16_f32 v4, v26, v27
	v_cvt_pk_bf16_f32 v5, v28, v29
	v_pk_add_f32 v[16:17], v[16:17], v[48:49]
	v_pk_add_f32 v[14:15], v[14:15], v[46:47]
	v_pk_add_f32 v[12:13], v[12:13], v[44:45]
	v_pk_add_f32 v[10:11], v[10:11], v[42:43]
	global_store_dwordx4 v[68:69], v[2:5], off
	v_pk_add_f32 v[24:25], v[24:25], v[52:53]
	v_pk_add_f32 v[22:23], v[22:23], v[50:51]
	v_cvt_pk_bf16_f32 v2, v14, v15
	v_cvt_pk_bf16_f32 v3, v16, v17
	v_cvt_pk_bf16_f32 v4, v10, v11
	v_cvt_pk_bf16_f32 v5, v12, v13
	v_pk_add_f32 v[20:21], v[20:21], v[56:57]
	v_pk_add_f32 v[18:19], v[18:19], v[54:55]
	global_store_dwordx4 v[68:69], v[2:5], off offset:256
	v_pk_add_f32 v[8:9], v[8:9], v[60:61]
	v_pk_add_f32 v[6:7], v[6:7], v[58:59]
	v_cvt_pk_bf16_f32 v2, v22, v23
	v_cvt_pk_bf16_f32 v3, v24, v25
	v_cvt_pk_bf16_f32 v4, v18, v19
	v_cvt_pk_bf16_f32 v5, v20, v21
	global_store_dwordx4 v[66:67], v[2:5], off
	s_nop 1
	v_cvt_pk_bf16_f32 v2, v6, v7
	v_cvt_pk_bf16_f32 v3, v8, v9
	v_cvt_pk_bf16_f32 v4, v36, v37
	v_cvt_pk_bf16_f32 v5, v34, v35
	global_store_dwordx4 v[66:67], v[2:5], off offset:256
	s_cbranch_vccnz .LBB0_828
	s_andn2_b64 vcc, exec, s[6:7]
	s_cbranch_vccnz .LBB0_827
	s_barrier
	s_branch .LBB0_827

.LBB0_940:
	s_or_b64 exec, exec, s[8:9]
	s_waitcnt lgkmcnt(0)
	s_barrier
	s_and_saveexec_b64 s[6:7], s[4:5]
	s_cbranch_execz .LBB0_943
	v_lshl_add_u32 v1, v0, 2, 0
	v_add_u32_e32 v1, 0x1ee80, v1
	ds_read_b32 v1, v1
	s_waitcnt lgkmcnt(0)
	v_cmp_lt_i32_e32 vcc, -1, v1
	s_and_b64 exec, exec, vcc
	s_cbranch_execz .LBB0_943
	v_bfe_u32 v2, v1, 8, 8
	v_mul_u32_u24_e32 v6, 0x4010, v2
	v_lshl_add_u32 v2, v2, 2, 0
	v_add_u32_e32 v2, 0x1ee00, v2
	ds_read_b32 v7, v2
	v_lshl_add_u32 v2, v0, 4, 0
	v_add_u32_e32 v2, 0x1f180, v2
	ds_read_b128 v[2:5], v2
	v_and_b32_e32 v8, 0xff, v1
	s_waitcnt lgkmcnt(1)
	v_add3_u32 v6, v6, v8, v7
	v_ashrrev_i32_e32 v7, 31, v6
	v_lshrrev_b32_e32 v1, 16, v1
	v_lshl_add_u64 v[8:9], v[6:7], 2, s[24:25]
	v_lshl_add_u64 v[6:7], v[6:7], 4, s[28:29]
	global_store_dword v[8:9], v1, off
	s_waitcnt lgkmcnt(0)
	global_store_dwordx4 v[6:7], v[2:5], off

.LBB0_1131:
	v_cmp_gt_i32_e64 s[18:19], s64, v187
	v_cmp_gt_i32_e64 s[16:17], s64, v188
	v_cmp_gt_i32_e64 s[14:15], s64, v189
	v_cndmask_b32_e64 v130, 0, v187, s[18:19]
	v_cndmask_b32_e64 v132, 0, v188, s[16:17]
	v_cndmask_b32_e64 v134, 0, v189, s[14:15]
	v_add_u32_e32 v130, s87, v130
	v_add_u32_e32 v132, s87, v132
	v_add_u32_e32 v134, s87, v134
	v_ashrrev_i32_e32 v131, 31, v130
	v_ashrrev_i32_e32 v133, 31, v132
	v_ashrrev_i32_e32 v135, 31, v134
	v_lshl_add_u64 v[130:131], v[130:131], 2, s[24:25]
	v_lshl_add_u64 v[132:133], v[132:133], 2, s[24:25]
	v_lshl_add_u64 v[134:135], v[134:135], 2, s[24:25]
	global_load_dword v130, v[130:131], off
	s_nop 0
	global_load_dword v132, v[132:133], off
	s_nop 0
	global_load_dword v134, v[134:135], off
	v_cmp_gt_i32_e64 s[12:13], s64, v195
	v_cmp_gt_i32_e64 s[10:11], s64, v196
	v_cmp_gt_i32_e64 s[8:9], s64, v197
	v_cmp_gt_i32_e32 vcc, s64, v198
	v_cndmask_b32_e64 v131, 0, v195, s[12:13]
	v_cndmask_b32_e64 v133, 0, v196, s[10:11]
	v_cndmask_b32_e64 v135, 0, v197, s[8:9]
	v_cndmask_b32_e32 v137, 0, v198, vcc
	v_lshl_or_b32 v166, s20, 8, v199
	v_add_u32_e32 v136, s87, v131
	v_add_u32_e32 v138, s87, v133
	v_add_u32_e32 v140, s87, v135
	v_add_u32_e32 v142, s87, v137
	v_ashrrev_i32_e32 v167, 31, v166
	v_ashrrev_i32_e32 v137, 31, v136
	v_ashrrev_i32_e32 v139, 31, v138
	v_ashrrev_i32_e32 v141, 31, v140
	v_ashrrev_i32_e32 v143, 31, v142
	v_lshl_add_u64 v[168:169], v[166:167], 1, s[82:83]
	v_lshl_add_u64 v[136:137], v[136:137], 2, s[24:25]
	v_lshl_add_u64 v[138:139], v[138:139], 2, s[24:25]
	v_lshl_add_u64 v[140:141], v[140:141], 2, s[24:25]
	v_lshl_add_u64 v[142:143], v[142:143], 2, s[24:25]
	global_load_dword v170, v[136:137], off
	global_load_dword v176, v[138:139], off
	global_load_dword v174, v[140:141], off
	global_load_dword v172, v[142:143], off
	v_cmp_gt_i32_e64 s[20:21], s64, v157
	s_waitcnt vmcnt(0)
	v_ashrrev_i32_e32 v131, 31, v130
	v_ashrrev_i32_e32 v133, 31, v132
	v_ashrrev_i32_e32 v135, 31, v134
	v_lshlrev_b64 v[182:183], 11, v[130:131]
	v_lshlrev_b64 v[180:181], 11, v[132:133]
	v_lshlrev_b64 v[178:179], 11, v[134:135]
	v_lshl_add_u64 v[130:131], v[168:169], 0, v[182:183]
	v_lshl_add_u64 v[132:133], v[168:169], 0, v[180:181]
	v_lshl_add_u64 v[190:191], v[168:169], 0, v[178:179]
	global_load_dwordx4 v[150:153], v[130:131], off
	global_load_dwordx4 v[146:149], v[130:131], off offset:256
	global_load_dwordx4 v[142:145], v[132:133], off
	global_load_dwordx4 v[138:141], v[132:133], off offset:256
	global_load_dwordx4 v[134:137], v[190:191], off
	s_nop 0
	global_load_dwordx4 v[130:133], v[190:191], off offset:256
	s_and_saveexec_b64 s[64:65], s[20:21]
	s_cbranch_execz .LBB0_1135
	v_add_u32_e32 v190, s87, v157
	v_ashrrev_i32_e32 v191, 31, v190
	v_lshl_add_u64 v[190:191], v[190:191], 2, s[24:25]
	global_load_dword v190, v[190:191], off
	s_waitcnt vmcnt(0)
	v_ashrrev_i32_e32 v191, 31, v190
	v_lshlrev_b64 v[190:191], 11, v[190:191]
	v_lshl_add_u64 v[208:209], v[168:169], 0, v[190:191]
	global_load_dwordx4 v[204:207], v[208:209], off offset:256
	global_load_dwordx4 v[210:213], v[208:209], off
	s_waitcnt vmcnt(0)
	v_lshlrev_b32_e32 v208, 16, v210
	v_and_b32_e32 v209, 0xffff0000, v210
	v_lshlrev_b32_e32 v210, 16, v211
	v_and_b32_e32 v211, 0xffff0000, v211
	v_pk_add_f32 v[128:129], v[128:129], v[210:211]
	v_pk_add_f32 v[126:127], v[126:127], v[208:209]
	v_lshlrev_b32_e32 v208, 16, v212
	v_and_b32_e32 v209, 0xffff0000, v212
	v_lshlrev_b32_e32 v210, 16, v213
	v_and_b32_e32 v211, 0xffff0000, v213
	v_pk_add_f32 v[210:211], v[124:125], v[210:211]
	v_pk_add_f32 v[124:125], v[122:123], v[208:209]
	v_cvt_pk_bf16_f32 v122, v126, v127
	v_lshl_add_u64 v[126:127], s[2:3], 0, v[190:191]
	v_cvt_pk_bf16_f32 v123, v128, v129
	v_cvt_pk_bf16_f32 v124, v124, v125
	v_cvt_pk_bf16_f32 v125, v210, v211
	v_lshl_add_u64 v[126:127], v[166:167], 1, v[126:127]
	global_store_dwordx4 v[126:127], v[122:125], off
	v_and_b32_e32 v208, 63, v0
	s_nop 0
	v_lshlrev_b32_e32 v122, 16, v204
	v_and_b32_e32 v123, 0xffff0000, v204
	v_lshlrev_b32_e32 v124, 16, v205
	v_and_b32_e32 v125, 0xffff0000, v205
	v_pk_add_f32 v[120:121], v[120:121], v[124:125]
	v_pk_add_f32 v[118:119], v[118:119], v[122:123]
	v_lshlrev_b32_e32 v122, 16, v206
	v_and_b32_e32 v123, 0xffff0000, v206
	v_lshlrev_b32_e32 v124, 16, v207
	v_and_b32_e32 v125, 0xffff0000, v207
	v_pk_add_f32 v[124:125], v[116:117], v[124:125]
	v_pk_add_f32 v[116:117], v[114:115], v[122:123]
	v_cvt_pk_bf16_f32 v114, v118, v119
	v_cvt_pk_bf16_f32 v115, v120, v121
	s_nop 0
	v_cvt_pk_bf16_f32 v116, v116, v117
	v_cvt_pk_bf16_f32 v117, v124, v125
	global_store_dwordx4 v[126:127], v[114:117], off offset:256
	s_or_b64 exec, exec, s[64:65]
	s_and_saveexec_b64 s[20:21], s[18:19]
	s_cbranch_execnz .LBB0_1136

.LBB0_1134:
	s_waitcnt vmcnt(0)
	v_lshlrev_b32_e32 v98, 16, v142
	v_and_b32_e32 v99, 0xffff0000, v142
	v_lshlrev_b32_e32 v100, 16, v143
	v_and_b32_e32 v101, 0xffff0000, v143
	v_pk_add_f32 v[96:97], v[96:97], v[100:101]
	v_pk_add_f32 v[94:95], v[94:95], v[98:99]
	v_lshlrev_b32_e32 v98, 16, v144
	v_and_b32_e32 v99, 0xffff0000, v144
	v_lshlrev_b32_e32 v100, 16, v145
	v_and_b32_e32 v101, 0xffff0000, v145
	v_pk_add_f32 v[100:101], v[92:93], v[100:101]
	v_pk_add_f32 v[92:93], v[90:91], v[98:99]
	v_cvt_pk_bf16_f32 v90, v94, v95
	v_lshl_add_u64 v[94:95], s[2:3], 0, v[180:181]
	v_cvt_pk_bf16_f32 v91, v96, v97
	v_cvt_pk_bf16_f32 v92, v92, v93
	v_cvt_pk_bf16_f32 v93, v100, v101
	v_lshl_add_u64 v[94:95], v[166:167], 1, v[94:95]
	global_store_dwordx4 v[94:95], v[90:93], off
	s_nop 1
	v_lshlrev_b32_e32 v90, 16, v138
	v_and_b32_e32 v91, 0xffff0000, v138
	v_lshlrev_b32_e32 v92, 16, v139
	v_and_b32_e32 v93, 0xffff0000, v139
	v_pk_add_f32 v[88:89], v[88:89], v[92:93]
	v_pk_add_f32 v[86:87], v[86:87], v[90:91]
	v_lshlrev_b32_e32 v90, 16, v140
	v_and_b32_e32 v91, 0xffff0000, v140
	v_lshlrev_b32_e32 v92, 16, v141
	v_and_b32_e32 v93, 0xffff0000, v141
	v_pk_add_f32 v[92:93], v[84:85], v[92:93]
	v_pk_add_f32 v[84:85], v[82:83], v[90:91]
	v_cvt_pk_bf16_f32 v82, v86, v87
	v_cvt_pk_bf16_f32 v83, v88, v89
	s_nop 0
	v_cvt_pk_bf16_f32 v84, v84, v85
	v_cvt_pk_bf16_f32 v85, v92, v93
	global_store_dwordx4 v[94:95], v[82:85], off offset:256
	s_or_b64 exec, exec, s[18:19]
	s_and_saveexec_b64 s[16:17], s[14:15]
	s_cbranch_execnz .LBB0_1138
	s_branch .LBB0_1139

.LBB0_1136:
	s_waitcnt vmcnt(0)
	v_lshlrev_b32_e32 v114, 16, v150
	v_and_b32_e32 v115, 0xffff0000, v150
	v_lshlrev_b32_e32 v116, 16, v151
	v_and_b32_e32 v117, 0xffff0000, v151
	v_pk_add_f32 v[112:113], v[112:113], v[116:117]
	v_pk_add_f32 v[110:111], v[110:111], v[114:115]
	v_lshlrev_b32_e32 v114, 16, v152
	v_and_b32_e32 v115, 0xffff0000, v152
	v_lshlrev_b32_e32 v116, 16, v153
	v_and_b32_e32 v117, 0xffff0000, v153
	v_pk_add_f32 v[116:117], v[108:109], v[116:117]
	v_pk_add_f32 v[108:109], v[106:107], v[114:115]
	v_cvt_pk_bf16_f32 v106, v110, v111
	v_lshl_add_u64 v[110:111], s[2:3], 0, v[182:183]
	v_cvt_pk_bf16_f32 v107, v112, v113
	v_cvt_pk_bf16_f32 v108, v108, v109
	v_cvt_pk_bf16_f32 v109, v116, v117
	v_lshl_add_u64 v[110:111], v[166:167], 1, v[110:111]
	global_store_dwordx4 v[110:111], v[106:109], off
	s_nop 1
	v_lshlrev_b32_e32 v106, 16, v146
	v_and_b32_e32 v107, 0xffff0000, v146
	v_lshlrev_b32_e32 v108, 16, v147
	v_and_b32_e32 v109, 0xffff0000, v147
	v_pk_add_f32 v[104:105], v[104:105], v[108:109]
	v_pk_add_f32 v[102:103], v[102:103], v[106:107]
	v_lshlrev_b32_e32 v106, 16, v148
	v_and_b32_e32 v107, 0xffff0000, v148
	v_lshlrev_b32_e32 v108, 16, v149
	v_and_b32_e32 v109, 0xffff0000, v149
	v_pk_add_f32 v[108:109], v[100:101], v[108:109]
	v_pk_add_f32 v[100:101], v[98:99], v[106:107]
	v_cvt_pk_bf16_f32 v98, v102, v103
	v_cvt_pk_bf16_f32 v99, v104, v105
	s_nop 0
	v_cvt_pk_bf16_f32 v100, v100, v101
	v_cvt_pk_bf16_f32 v101, v108, v109
	global_store_dwordx4 v[110:111], v[98:101], off offset:256
	s_or_b64 exec, exec, s[20:21]
	s_and_saveexec_b64 s[18:19], s[16:17]
	s_cbranch_execnz .LBB0_1134

.LBB0_1138:
	s_waitcnt vmcnt(0)
	v_lshlrev_b32_e32 v82, 16, v134
	v_and_b32_e32 v83, 0xffff0000, v134
	v_lshlrev_b32_e32 v84, 16, v135
	v_and_b32_e32 v85, 0xffff0000, v135
	v_pk_add_f32 v[80:81], v[80:81], v[84:85]
	v_pk_add_f32 v[78:79], v[78:79], v[82:83]
	v_lshlrev_b32_e32 v82, 16, v136
	v_and_b32_e32 v83, 0xffff0000, v136
	v_lshlrev_b32_e32 v84, 16, v137
	v_and_b32_e32 v85, 0xffff0000, v137
	v_pk_add_f32 v[84:85], v[76:77], v[84:85]
	v_pk_add_f32 v[76:77], v[74:75], v[82:83]
	v_cvt_pk_bf16_f32 v74, v78, v79
	v_lshl_add_u64 v[78:79], s[2:3], 0, v[178:179]
	v_cvt_pk_bf16_f32 v75, v80, v81
	v_cvt_pk_bf16_f32 v76, v76, v77
	v_cvt_pk_bf16_f32 v77, v84, v85
	v_lshl_add_u64 v[78:79], v[166:167], 1, v[78:79]
	global_store_dwordx4 v[78:79], v[74:77], off
	s_nop 1
	v_lshlrev_b32_e32 v74, 16, v130
	v_and_b32_e32 v75, 0xffff0000, v130
	v_lshlrev_b32_e32 v76, 16, v131
	v_and_b32_e32 v77, 0xffff0000, v131
	v_pk_add_f32 v[64:65], v[64:65], v[76:77]
	v_pk_add_f32 v[62:63], v[62:63], v[74:75]
	v_lshlrev_b32_e32 v74, 16, v132
	v_and_b32_e32 v75, 0xffff0000, v132
	v_lshlrev_b32_e32 v76, 16, v133
	v_and_b32_e32 v77, 0xffff0000, v133
	v_pk_add_f32 v[76:77], v[60:61], v[76:77]
	v_pk_add_f32 v[60:61], v[58:59], v[74:75]
	v_cvt_pk_bf16_f32 v58, v62, v63
	v_cvt_pk_bf16_f32 v59, v64, v65
	s_nop 0
	v_cvt_pk_bf16_f32 v60, v60, v61
	v_cvt_pk_bf16_f32 v61, v76, v77
	global_store_dwordx4 v[78:79], v[58:61], off offset:256
.LBB0_1139:
	s_or_b64 exec, exec, s[16:17]
	v_ashrrev_i32_e32 v177, 31, v176
	v_lshlrev_b64 v[94:95], 11, v[176:177]
	v_ashrrev_i32_e32 v175, 31, v174
	v_lshl_add_u64 v[58:59], v[168:169], 0, v[94:95]
	v_lshlrev_b64 v[92:93], 11, v[174:175]
	v_ashrrev_i32_e32 v173, 31, v172
	global_load_dwordx4 v[86:89], v[58:59], off
	global_load_dwordx4 v[82:85], v[58:59], off offset:256
	v_lshl_add_u64 v[58:59], v[168:169], 0, v[92:93]
	v_lshlrev_b64 v[90:91], 11, v[172:173]
	global_load_dwordx4 v[78:81], v[58:59], off
	global_load_dwordx4 v[74:77], v[58:59], off offset:256
	v_lshl_add_u64 v[58:59], v[168:169], 0, v[90:91]
	global_load_dwordx4 v[62:65], v[58:59], off
	s_nop 0
	global_load_dwordx4 v[58:61], v[58:59], off offset:256
	s_and_saveexec_b64 s[14:15], s[12:13]
	s_cbranch_execz .LBB0_1144
	v_ashrrev_i32_e32 v171, 31, v170
	v_lshlrev_b64 v[104:105], 11, v[170:171]
	v_lshl_add_u64 v[100:101], v[168:169], 0, v[104:105]
	global_load_dwordx4 v[96:99], v[100:101], off offset:256
	s_nop 0
	global_load_dwordx4 v[100:103], v[100:101], off
	s_waitcnt vmcnt(0)
	v_lshlrev_b32_e32 v106, 16, v100
	v_and_b32_e32 v107, 0xffff0000, v100
	v_lshlrev_b32_e32 v100, 16, v101
	v_and_b32_e32 v101, 0xffff0000, v101
	v_pk_add_f32 v[72:73], v[72:73], v[100:101]
	v_pk_add_f32 v[70:71], v[70:71], v[106:107]
	v_lshlrev_b32_e32 v100, 16, v102
	v_and_b32_e32 v101, 0xffff0000, v102
	v_lshlrev_b32_e32 v102, 16, v103
	v_and_b32_e32 v103, 0xffff0000, v103
	v_pk_add_f32 v[102:103], v[68:69], v[102:103]
	v_pk_add_f32 v[68:69], v[66:67], v[100:101]
	v_cvt_pk_bf16_f32 v66, v70, v71
	v_lshl_add_u64 v[70:71], s[2:3], 0, v[104:105]
	v_cvt_pk_bf16_f32 v67, v72, v73
	v_cvt_pk_bf16_f32 v68, v68, v69
	v_cvt_pk_bf16_f32 v69, v102, v103
	v_lshl_add_u64 v[70:71], v[166:167], 1, v[70:71]
	global_store_dwordx4 v[70:71], v[66:69], off
	s_nop 1
	v_lshlrev_b32_e32 v66, 16, v96
	v_and_b32_e32 v67, 0xffff0000, v96
	v_lshlrev_b32_e32 v68, 16, v97
	v_and_b32_e32 v69, 0xffff0000, v97
	v_pk_add_f32 v[56:57], v[56:57], v[68:69]
	v_pk_add_f32 v[54:55], v[54:55], v[66:67]
	v_lshlrev_b32_e32 v66, 16, v98
	v_and_b32_e32 v67, 0xffff0000, v98
	v_lshlrev_b32_e32 v68, 16, v99
	v_and_b32_e32 v69, 0xffff0000, v99
	v_pk_add_f32 v[68:69], v[52:53], v[68:69]
	v_pk_add_f32 v[52:53], v[50:51], v[66:67]
	v_cvt_pk_bf16_f32 v50, v54, v55
	v_cvt_pk_bf16_f32 v51, v56, v57
	s_nop 0
	v_cvt_pk_bf16_f32 v52, v52, v53
	v_cvt_pk_bf16_f32 v53, v68, v69
	global_store_dwordx4 v[70:71], v[50:53], off offset:256
	s_or_b64 exec, exec, s[14:15]
	s_and_saveexec_b64 s[12:13], s[10:11]
	s_cbranch_execnz .LBB0_1145

.LBB0_1142:
	s_waitcnt vmcnt(0)
	v_lshlrev_b32_e32 v34, 16, v78
	v_and_b32_e32 v35, 0xffff0000, v78
	v_lshlrev_b32_e32 v36, 16, v79
	v_and_b32_e32 v37, 0xffff0000, v79
	v_pk_add_f32 v[32:33], v[32:33], v[36:37]
	v_pk_add_f32 v[30:31], v[30:31], v[34:35]
	v_lshlrev_b32_e32 v34, 16, v80
	v_and_b32_e32 v35, 0xffff0000, v80
	v_lshlrev_b32_e32 v36, 16, v81
	v_and_b32_e32 v37, 0xffff0000, v81
	v_pk_add_f32 v[36:37], v[28:29], v[36:37]
	v_pk_add_f32 v[28:29], v[26:27], v[34:35]
	v_cvt_pk_bf16_f32 v26, v30, v31
	v_lshl_add_u64 v[30:31], s[2:3], 0, v[92:93]
	v_cvt_pk_bf16_f32 v27, v32, v33
	v_cvt_pk_bf16_f32 v28, v28, v29
	v_cvt_pk_bf16_f32 v29, v36, v37
	v_lshl_add_u64 v[30:31], v[166:167], 1, v[30:31]
	global_store_dwordx4 v[30:31], v[26:29], off
	s_nop 1
	v_lshlrev_b32_e32 v26, 16, v74
	v_and_b32_e32 v27, 0xffff0000, v74
	v_lshlrev_b32_e32 v28, 16, v75
	v_and_b32_e32 v29, 0xffff0000, v75
	v_pk_add_f32 v[24:25], v[24:25], v[28:29]
	v_pk_add_f32 v[22:23], v[22:23], v[26:27]
	v_lshlrev_b32_e32 v26, 16, v76
	v_and_b32_e32 v27, 0xffff0000, v76
	v_lshlrev_b32_e32 v28, 16, v77
	v_and_b32_e32 v29, 0xffff0000, v77
	v_pk_add_f32 v[28:29], v[20:21], v[28:29]
	v_pk_add_f32 v[20:21], v[18:19], v[26:27]
	v_cvt_pk_bf16_f32 v18, v22, v23
	v_cvt_pk_bf16_f32 v19, v24, v25
	s_nop 0
	v_cvt_pk_bf16_f32 v20, v20, v21
	v_cvt_pk_bf16_f32 v21, v28, v29
	global_store_dwordx4 v[30:31], v[18:21], off offset:256
	s_or_b64 exec, exec, s[10:11]
	s_and_saveexec_b64 s[8:9], vcc
	s_cbranch_execnz .LBB0_1147

.LBB0_1145:
	s_waitcnt vmcnt(0)
	v_lshlrev_b32_e32 v50, 16, v86
	v_and_b32_e32 v51, 0xffff0000, v86
	v_lshlrev_b32_e32 v52, 16, v87
	v_and_b32_e32 v53, 0xffff0000, v87
	v_pk_add_f32 v[48:49], v[48:49], v[52:53]
	v_pk_add_f32 v[46:47], v[46:47], v[50:51]
	v_lshlrev_b32_e32 v50, 16, v88
	v_and_b32_e32 v51, 0xffff0000, v88
	v_lshlrev_b32_e32 v52, 16, v89
	v_and_b32_e32 v53, 0xffff0000, v89
	v_pk_add_f32 v[52:53], v[44:45], v[52:53]
	v_pk_add_f32 v[44:45], v[42:43], v[50:51]
	v_cvt_pk_bf16_f32 v42, v46, v47
	v_lshl_add_u64 v[46:47], s[2:3], 0, v[94:95]
	v_cvt_pk_bf16_f32 v43, v48, v49
	v_cvt_pk_bf16_f32 v44, v44, v45
	v_cvt_pk_bf16_f32 v45, v52, v53
	v_lshl_add_u64 v[46:47], v[166:167], 1, v[46:47]
	global_store_dwordx4 v[46:47], v[42:45], off
	s_nop 1
	v_lshlrev_b32_e32 v42, 16, v82
	v_and_b32_e32 v43, 0xffff0000, v82
	v_lshlrev_b32_e32 v44, 16, v83
	v_and_b32_e32 v45, 0xffff0000, v83
	v_pk_add_f32 v[40:41], v[40:41], v[44:45]
	v_pk_add_f32 v[38:39], v[38:39], v[42:43]
	v_lshlrev_b32_e32 v42, 16, v84
	v_and_b32_e32 v43, 0xffff0000, v84
	v_lshlrev_b32_e32 v44, 16, v85
	v_and_b32_e32 v45, 0xffff0000, v85
	v_pk_add_f32 v[44:45], v[36:37], v[44:45]
	v_pk_add_f32 v[36:37], v[34:35], v[42:43]
	v_cvt_pk_bf16_f32 v34, v38, v39
	v_cvt_pk_bf16_f32 v35, v40, v41
	s_nop 0
	v_cvt_pk_bf16_f32 v36, v36, v37
	v_cvt_pk_bf16_f32 v37, v44, v45
	global_store_dwordx4 v[46:47], v[34:37], off offset:256
	s_or_b64 exec, exec, s[12:13]
	s_and_saveexec_b64 s[10:11], s[8:9]
	s_cbranch_execnz .LBB0_1142

.LBB0_1147:
	s_waitcnt vmcnt(0)
	v_lshlrev_b32_e32 v18, 16, v62
	v_and_b32_e32 v19, 0xffff0000, v62
	v_lshlrev_b32_e32 v20, 16, v63
	v_and_b32_e32 v21, 0xffff0000, v63
	v_pk_add_f32 v[16:17], v[16:17], v[20:21]
	v_pk_add_f32 v[14:15], v[14:15], v[18:19]
	v_lshlrev_b32_e32 v18, 16, v64
	v_and_b32_e32 v19, 0xffff0000, v64
	v_lshlrev_b32_e32 v20, 16, v65
	v_and_b32_e32 v21, 0xffff0000, v65
	v_pk_add_f32 v[20:21], v[12:13], v[20:21]
	v_pk_add_f32 v[12:13], v[10:11], v[18:19]
	v_cvt_pk_bf16_f32 v10, v14, v15
	v_lshl_add_u64 v[14:15], s[2:3], 0, v[90:91]
	v_cvt_pk_bf16_f32 v11, v16, v17
	v_cvt_pk_bf16_f32 v12, v12, v13
	v_cvt_pk_bf16_f32 v13, v20, v21
	v_lshl_add_u64 v[14:15], v[166:167], 1, v[14:15]
	global_store_dwordx4 v[14:15], v[10:13], off
	s_nop 1
	v_lshlrev_b32_e32 v10, 16, v58
	v_and_b32_e32 v11, 0xffff0000, v58
	v_lshlrev_b32_e32 v12, 16, v59
	v_and_b32_e32 v13, 0xffff0000, v59
	v_pk_add_f32 v[8:9], v[8:9], v[12:13]
	v_pk_add_f32 v[6:7], v[6:7], v[10:11]
	v_lshlrev_b32_e32 v10, 16, v60
	v_and_b32_e32 v11, 0xffff0000, v60
	v_lshlrev_b32_e32 v12, 16, v61
	v_and_b32_e32 v13, 0xffff0000, v61
	v_pk_add_f32 v[12:13], v[4:5], v[12:13]
	v_pk_add_f32 v[4:5], v[2:3], v[10:11]
	v_cvt_pk_bf16_f32 v2, v6, v7
	v_cvt_pk_bf16_f32 v3, v8, v9
	s_nop 0
	v_cvt_pk_bf16_f32 v4, v4, v5
	v_cvt_pk_bf16_f32 v5, v12, v13
	global_store_dwordx4 v[14:15], v[2:5], off offset:256
	s_or_b64 exec, exec, s[8:9]
	s_and_b64 vcc, exec, s[6:7]
	s_mov_b64 s[6:7], -1
	s_cbranch_vccnz .LBB0_1074

.LBB0_1168:
	s_mov_b64 s[8:9], exec
	s_lshl_b32 s6, s76, 8
	v_mbcnt_lo_u32_b32 v2, s8, 0
	s_add_u32 s6, s84, s6
	v_mbcnt_hi_u32_b32 v2, s9, v2
	s_addc_u32 s7, s85, 0
	v_cmp_eq_u32_e32 vcc, 0, v2
	s_and_saveexec_b64 s[10:11], vcc
	s_cbranch_execz .LBB0_1170
	s_bcnt1_i32_b64 s8, s[8:9]
	v_mov_b32_e32 v4, 0x1000
	v_mov_b32_e32 v5, s8
	global_atomic_add v4, v4, v5, s[6:7] offset:1024 sc0
	buffer_inv sc1

.LBB0_1208:
	s_ashr_i32 s4, s93, 2
	s_bfe_i32 s5, s93, 0x10001
	s_add_i32 s4, s4, 16
	s_and_b32 s5, s5, 0x2040
	s_ashr_i32 s6, s4, 31
	s_add_u32 s4, s5, s4
	s_addc_u32 s5, 0, s6
	s_add_i32 s93, s93, s94
	s_lshl_b64 s[4:5], s[4:5], 11
	v_lshl_add_u64 v[8:9], v[2:3], 0, s[4:5]
	s_cmpk_gt_i32 s93, 0xbf
	global_store_dwordx4 v[8:9], v[4:7], off
	global_store_dwordx4 v[8:9], v[4:7], off offset:16
	s_cbranch_scc0 .LBB0_1208

.LBB0_1237:
	s_mov_b64 s[8:9], exec
	s_lshl_b32 s6, s76, 8
	v_mbcnt_lo_u32_b32 v2, s8, 0
	s_add_u32 s6, s84, s6
	v_mbcnt_hi_u32_b32 v2, s9, v2
	s_addc_u32 s7, s85, 0
	v_cmp_eq_u32_e32 vcc, 0, v2
	s_and_saveexec_b64 s[12:13], vcc
	s_cbranch_execz .LBB0_1239
	s_bcnt1_i32_b64 s8, s[8:9]
	v_mov_b32_e32 v4, 0x1000
	v_mov_b32_e32 v5, s8
	global_atomic_add v4, v4, v5, s[6:7] offset:1024 sc0
	buffer_inv sc1

.LBB0_1270:
	s_or_b64 exec, exec, s[8:9]
	s_mov_b64 s[8:9], exec
	v_mbcnt_lo_u32_b32 v1, s8, 0
	v_mbcnt_hi_u32_b32 v1, s9, v1
	v_cmp_eq_u32_e32 vcc, 0, v1
	s_waitcnt vmcnt(0)
	s_and_saveexec_b64 s[12:13], vcc
	s_cbranch_execz .LBB0_1272
	s_bcnt1_i32_b64 s8, s[8:9]
	v_mov_b32_e32 v1, 0x2000
	v_mov_b32_e32 v2, s8
	global_atomic_add v1, v2, s[6:7] offset:1024

.LBB0_1435:
	v_pk_mul_f32 v[4:5], v[4:5], v[68:69] op_sel_hi:[1,0]
	v_pk_mul_f32 v[2:3], v[2:3], v[68:69] op_sel_hi:[1,0]
	v_add_u32_e32 v68, 0x8000, v67
	ds_write2_b32 v68, v2, v3 offset1:1
	v_add_u32_e32 v2, 0x8008, v67
	ds_write2_b32 v2, v4, v5 offset1:1
	v_pk_mul_f32 v[4:5], v[6:7], v[66:67] op_sel_hi:[1,0]
	v_add_u32_e32 v6, 0x8000, v69
	v_pk_mul_f32 v[2:3], v[8:9], v[66:67] op_sel_hi:[1,0]
	ds_write2_b32 v6, v4, v5 offset1:1
	v_add_u32_e32 v4, 0x8008, v69
	ds_write2_b32 v4, v2, v3 offset1:1
	s_waitcnt vmcnt(0)
	v_pk_mul_f32 v[4:5], v[10:11], v[72:73] op_sel_hi:[1,0]
	v_add_u32_e32 v6, 0x8420, v69
	v_pk_mul_f32 v[2:3], v[12:13], v[72:73] op_sel_hi:[1,0]
	ds_write2_b32 v6, v4, v5 offset1:1
	v_add_u32_e32 v4, 0x8428, v69
	ds_write2_b32 v4, v2, v3 offset1:1
	v_pk_mul_f32 v[4:5], v[14:15], v[70:71] op_sel_hi:[1,0]
	v_add_u32_e32 v6, 0x8840, v69
	v_pk_mul_f32 v[2:3], v[16:17], v[70:71] op_sel_hi:[1,0]
	ds_write2_b32 v6, v4, v5 offset1:1
	v_add_u32_e32 v4, 0x8848, v69
	ds_write2_b32 v4, v2, v3 offset1:1
	v_pk_mul_f32 v[4:5], v[18:19], v[76:77] op_sel_hi:[1,0]
	v_add_u32_e32 v6, 0x8c60, v69
	v_pk_mul_f32 v[2:3], v[20:21], v[76:77] op_sel_hi:[1,0]
	ds_write2_b32 v6, v4, v5 offset1:1
	v_add_u32_e32 v4, 0x8c68, v69
	ds_write2_b32 v4, v2, v3 offset1:1
	v_pk_mul_f32 v[4:5], v[22:23], v[74:75] op_sel_hi:[1,0]
	v_add_u32_e32 v6, 0x9080, v69
	v_pk_mul_f32 v[2:3], v[24:25], v[74:75] op_sel_hi:[1,0]
	ds_write2_b32 v6, v4, v5 offset1:1
	v_add_u32_e32 v4, 0x9088, v69
	ds_write2_b32 v4, v2, v3 offset1:1
	v_pk_mul_f32 v[4:5], v[26:27], v[86:87] op_sel_hi:[1,0]
	v_add_u32_e32 v6, 0x94a0, v69
	v_pk_mul_f32 v[2:3], v[28:29], v[86:87] op_sel_hi:[1,0]
	ds_write2_b32 v6, v4, v5 offset1:1
	v_add_u32_e32 v4, 0x94a8, v69
	ds_write2_b32 v4, v2, v3 offset1:1
	v_pk_mul_f32 v[4:5], v[30:31], v[78:79] op_sel_hi:[1,0]
	v_add_u32_e32 v6, 0x98c0, v69
	v_pk_mul_f32 v[2:3], v[32:33], v[78:79] op_sel_hi:[1,0]
	ds_write2_b32 v6, v4, v5 offset1:1
	v_add_u32_e32 v4, 0x98c8, v69
	ds_write2_b32 v4, v2, v3 offset1:1
	s_waitcnt lgkmcnt(0)
	v_add_u32_e32 v10, 0x8000, v1
	ds_read2_b32 v[2:3], v10 offset1:33
	ds_read2_b32 v[4:5], v10 offset0:66 offset1:99
	ds_read2_b32 v[8:9], v10 offset0:132 offset1:165
	ds_read2_b32 v[12:13], v10 offset0:198 offset1:231
	v_mov_b32_e32 v95, v81
	v_lshl_add_u64 v[6:7], s[10:11], 0, v[94:95]
	s_cmp_lg_u32 s8, 0
	s_waitcnt lgkmcnt(0)
	v_cvt_pk_bf16_f32 v2, v2, v3
	v_cvt_pk_bf16_f32 v3, v4, v5
	v_cvt_pk_bf16_f32 v4, v8, v9
	v_mad_u64_u32 v[8:9], s[4:5], s35, v82, 0
	s_cselect_b64 s[10:11], -1, 0
	s_cmp_eq_u32 s8, 0
	s_mov_b32 s9, s7
	v_cvt_pk_bf16_f32 v5, v12, v13
	v_lshl_add_u64 v[8:9], v[8:9], 1, v[6:7]
	global_store_dwordx4 v[8:9], v[2:5], off
	s_cbranch_scc1 .LBB0_1437
	v_lshl_add_u64 v[8:9], s[8:9], 1, v[8:9]
	global_store_dwordx4 v[8:9], v[2:5], off
.LBB0_1437:
	ds_read2_b32 v[2:3], v10 offset0:8 offset1:41
	ds_read2_b32 v[4:5], v10 offset0:74 offset1:107
	ds_read2_b32 v[8:9], v10 offset0:140 offset1:173
	ds_read2_b32 v[12:13], v10 offset0:206 offset1:239
	v_cndmask_b32_e64 v11, 0, 1, s[10:11]
	s_waitcnt lgkmcnt(3)
	v_cvt_pk_bf16_f32 v2, v2, v3
	s_waitcnt lgkmcnt(2)
	v_cvt_pk_bf16_f32 v3, v4, v5
	s_waitcnt lgkmcnt(1)
	v_cvt_pk_bf16_f32 v4, v8, v9
	v_mad_u64_u32 v[8:9], s[4:5], s35, v84, 0
	s_waitcnt lgkmcnt(0)
	v_cvt_pk_bf16_f32 v5, v12, v13
	v_lshl_add_u64 v[8:9], v[8:9], 1, v[6:7]
	v_cmp_ne_u32_e64 s[4:5], 1, v11
	s_andn2_b64 vcc, exec, s[10:11]
	global_store_dwordx4 v[8:9], v[2:5], off
	s_cbranch_vccnz .LBB0_1439
	v_lshl_add_u64 v[8:9], s[8:9], 1, v[8:9]
	global_store_dwordx4 v[8:9], v[2:5], off
.LBB0_1439:
	ds_read2_b32 v[2:3], v10 offset0:16 offset1:49
	ds_read2_b32 v[4:5], v10 offset0:82 offset1:115
	ds_read2_b32 v[8:9], v10 offset0:148 offset1:181
	ds_read2_b32 v[12:13], v10 offset0:214 offset1:247
	s_and_b64 vcc, exec, s[4:5]
	s_waitcnt lgkmcnt(3)
	v_cvt_pk_bf16_f32 v2, v2, v3
	s_waitcnt lgkmcnt(2)
	v_cvt_pk_bf16_f32 v3, v4, v5
	s_waitcnt lgkmcnt(1)
	v_cvt_pk_bf16_f32 v4, v8, v9
	v_mad_u64_u32 v[8:9], s[10:11], s35, v88, 0
	s_waitcnt lgkmcnt(0)
	v_cvt_pk_bf16_f32 v5, v12, v13
	v_lshl_add_u64 v[8:9], v[8:9], 1, v[6:7]
	global_store_dwordx4 v[8:9], v[2:5], off
	s_cbranch_vccnz .LBB0_1441
	v_lshl_add_u64 v[8:9], s[8:9], 1, v[8:9]
	global_store_dwordx4 v[8:9], v[2:5], off
.LBB0_1441:
	ds_read2_b32 v[2:3], v10 offset0:24 offset1:57
	ds_read2_b32 v[4:5], v10 offset0:90 offset1:123
	ds_read2_b32 v[8:9], v10 offset0:156 offset1:189
	ds_read2_b32 v[10:11], v10 offset0:222 offset1:255
	s_and_b64 vcc, exec, s[4:5]
	s_waitcnt lgkmcnt(3)
	v_cvt_pk_bf16_f32 v2, v2, v3
	s_waitcnt lgkmcnt(2)
	v_cvt_pk_bf16_f32 v3, v4, v5
	s_waitcnt lgkmcnt(1)
	v_cvt_pk_bf16_f32 v4, v8, v9
	v_mad_u64_u32 v[8:9], s[10:11], s35, v90, 0
	s_waitcnt lgkmcnt(0)
	v_cvt_pk_bf16_f32 v5, v10, v11
	v_lshl_add_u64 v[6:7], v[8:9], 1, v[6:7]
	global_store_dwordx4 v[6:7], v[2:5], off
	s_cbranch_vccnz .LBB0_1406
	v_lshl_add_u64 v[6:7], s[8:9], 1, v[6:7]
	global_store_dwordx4 v[6:7], v[2:5], off
	s_branch .LBB0_1406

.LBB0_1492:
	s_and_b64 s[34:35], s[36:37], exec
	s_cselect_b32 s19, s27, s59
	s_cselect_b32 s21, s26, s58
	s_lshl_b32 s8, s8, 8
	v_mov_b32_e32 v175, s19
	s_add_i32 s19, s8, 0xfffffc00
	s_and_b64 s[34:35], s[36:37], exec
	s_cselect_b32 s8, s8, s19
	v_or_b32_e32 v190, s8, v213
	s_ashr_i32 s8, s9, 13
	s_mul_hi_i32 s9, s8, 0x2040
	s_mulk_i32 s8, 0x2040
	v_mov_b32_e32 v174, s21
	v_ashrrev_i32_e32 v191, 31, v190
	s_add_u32 s34, s8, 64
	v_lshl_add_u64 v[174:175], v[190:191], 1, v[174:175]
	s_addc_u32 s35, s9, 0
	v_cmp_gt_i32_e32 vcc, s57, v172
	s_and_saveexec_b64 s[36:37], vcc
	s_cbranch_execz .LBB0_1501
	v_cmp_lt_i32_e32 vcc, s60, v172
	v_cmp_gt_i32_e64 s[8:9], s46, v172
	s_and_saveexec_b64 s[38:39], s[8:9]
	s_xor_b64 s[8:9], exec, s[38:39]
	v_and_b32_e32 v156, 0x1fcf, v172
	v_lshl_add_u64 v[202:203], s[34:35], 0, v[156:157]
	s_or_saveexec_b64 s[8:9], s[8:9]
	v_mov_b64_e32 v[206:207], v[202:203]
	s_xor_b64 exec, exec, s[8:9]
	v_add_u32_e32 v156, 0xffffc000, v172
	v_add_u32_e32 v206, 0xffffe040, v172
	v_mov_b32_e32 v207, v157
	v_mov_b64_e32 v[202:203], v[156:157]
	s_or_b64 exec, exec, s[8:9]
	v_lshlrev_b64 v[190:191], 11, v[202:203]
	v_lshl_add_u64 v[204:205], v[174:175], 0, v[190:191]
	v_lshlrev_b64 v[190:191], 11, v[206:207]
	s_waitcnt vmcnt(0)
	v_pk_mul_f32 v[140:141], v[140:141], v[200:201] op_sel_hi:[1,0]
	v_pk_mul_f32 v[138:139], v[138:139], v[200:201] op_sel_hi:[1,0]
	v_lshl_add_u64 v[202:203], v[174:175], 0, v[190:191]
	v_pk_mul_f32 v[144:145], v[144:145], v[200:201] op_sel_hi:[1,0]
	v_pk_mul_f32 v[142:143], v[142:143], v[200:201] op_sel_hi:[1,0]
	v_pk_mul_f32 v[190:191], v[68:69], v[140:141]
	v_pk_mul_f32 v[140:141], v[66:67], v[138:139]
	v_pk_mul_f32 v[144:145], v[76:77], v[144:145]
	v_pk_mul_f32 v[142:143], v[74:75], v[142:143]
	s_nop 0
	v_cvt_pk_bf16_f32 v138, v142, v143
	v_cvt_pk_bf16_f32 v139, v144, v145
	v_cvt_pk_bf16_f32 v140, v140, v141
	v_cvt_pk_bf16_f32 v141, v190, v191
	global_store_dwordx4 v[204:205], v[138:141], off
	s_and_saveexec_b64 s[8:9], vcc
	s_cbranch_execz .LBB0_1499
	global_store_dwordx4 v[202:203], v[138:141], off
.LBB0_1499:
	s_or_b64 exec, exec, s[8:9]
	v_mov_b32_e32 v201, v200
	v_mov_b32_e32 v138, v200
	v_mov_b32_e32 v139, v200
	v_pk_mul_f32 v[132:133], v[132:133], v[138:139]
	v_pk_mul_f32 v[130:131], v[130:131], v[200:201]
	v_pk_mul_f32 v[136:137], v[136:137], v[138:139]
	v_pk_mul_f32 v[134:135], v[134:135], v[200:201]
	v_pk_mul_f32 v[138:139], v[72:73], v[132:133]
	v_pk_mul_f32 v[132:133], v[70:71], v[130:131]
	v_pk_mul_f32 v[136:137], v[80:81], v[136:137]
	v_pk_mul_f32 v[134:135], v[78:79], v[134:135]
	s_nop 0
	v_cvt_pk_bf16_f32 v130, v134, v135
	v_cvt_pk_bf16_f32 v131, v136, v137
	v_cvt_pk_bf16_f32 v132, v132, v133
	v_cvt_pk_bf16_f32 v133, v138, v139
	global_store_dwordx4 v[204:205], v[130:133], off offset:64
	s_and_b64 exec, exec, vcc
	s_cbranch_execz .LBB0_1501
	global_store_dwordx4 v[202:203], v[130:133], off offset:64

.LBB0_1503:
	v_cmp_gt_i32_e32 vcc, s57, v198
	s_and_saveexec_b64 s[36:37], vcc
	s_cbranch_execz .LBB0_1512
	v_cmp_lt_i32_e32 vcc, s60, v198
	v_cmp_gt_i32_e64 s[8:9], s46, v198
	s_and_saveexec_b64 s[38:39], s[8:9]
	s_xor_b64 s[8:9], exec, s[38:39]
	v_and_b32_e32 v156, 0x1fdf, v198
	v_lshl_add_u64 v[130:131], s[34:35], 0, v[156:157]
	s_or_saveexec_b64 s[8:9], s[8:9]
	v_mov_b64_e32 v[134:135], v[130:131]
	s_xor_b64 exec, exec, s[8:9]
	v_add_u32_e32 v156, 0xffffc010, v172
	v_add_u32_e32 v134, 0xffffe050, v172
	v_mov_b32_e32 v135, v157
	v_mov_b64_e32 v[130:131], v[156:157]
	s_or_b64 exec, exec, s[8:9]
	v_lshlrev_b64 v[130:131], 11, v[130:131]
	v_lshl_add_u64 v[132:133], v[174:175], 0, v[130:131]
	v_lshlrev_b64 v[130:131], 11, v[134:135]
	s_waitcnt vmcnt(0)
	v_pk_mul_f32 v[124:125], v[124:125], v[196:197] op_sel_hi:[1,0]
	v_pk_mul_f32 v[122:123], v[122:123], v[196:197] op_sel_hi:[1,0]
	v_lshl_add_u64 v[130:131], v[174:175], 0, v[130:131]
	v_pk_mul_f32 v[128:129], v[128:129], v[196:197] op_sel_hi:[1,0]
	v_pk_mul_f32 v[126:127], v[126:127], v[196:197] op_sel_hi:[1,0]
	v_pk_mul_f32 v[134:135], v[68:69], v[124:125]
	v_pk_mul_f32 v[124:125], v[66:67], v[122:123]
	v_pk_mul_f32 v[128:129], v[76:77], v[128:129]
	v_pk_mul_f32 v[126:127], v[74:75], v[126:127]
	s_nop 0
	v_cvt_pk_bf16_f32 v122, v126, v127
	v_cvt_pk_bf16_f32 v123, v128, v129
	v_cvt_pk_bf16_f32 v124, v124, v125
	v_cvt_pk_bf16_f32 v125, v134, v135
	global_store_dwordx4 v[132:133], v[122:125], off
	s_and_saveexec_b64 s[8:9], vcc
	s_cbranch_execz .LBB0_1510
	global_store_dwordx4 v[130:131], v[122:125], off
.LBB0_1510:
	s_or_b64 exec, exec, s[8:9]
	v_mov_b32_e32 v197, v196
	v_mov_b32_e32 v122, v196
	v_mov_b32_e32 v123, v196
	v_pk_mul_f32 v[116:117], v[116:117], v[122:123]
	v_pk_mul_f32 v[114:115], v[114:115], v[196:197]
	v_pk_mul_f32 v[120:121], v[120:121], v[122:123]
	v_pk_mul_f32 v[118:119], v[118:119], v[196:197]
	v_pk_mul_f32 v[122:123], v[72:73], v[116:117]
	v_pk_mul_f32 v[116:117], v[70:71], v[114:115]
	v_pk_mul_f32 v[120:121], v[80:81], v[120:121]
	v_pk_mul_f32 v[118:119], v[78:79], v[118:119]
	s_nop 0
	v_cvt_pk_bf16_f32 v114, v118, v119
	v_cvt_pk_bf16_f32 v115, v120, v121
	v_cvt_pk_bf16_f32 v116, v116, v117
	v_cvt_pk_bf16_f32 v117, v122, v123
	global_store_dwordx4 v[132:133], v[114:117], off offset:64
	s_and_b64 exec, exec, vcc
	s_cbranch_execz .LBB0_1512
	global_store_dwordx4 v[130:131], v[114:117], off offset:64

.LBB0_1514:
	v_cmp_gt_i32_e32 vcc, s57, v188
	s_and_saveexec_b64 s[36:37], vcc
	s_cbranch_execz .LBB0_1523
	v_cmp_lt_i32_e32 vcc, s60, v188
	v_cmp_gt_i32_e64 s[8:9], s46, v188
	s_and_saveexec_b64 s[38:39], s[8:9]
	s_xor_b64 s[8:9], exec, s[38:39]
	v_and_b32_e32 v156, 0x1fef, v188
	v_lshl_add_u64 v[114:115], s[34:35], 0, v[156:157]
	s_or_saveexec_b64 s[8:9], s[8:9]
	v_mov_b64_e32 v[118:119], v[114:115]
	s_xor_b64 exec, exec, s[8:9]
	v_add_u32_e32 v156, 0xffffc020, v172
	v_add_u32_e32 v118, 0xffffe060, v172
	v_mov_b32_e32 v119, v157
	v_mov_b64_e32 v[114:115], v[156:157]
	s_or_b64 exec, exec, s[8:9]
	v_lshlrev_b64 v[114:115], 11, v[114:115]
	v_lshl_add_u64 v[116:117], v[174:175], 0, v[114:115]
	v_lshlrev_b64 v[114:115], 11, v[118:119]
	s_waitcnt vmcnt(0)
	v_pk_mul_f32 v[108:109], v[108:109], v[186:187] op_sel_hi:[1,0]
	v_pk_mul_f32 v[106:107], v[106:107], v[186:187] op_sel_hi:[1,0]
	v_lshl_add_u64 v[114:115], v[174:175], 0, v[114:115]
	v_pk_mul_f32 v[112:113], v[112:113], v[186:187] op_sel_hi:[1,0]
	v_pk_mul_f32 v[110:111], v[110:111], v[186:187] op_sel_hi:[1,0]
	v_pk_mul_f32 v[118:119], v[68:69], v[108:109]
	v_pk_mul_f32 v[108:109], v[66:67], v[106:107]
	v_pk_mul_f32 v[112:113], v[76:77], v[112:113]
	v_pk_mul_f32 v[110:111], v[74:75], v[110:111]
	s_nop 0
	v_cvt_pk_bf16_f32 v106, v110, v111
	v_cvt_pk_bf16_f32 v107, v112, v113
	v_cvt_pk_bf16_f32 v108, v108, v109
	v_cvt_pk_bf16_f32 v109, v118, v119
	global_store_dwordx4 v[116:117], v[106:109], off
	s_and_saveexec_b64 s[8:9], vcc
	s_cbranch_execz .LBB0_1521
	global_store_dwordx4 v[114:115], v[106:109], off
.LBB0_1521:
	s_or_b64 exec, exec, s[8:9]
	v_mov_b32_e32 v187, v186
	v_mov_b32_e32 v106, v186
	v_mov_b32_e32 v107, v186
	v_pk_mul_f32 v[100:101], v[100:101], v[106:107]
	v_pk_mul_f32 v[98:99], v[98:99], v[186:187]
	v_pk_mul_f32 v[104:105], v[104:105], v[106:107]
	v_pk_mul_f32 v[102:103], v[102:103], v[186:187]
	v_pk_mul_f32 v[106:107], v[72:73], v[100:101]
	v_pk_mul_f32 v[100:101], v[70:71], v[98:99]
	v_pk_mul_f32 v[104:105], v[80:81], v[104:105]
	v_pk_mul_f32 v[102:103], v[78:79], v[102:103]
	s_nop 0
	v_cvt_pk_bf16_f32 v98, v102, v103
	v_cvt_pk_bf16_f32 v99, v104, v105
	v_cvt_pk_bf16_f32 v100, v100, v101
	v_cvt_pk_bf16_f32 v101, v106, v107
	global_store_dwordx4 v[116:117], v[98:101], off offset:64
	s_and_b64 exec, exec, vcc
	s_cbranch_execz .LBB0_1523
	global_store_dwordx4 v[114:115], v[98:101], off offset:64

.LBB0_1525:
	v_cmp_gt_i32_e32 vcc, s57, v184
	s_and_saveexec_b64 s[36:37], vcc
	s_cbranch_execz .LBB0_1534
	v_cmp_lt_i32_e32 vcc, s60, v184
	v_cmp_gt_i32_e64 s[8:9], s46, v184
	s_and_saveexec_b64 s[38:39], s[8:9]
	s_xor_b64 s[8:9], exec, s[38:39]
	v_and_b32_e32 v156, 0x1fff, v184
	v_lshl_add_u64 v[98:99], s[34:35], 0, v[156:157]
	s_or_saveexec_b64 s[8:9], s[8:9]
	v_mov_b64_e32 v[102:103], v[98:99]
	s_xor_b64 exec, exec, s[8:9]
	v_add_u32_e32 v156, 0xffffc030, v172
	v_add_u32_e32 v102, 0xffffe070, v172
	v_mov_b32_e32 v103, v157
	v_mov_b64_e32 v[98:99], v[156:157]
	s_or_b64 exec, exec, s[8:9]
	v_lshlrev_b64 v[98:99], 11, v[98:99]
	v_lshl_add_u64 v[100:101], v[174:175], 0, v[98:99]
	v_lshlrev_b64 v[98:99], 11, v[102:103]
	s_waitcnt vmcnt(0)
	v_pk_mul_f32 v[92:93], v[92:93], v[182:183] op_sel_hi:[1,0]
	v_pk_mul_f32 v[90:91], v[90:91], v[182:183] op_sel_hi:[1,0]
	v_lshl_add_u64 v[98:99], v[174:175], 0, v[98:99]
	v_pk_mul_f32 v[96:97], v[96:97], v[182:183] op_sel_hi:[1,0]
	v_pk_mul_f32 v[94:95], v[94:95], v[182:183] op_sel_hi:[1,0]
	v_pk_mul_f32 v[102:103], v[68:69], v[92:93]
	v_pk_mul_f32 v[92:93], v[66:67], v[90:91]
	v_pk_mul_f32 v[96:97], v[76:77], v[96:97]
	v_pk_mul_f32 v[94:95], v[74:75], v[94:95]
	s_nop 0
	v_cvt_pk_bf16_f32 v90, v94, v95
	v_cvt_pk_bf16_f32 v91, v96, v97
	v_cvt_pk_bf16_f32 v92, v92, v93
	v_cvt_pk_bf16_f32 v93, v102, v103
	global_store_dwordx4 v[100:101], v[90:93], off
	s_and_saveexec_b64 s[8:9], vcc
	s_cbranch_execz .LBB0_1532
	global_store_dwordx4 v[98:99], v[90:93], off
.LBB0_1532:
	s_or_b64 exec, exec, s[8:9]
	v_mov_b32_e32 v183, v182
	v_mov_b32_e32 v90, v182
	v_mov_b32_e32 v91, v182
	v_pk_mul_f32 v[84:85], v[84:85], v[90:91]
	v_pk_mul_f32 v[82:83], v[82:83], v[182:183]
	v_pk_mul_f32 v[88:89], v[88:89], v[90:91]
	v_pk_mul_f32 v[86:87], v[86:87], v[182:183]
	v_pk_mul_f32 v[90:91], v[72:73], v[84:85]
	v_pk_mul_f32 v[84:85], v[70:71], v[82:83]
	v_pk_mul_f32 v[88:89], v[80:81], v[88:89]
	v_pk_mul_f32 v[86:87], v[78:79], v[86:87]
	s_nop 0
	v_cvt_pk_bf16_f32 v82, v86, v87
	v_cvt_pk_bf16_f32 v83, v88, v89
	v_cvt_pk_bf16_f32 v84, v84, v85
	v_cvt_pk_bf16_f32 v85, v90, v91
	global_store_dwordx4 v[100:101], v[82:85], off offset:64
	s_and_b64 exec, exec, vcc
	s_cbranch_execz .LBB0_1534
	global_store_dwordx4 v[98:99], v[82:85], off offset:64

.LBB0_1536:
	v_add_u32_e32 v86, 0x80, v172
	v_ashrrev_i32_e32 v82, 13, v86
	v_mul_hi_i32_i24_e32 v83, 0x2040, v82
	v_mul_i32_i24_e32 v82, 0x2040, v82
	s_movk_i32 s8, 0x3f90
	v_lshl_add_u64 v[82:83], v[82:83], 0, 64
	v_cmp_gt_i32_e32 vcc, s8, v172
	s_and_saveexec_b64 s[34:35], vcc
	s_cbranch_execz .LBB0_1545
	s_movk_i32 s8, 0x3f7f
	v_cmp_lt_i32_e32 vcc, s8, v172
	v_cmp_gt_i32_e64 s[8:9], s61, v172
	s_and_saveexec_b64 s[36:37], s[8:9]
	s_xor_b64 s[8:9], exec, s[36:37]
	v_and_b32_e32 v156, 0x1fcf, v86
	v_lshl_add_u64 v[84:85], v[82:83], 0, v[156:157]
	s_or_saveexec_b64 s[8:9], s[8:9]
	v_mov_b64_e32 v[88:89], v[84:85]
	s_xor_b64 exec, exec, s[8:9]
	v_add_u32_e32 v156, 0xffffc080, v172
	v_add_u32_e32 v88, 0xffffe0c0, v172
	v_mov_b32_e32 v89, v157
	v_mov_b64_e32 v[84:85], v[156:157]
	s_or_b64 exec, exec, s[8:9]
	v_lshlrev_b64 v[84:85], 11, v[84:85]
	v_lshl_add_u64 v[86:87], v[174:175], 0, v[84:85]
	v_lshlrev_b64 v[84:85], 11, v[88:89]
	s_waitcnt vmcnt(0)
	v_pk_mul_f32 v[60:61], v[60:61], v[180:181] op_sel_hi:[1,0]
	v_pk_mul_f32 v[58:59], v[58:59], v[180:181] op_sel_hi:[1,0]
	v_lshl_add_u64 v[84:85], v[174:175], 0, v[84:85]
	v_pk_mul_f32 v[64:65], v[64:65], v[180:181] op_sel_hi:[1,0]
	v_pk_mul_f32 v[62:63], v[62:63], v[180:181] op_sel_hi:[1,0]
	v_pk_mul_f32 v[88:89], v[68:69], v[60:61]
	v_pk_mul_f32 v[60:61], v[66:67], v[58:59]
	v_pk_mul_f32 v[64:65], v[76:77], v[64:65]
	v_pk_mul_f32 v[62:63], v[74:75], v[62:63]
	s_nop 0
	v_cvt_pk_bf16_f32 v58, v62, v63
	v_cvt_pk_bf16_f32 v59, v64, v65
	v_cvt_pk_bf16_f32 v60, v60, v61
	v_cvt_pk_bf16_f32 v61, v88, v89
	global_store_dwordx4 v[86:87], v[58:61], off
	s_and_saveexec_b64 s[8:9], vcc
	s_cbranch_execz .LBB0_1543
	global_store_dwordx4 v[84:85], v[58:61], off
.LBB0_1543:
	s_or_b64 exec, exec, s[8:9]
	v_mov_b32_e32 v181, v180
	v_mov_b32_e32 v58, v180
	v_mov_b32_e32 v59, v180
	v_pk_mul_f32 v[52:53], v[52:53], v[58:59]
	v_pk_mul_f32 v[50:51], v[50:51], v[180:181]
	v_pk_mul_f32 v[56:57], v[56:57], v[58:59]
	v_pk_mul_f32 v[54:55], v[54:55], v[180:181]
	v_pk_mul_f32 v[58:59], v[72:73], v[52:53]
	v_pk_mul_f32 v[52:53], v[70:71], v[50:51]
	v_pk_mul_f32 v[56:57], v[80:81], v[56:57]
	v_pk_mul_f32 v[54:55], v[78:79], v[54:55]
	s_nop 0
	v_cvt_pk_bf16_f32 v50, v54, v55
	v_cvt_pk_bf16_f32 v51, v56, v57
	v_cvt_pk_bf16_f32 v52, v52, v53
	v_cvt_pk_bf16_f32 v53, v58, v59
	global_store_dwordx4 v[86:87], v[50:53], off offset:64
	s_and_b64 exec, exec, vcc
	s_cbranch_execz .LBB0_1545
	global_store_dwordx4 v[84:85], v[50:53], off offset:64

.LBB0_1547:
	v_cmp_gt_i32_e32 vcc, s61, v172
	s_and_saveexec_b64 s[34:35], vcc
	s_cbranch_execz .LBB0_1556
	s_movk_i32 s8, 0x3f6f
	v_cmp_lt_i32_e32 vcc, s8, v172
	v_cmp_gt_i32_e64 s[8:9], s62, v172
	s_and_saveexec_b64 s[36:37], s[8:9]
	s_xor_b64 s[8:9], exec, s[36:37]
	v_add_u32_e32 v50, 0x90, v172
	v_and_b32_e32 v156, 0x1fdf, v50
	v_lshl_add_u64 v[50:51], v[82:83], 0, v[156:157]
	s_or_saveexec_b64 s[8:9], s[8:9]
	v_mov_b64_e32 v[54:55], v[50:51]
	s_xor_b64 exec, exec, s[8:9]
	v_add_u32_e32 v156, 0xffffc090, v172
	v_add_u32_e32 v54, 0xffffe0d0, v172
	v_mov_b32_e32 v55, v157
	v_mov_b64_e32 v[50:51], v[156:157]
	s_or_b64 exec, exec, s[8:9]
	v_lshlrev_b64 v[50:51], 11, v[50:51]
	v_lshl_add_u64 v[52:53], v[174:175], 0, v[50:51]
	v_lshlrev_b64 v[50:51], 11, v[54:55]
	s_waitcnt vmcnt(0)
	v_pk_mul_f32 v[44:45], v[44:45], v[178:179] op_sel_hi:[1,0]
	v_pk_mul_f32 v[42:43], v[42:43], v[178:179] op_sel_hi:[1,0]
	v_lshl_add_u64 v[50:51], v[174:175], 0, v[50:51]
	v_pk_mul_f32 v[48:49], v[48:49], v[178:179] op_sel_hi:[1,0]
	v_pk_mul_f32 v[46:47], v[46:47], v[178:179] op_sel_hi:[1,0]
	v_pk_mul_f32 v[54:55], v[68:69], v[44:45]
	v_pk_mul_f32 v[44:45], v[66:67], v[42:43]
	v_pk_mul_f32 v[48:49], v[76:77], v[48:49]
	v_pk_mul_f32 v[46:47], v[74:75], v[46:47]
	s_nop 0
	v_cvt_pk_bf16_f32 v42, v46, v47
	v_cvt_pk_bf16_f32 v43, v48, v49
	v_cvt_pk_bf16_f32 v44, v44, v45
	v_cvt_pk_bf16_f32 v45, v54, v55
	global_store_dwordx4 v[52:53], v[42:45], off
	s_and_saveexec_b64 s[8:9], vcc
	s_cbranch_execz .LBB0_1554
	global_store_dwordx4 v[50:51], v[42:45], off
.LBB0_1554:
	s_or_b64 exec, exec, s[8:9]
	v_mov_b32_e32 v179, v178
	v_mov_b32_e32 v42, v178
	v_mov_b32_e32 v43, v178
	v_pk_mul_f32 v[36:37], v[36:37], v[42:43]
	v_pk_mul_f32 v[34:35], v[34:35], v[178:179]
	v_pk_mul_f32 v[40:41], v[40:41], v[42:43]
	v_pk_mul_f32 v[38:39], v[38:39], v[178:179]
	v_pk_mul_f32 v[42:43], v[72:73], v[36:37]
	v_pk_mul_f32 v[36:37], v[70:71], v[34:35]
	v_pk_mul_f32 v[40:41], v[80:81], v[40:41]
	v_pk_mul_f32 v[38:39], v[78:79], v[38:39]
	s_nop 0
	v_cvt_pk_bf16_f32 v34, v38, v39
	v_cvt_pk_bf16_f32 v35, v40, v41
	v_cvt_pk_bf16_f32 v36, v36, v37
	v_cvt_pk_bf16_f32 v37, v42, v43
	global_store_dwordx4 v[52:53], v[34:37], off offset:64
	s_and_b64 exec, exec, vcc
	s_cbranch_execz .LBB0_1556
	global_store_dwordx4 v[50:51], v[34:37], off offset:64

.LBB0_1558:
	v_cmp_gt_i32_e32 vcc, s62, v172
	s_and_saveexec_b64 s[34:35], vcc
	s_cbranch_execz .LBB0_1567
	s_movk_i32 s8, 0x3f5f
	v_cmp_lt_i32_e32 vcc, s8, v172
	v_cmp_gt_i32_e64 s[8:9], s63, v172
	s_and_saveexec_b64 s[36:37], s[8:9]
	s_xor_b64 s[8:9], exec, s[36:37]
	v_add_u32_e32 v34, 0xa0, v172
	v_and_b32_e32 v156, 0x1fef, v34
	v_lshl_add_u64 v[34:35], v[82:83], 0, v[156:157]
	s_or_saveexec_b64 s[8:9], s[8:9]
	v_mov_b64_e32 v[38:39], v[34:35]
	s_xor_b64 exec, exec, s[8:9]
	v_add_u32_e32 v156, 0xffffc0a0, v172
	v_add_u32_e32 v38, 0xffffe0e0, v172
	v_mov_b32_e32 v39, v157
	v_mov_b64_e32 v[34:35], v[156:157]
	s_or_b64 exec, exec, s[8:9]
	v_lshlrev_b64 v[34:35], 11, v[34:35]
	v_lshl_add_u64 v[36:37], v[174:175], 0, v[34:35]
	v_lshlrev_b64 v[34:35], 11, v[38:39]
	s_waitcnt vmcnt(0)
	v_pk_mul_f32 v[28:29], v[28:29], v[176:177] op_sel_hi:[1,0]
	v_pk_mul_f32 v[26:27], v[26:27], v[176:177] op_sel_hi:[1,0]
	v_lshl_add_u64 v[34:35], v[174:175], 0, v[34:35]
	v_pk_mul_f32 v[32:33], v[32:33], v[176:177] op_sel_hi:[1,0]
	v_pk_mul_f32 v[30:31], v[30:31], v[176:177] op_sel_hi:[1,0]
	v_pk_mul_f32 v[38:39], v[68:69], v[28:29]
	v_pk_mul_f32 v[28:29], v[66:67], v[26:27]
	v_pk_mul_f32 v[32:33], v[76:77], v[32:33]
	v_pk_mul_f32 v[30:31], v[74:75], v[30:31]
	s_nop 0
	v_cvt_pk_bf16_f32 v26, v30, v31
	v_cvt_pk_bf16_f32 v27, v32, v33
	v_cvt_pk_bf16_f32 v28, v28, v29
	v_cvt_pk_bf16_f32 v29, v38, v39
	global_store_dwordx4 v[36:37], v[26:29], off
	s_and_saveexec_b64 s[8:9], vcc
	s_cbranch_execz .LBB0_1565
	global_store_dwordx4 v[34:35], v[26:29], off
.LBB0_1565:
	s_or_b64 exec, exec, s[8:9]
	v_mov_b32_e32 v177, v176
	v_mov_b32_e32 v26, v176
	v_mov_b32_e32 v27, v176
	v_pk_mul_f32 v[20:21], v[20:21], v[26:27]
	v_pk_mul_f32 v[18:19], v[18:19], v[176:177]
	v_pk_mul_f32 v[24:25], v[24:25], v[26:27]
	v_pk_mul_f32 v[22:23], v[22:23], v[176:177]
	v_pk_mul_f32 v[26:27], v[72:73], v[20:21]
	v_pk_mul_f32 v[20:21], v[70:71], v[18:19]
	v_pk_mul_f32 v[24:25], v[80:81], v[24:25]
	v_pk_mul_f32 v[22:23], v[78:79], v[22:23]
	s_nop 0
	v_cvt_pk_bf16_f32 v18, v22, v23
	v_cvt_pk_bf16_f32 v19, v24, v25
	v_cvt_pk_bf16_f32 v20, v20, v21
	v_cvt_pk_bf16_f32 v21, v26, v27
	global_store_dwordx4 v[36:37], v[18:21], off offset:64
	s_and_b64 exec, exec, vcc
	s_cbranch_execz .LBB0_1567
	global_store_dwordx4 v[34:35], v[18:21], off offset:64

.LBB0_1569:
	v_cmp_gt_i32_e32 vcc, s63, v172
	s_and_saveexec_b64 s[8:9], vcc
	s_cbranch_execz .LBB0_1578
	s_movk_i32 s6, 0x3f4f
	v_cmp_lt_i32_e32 vcc, s6, v172
	s_movk_i32 s6, 0x3f50
	v_cmp_gt_i32_e64 s[6:7], s6, v172
	s_and_saveexec_b64 s[34:35], s[6:7]
	s_xor_b64 s[6:7], exec, s[34:35]
	v_add_u32_e32 v18, 0xb0, v172
	v_and_b32_e32 v156, 0x1fff, v18
	v_lshl_add_u64 v[18:19], v[82:83], 0, v[156:157]
	s_or_saveexec_b64 s[6:7], s[6:7]
	v_mov_b64_e32 v[22:23], v[18:19]
	s_xor_b64 exec, exec, s[6:7]
	v_add_u32_e32 v156, 0xffffc0b0, v172
	v_add_u32_e32 v22, 0xffffe0f0, v172
	v_mov_b32_e32 v23, v157
	v_mov_b64_e32 v[18:19], v[156:157]
	s_or_b64 exec, exec, s[6:7]
	v_lshlrev_b64 v[18:19], 11, v[18:19]
	v_lshl_add_u64 v[20:21], v[174:175], 0, v[18:19]
	v_lshlrev_b64 v[18:19], 11, v[22:23]
	s_waitcnt vmcnt(0)
	v_pk_mul_f32 v[12:13], v[12:13], v[170:171] op_sel_hi:[1,0]
	v_pk_mul_f32 v[10:11], v[10:11], v[170:171] op_sel_hi:[1,0]
	v_lshl_add_u64 v[18:19], v[174:175], 0, v[18:19]
	v_pk_mul_f32 v[16:17], v[16:17], v[170:171] op_sel_hi:[1,0]
	v_pk_mul_f32 v[14:15], v[14:15], v[170:171] op_sel_hi:[1,0]
	v_pk_mul_f32 v[22:23], v[68:69], v[12:13]
	v_pk_mul_f32 v[12:13], v[66:67], v[10:11]
	v_pk_mul_f32 v[16:17], v[76:77], v[16:17]
	v_pk_mul_f32 v[14:15], v[74:75], v[14:15]
	s_nop 0
	v_cvt_pk_bf16_f32 v10, v14, v15
	v_cvt_pk_bf16_f32 v11, v16, v17
	v_cvt_pk_bf16_f32 v12, v12, v13
	v_cvt_pk_bf16_f32 v13, v22, v23
	global_store_dwordx4 v[20:21], v[10:13], off
	s_and_saveexec_b64 s[6:7], vcc
	s_cbranch_execz .LBB0_1576
	global_store_dwordx4 v[18:19], v[10:13], off
.LBB0_1576:
	s_or_b64 exec, exec, s[6:7]
	v_mov_b32_e32 v171, v170
	v_mov_b32_e32 v10, v170
	v_mov_b32_e32 v11, v170
	v_pk_mul_f32 v[4:5], v[4:5], v[10:11]
	v_pk_mul_f32 v[2:3], v[2:3], v[170:171]
	v_pk_mul_f32 v[8:9], v[8:9], v[10:11]
	v_pk_mul_f32 v[6:7], v[6:7], v[170:171]
	v_pk_mul_f32 v[10:11], v[72:73], v[4:5]
	v_pk_mul_f32 v[4:5], v[70:71], v[2:3]
	v_pk_mul_f32 v[8:9], v[80:81], v[8:9]
	v_pk_mul_f32 v[6:7], v[78:79], v[6:7]
	s_nop 0
	v_cvt_pk_bf16_f32 v2, v6, v7
	v_cvt_pk_bf16_f32 v3, v8, v9
	v_cvt_pk_bf16_f32 v4, v4, v5
	v_cvt_pk_bf16_f32 v5, v10, v11
	global_store_dwordx4 v[20:21], v[2:5], off offset:64
	s_and_b64 exec, exec, vcc
	s_cbranch_execz .LBB0_1578
	global_store_dwordx4 v[18:19], v[2:5], off offset:64

.LBB0_1602:
	v_lshl_add_u32 v144, s34, 8, v170
	v_ashrrev_i32_e32 v145, 31, v144
	global_load_dwordx4 v[140:143], v[130:131], off offset:16
	global_load_dwordx4 v[154:157], v[130:131], off
	v_lshl_add_u64 v[160:161], v[144:145], 2, s[0:1]
	global_load_dwordx4 v[182:185], v[130:131], off offset:128
	global_load_dword v195, v[160:161], off
	global_load_dwordx4 v[186:189], v[130:131], off offset:144
	v_pk_mul_f32 v[162:163], v[128:129], v[128:129]
	v_pk_mul_f32 v[164:165], v[126:127], v[126:127]
	v_pk_mul_f32 v[176:177], v[124:125], v[124:125]
	v_pk_mul_f32 v[178:179], v[122:123], v[122:123]
	v_pk_mov_b32 v[200:201], v[164:165], v[162:163] op_sel:[1,0]
	v_mov_b32_e32 v165, v163
	v_pk_mov_b32 v[162:163], v[178:179], v[176:177] op_sel:[1,0]
	v_mov_b32_e32 v179, v177
	v_mul_f32_e32 v180, v119, v119
	v_mul_f32_e32 v196, v121, v121
	v_pk_add_f32 v[164:165], v[200:201], v[164:165]
	v_pk_add_f32 v[162:163], v[162:163], v[178:179]
	v_and_b32_e32 v167, 64, v174
	v_mul_f32_e32 v203, v110, v110
	v_mul_f32_e32 v204, v111, v111
	v_mul_f32_e32 v205, v112, v112
	v_mul_f32_e32 v206, v113, v113
	v_or_b32_e32 v198, 16, v144
	v_or_b32_e32 v168, 32, v144
	v_or_b32_e32 v166, 48, v144
	v_pk_fma_f32 v[180:181], v[118:119], v[118:119], v[180:181] op_sel_hi:[1,1,0]
	v_pk_fma_f32 v[196:197], v[120:121], v[120:121], v[196:197] op_sel_hi:[1,1,0]
	v_lshlrev_b64 v[200:201], 11, v[144:145]
	v_pk_add_f32 v[144:145], v[164:165], v[164:165] op_sel:[0,1] op_sel_hi:[1,0]
	v_pk_add_f32 v[162:163], v[162:163], v[162:163] op_sel:[0,1] op_sel_hi:[1,0]
	v_xor_b32_e32 v175, 16, v174
	v_add_u32_e32 v207, 64, v167
	v_mov_b32_e32 v181, v205
	v_mov_b32_e32 v197, v206
	v_mov_b32_e32 v145, v203
	v_mov_b32_e32 v163, v204
	v_cmp_lt_i32_e32 vcc, v175, v207
	v_pk_add_f32 v[164:165], v[180:181], v[196:197]
	v_pk_add_f32 v[144:145], v[144:145], v[162:163]
	v_cndmask_b32_e32 v175, v174, v175, vcc
	v_pk_add_f32 v[144:145], v[144:145], v[164:165]
	v_lshlrev_b32_e32 v176, 2, v175
	v_add_f32_e32 v175, v144, v145
	ds_bpermute_b32 v178, v176, v175
	v_xor_b32_e32 v202, 32, v174
	v_ashrrev_i32_e32 v199, 31, v198
	v_ashrrev_i32_e32 v169, 31, v168
	v_ashrrev_i32_e32 v167, 31, v166
	v_cmp_lt_i32_e32 vcc, v202, v207
	v_lshl_add_u64 v[144:145], v[198:199], 2, s[0:1]
	v_lshl_add_u64 v[162:163], v[168:169], 2, s[0:1]
	v_cndmask_b32_e32 v177, v174, v202, vcc
	v_lshl_add_u64 v[164:165], v[166:167], 2, s[0:1]
	s_waitcnt lgkmcnt(0)
	v_add_f32_e32 v181, v175, v178
	global_load_dword v180, v[160:161], off offset:512
	global_load_dword v179, v[160:161], off offset:576
	global_load_dword v178, v[160:161], off offset:640
	global_load_dword v197, v[144:145], off
	global_load_dword v202, v[162:163], off
	global_load_dword v203, v[164:165], off
	global_load_dword v175, v[160:161], off offset:704
	v_lshlrev_b32_e32 v177, 2, v177
	ds_bpermute_b32 v196, v177, v181
	v_lshl_or_b32 v190, s57, 8, v172
	v_ashrrev_i32_e32 v191, 31, v190
	s_mov_b32 s19, 0x40000
	s_mov_b64 s[36:37], 0x40000
	s_waitcnt lgkmcnt(0)
	v_add_f32_e32 v144, v181, v196
	s_waitcnt vmcnt(0)
	v_pk_mul_f32 v[160:161], v[140:141], s[14:15] op_sel_hi:[1,0]
	v_pk_mul_f32 v[162:163], v[156:157], s[14:15] op_sel_hi:[1,0]
	v_pk_mul_f32 v[156:157], v[142:143], s[14:15] op_sel_hi:[1,0]
	v_mul_f32_e32 v142, v195, v195
	v_mul_f32_e32 v142, 0x3c800000, v142
	v_fmaak_f32 v142, v142, v144, 0x358637bd
	v_mul_f32_e32 v143, 0x4b800000, v142
	v_cmp_gt_f32_e32 vcc, s52, v142
	v_pk_mul_f32 v[164:165], v[154:155], s[14:15] op_sel_hi:[1,0]
	v_pk_mul_f32 v[154:155], v[182:183], s[14:15] op_sel_hi:[1,0]
	v_cndmask_b32_e32 v142, v142, v143, vcc
	v_rsq_f32_e32 v181, v142
	v_pk_mul_f32 v[140:141], v[184:185], s[14:15] op_sel_hi:[1,0]
	v_pk_mul_f32 v[144:145], v[186:187], s[14:15] op_sel_hi:[1,0]
	v_pk_mul_f32 v[142:143], v[188:189], s[14:15] op_sel_hi:[1,0]
	v_mul_f32_e32 v182, 0x45800000, v181
	v_cndmask_b32_e32 v181, v181, v182, vcc
	v_mul_f32_e32 v182, v195, v181
	v_pk_mul_f32 v[126:127], v[126:127], v[182:183] op_sel_hi:[1,0]
	v_pk_mul_f32 v[128:129], v[128:129], v[182:183] op_sel_hi:[1,0]
	v_pk_mul_f32 v[122:123], v[122:123], v[182:183] op_sel_hi:[1,0]
	v_pk_mul_f32 v[124:125], v[124:125], v[182:183] op_sel_hi:[1,0]
	v_pk_mul_f32 v[128:129], v[162:163], v[128:129]
	v_pk_mul_f32 v[126:127], v[164:165], v[126:127]
	v_pk_mul_f32 v[124:125], v[156:157], v[124:125]
	v_pk_mul_f32 v[122:123], v[160:161], v[122:123]
	v_cvt_pk_bf16_f32 v126, v126, v127
	v_cvt_pk_bf16_f32 v127, v128, v129
	v_pk_mul_f32 v[118:119], v[118:119], v[182:183] op_sel_hi:[1,0]
	v_cvt_pk_bf16_f32 v128, v122, v123
	v_cvt_pk_bf16_f32 v129, v124, v125
	v_lshl_add_u64 v[122:123], s[28:29], 0, v[200:201]
	v_lshlrev_b64 v[124:125], 1, v[190:191]
	v_lshl_add_u64 v[122:123], v[122:123], 0, v[124:125]
	global_store_dwordx4 v[122:123], v[126:129], off
	v_pk_mul_f32 v[120:121], v[120:121], v[182:183] op_sel_hi:[1,0]
	v_mul_f32_e32 v181, v94, v94
	v_pk_mul_f32 v[126:127], v[116:117], v[116:117]
	v_pk_mul_f32 v[128:129], v[114:115], v[114:115]
	v_mul_f32_e32 v183, v95, v95
	v_pk_mov_b32 v[184:185], v[128:129], v[126:127] op_sel:[1,0]
	v_mov_b32_e32 v129, v127
	v_pk_add_f32 v[126:127], v[184:185], v[128:129]
	v_pk_mul_f32 v[128:129], v[108:109], v[108:109]
	v_pk_mul_f32 v[184:185], v[106:107], v[106:107]
	v_pk_add_f32 v[126:127], v[126:127], v[126:127] op_sel:[0,1] op_sel_hi:[1,0]
	v_pk_mov_b32 v[186:187], v[184:185], v[128:129] op_sel:[1,0]
	v_mov_b32_e32 v185, v129
	v_pk_add_f32 v[128:129], v[186:187], v[184:185]
	v_mov_b32_e32 v127, v181
	v_pk_add_f32 v[128:129], v[128:129], v[128:129] op_sel:[0,1] op_sel_hi:[1,0]
	v_mul_f32_e32 v184, v96, v96
	v_mov_b32_e32 v129, v183
	v_pk_add_f32 v[126:127], v[126:127], v[128:129]
	v_mul_f32_e32 v128, v103, v103
	v_pk_fma_f32 v[128:129], v[102:103], v[102:103], v[128:129] op_sel_hi:[1,1,0]
	v_mul_f32_e32 v186, v97, v97
	v_mov_b32_e32 v129, v184
	v_mul_f32_e32 v184, v105, v105
	v_pk_fma_f32 v[184:185], v[104:105], v[104:105], v[184:185] op_sel_hi:[1,1,0]
	v_pk_mul_f32 v[118:119], v[154:155], v[118:119]
	v_mov_b32_e32 v185, v186
	v_pk_add_f32 v[128:129], v[128:129], v[184:185]
	v_pk_mul_f32 v[110:111], v[110:111], v[182:183] op_sel_hi:[1,0]
	v_pk_add_f32 v[126:127], v[126:127], v[128:129]
	v_pk_mul_f32 v[112:113], v[112:113], v[182:183] op_sel_hi:[1,0]
	v_add_f32_e32 v126, v126, v127
	ds_bpermute_b32 v127, v176, v126
	v_pk_mul_f32 v[120:121], v[140:141], v[120:121]
	s_waitcnt lgkmcnt(0)
	v_add_f32_e32 v128, v126, v127
	ds_bpermute_b32 v129, v177, v128
	v_pk_mul_f32 v[126:127], v[142:143], v[112:113]
	v_pk_mul_f32 v[112:113], v[144:145], v[110:111]
	v_cvt_pk_bf16_f32 v110, v118, v119
	v_mul_f32_e32 v119, v197, v197
	s_waitcnt lgkmcnt(0)
	v_add_f32_e32 v118, v128, v129
	v_mul_f32_e32 v119, 0x3c800000, v119
	v_fmaak_f32 v118, v119, v118, 0x358637bd
	v_mul_f32_e32 v119, 0x4b800000, v118
	v_cmp_gt_f32_e32 vcc, s52, v118
	v_cvt_pk_bf16_f32 v111, v120, v121
	v_cvt_pk_bf16_f32 v112, v112, v113
	v_cvt_pk_bf16_f32 v113, v126, v127
	global_store_dwordx4 v[122:123], v[110:113], off offset:64
	s_nop 0
	v_cndmask_b32_e32 v118, v118, v119, vcc
	v_rsq_f32_e32 v118, v118
	v_lshlrev_b64 v[112:113], 11, v[198:199]
	v_lshl_add_u64 v[112:113], s[28:29], 0, v[112:113]
	v_lshl_add_u64 v[112:113], v[112:113], 0, v[124:125]
	v_mul_f32_e32 v110, 0x45800000, v118
	v_cndmask_b32_e32 v110, v118, v110, vcc
	v_mul_f32_e32 v110, v197, v110
	v_pk_mul_f32 v[106:107], v[106:107], v[110:111] op_sel_hi:[1,0]
	v_pk_mul_f32 v[108:109], v[108:109], v[110:111] op_sel_hi:[1,0]
	v_pk_mul_f32 v[114:115], v[114:115], v[110:111] op_sel_hi:[1,0]
	v_pk_mul_f32 v[116:117], v[116:117], v[110:111] op_sel_hi:[1,0]
	v_pk_mul_f32 v[118:119], v[156:157], v[108:109]
	v_pk_mul_f32 v[108:109], v[160:161], v[106:107]
	v_pk_mul_f32 v[116:117], v[162:163], v[116:117]
	v_pk_mul_f32 v[114:115], v[164:165], v[114:115]
	v_pk_mul_f32 v[102:103], v[102:103], v[110:111] op_sel_hi:[1,0]
	v_cvt_pk_bf16_f32 v106, v114, v115
	v_cvt_pk_bf16_f32 v107, v116, v117
	v_cvt_pk_bf16_f32 v108, v108, v109
	v_cvt_pk_bf16_f32 v109, v118, v119
	global_store_dwordx4 v[112:113], v[106:109], off
	v_pk_mul_f32 v[104:105], v[104:105], v[110:111] op_sel_hi:[1,0]
	v_mul_f32_e32 v111, v78, v78
	v_pk_mul_f32 v[106:107], v[100:101], v[100:101]
	v_pk_mul_f32 v[108:109], v[98:99], v[98:99]
	v_pk_mul_f32 v[102:103], v[154:155], v[102:103]
	v_pk_mov_b32 v[114:115], v[108:109], v[106:107] op_sel:[1,0]
	v_mov_b32_e32 v109, v107
	v_pk_add_f32 v[106:107], v[114:115], v[108:109]
	v_pk_mul_f32 v[108:109], v[92:93], v[92:93]
	v_pk_mul_f32 v[114:115], v[90:91], v[90:91]
	v_pk_add_f32 v[106:107], v[106:107], v[106:107] op_sel:[0,1] op_sel_hi:[1,0]
	v_pk_mov_b32 v[116:117], v[114:115], v[108:109] op_sel:[1,0]
	v_mov_b32_e32 v115, v109
	v_pk_add_f32 v[108:109], v[116:117], v[114:115]
	v_mul_f32_e32 v114, v79, v79
	v_pk_add_f32 v[108:109], v[108:109], v[108:109] op_sel:[0,1] op_sel_hi:[1,0]
	v_mov_b32_e32 v107, v111
	v_mov_b32_e32 v109, v114
	v_pk_add_f32 v[106:107], v[106:107], v[108:109]
	v_mul_f32_e32 v108, v87, v87
	v_mul_f32_e32 v115, v80, v80
	v_pk_fma_f32 v[108:109], v[86:87], v[86:87], v[108:109] op_sel_hi:[1,1,0]
	v_mul_f32_e32 v114, v89, v89
	v_mul_f32_e32 v116, v81, v81
	v_mov_b32_e32 v109, v115
	v_pk_fma_f32 v[114:115], v[88:89], v[88:89], v[114:115] op_sel_hi:[1,1,0]
	v_pk_mul_f32 v[94:95], v[94:95], v[110:111] op_sel_hi:[1,0]
	v_mov_b32_e32 v115, v116
	v_pk_add_f32 v[108:109], v[108:109], v[114:115]
	v_pk_mul_f32 v[96:97], v[96:97], v[110:111] op_sel_hi:[1,0]
	v_pk_add_f32 v[106:107], v[106:107], v[108:109]
	v_pk_mul_f32 v[104:105], v[140:141], v[104:105]
	v_add_f32_e32 v106, v106, v107
	ds_bpermute_b32 v107, v176, v106
	s_waitcnt lgkmcnt(0)
	v_add_f32_e32 v108, v106, v107
	ds_bpermute_b32 v109, v177, v108
	v_pk_mul_f32 v[106:107], v[142:143], v[96:97]
	v_pk_mul_f32 v[96:97], v[144:145], v[94:95]
	v_cvt_pk_bf16_f32 v94, v102, v103
	v_mul_f32_e32 v103, v202, v202
	s_waitcnt lgkmcnt(0)
	v_add_f32_e32 v102, v108, v109
	v_mul_f32_e32 v103, 0x3c800000, v103
	v_fmaak_f32 v102, v103, v102, 0x358637bd
	v_mul_f32_e32 v103, 0x4b800000, v102
	v_cmp_gt_f32_e32 vcc, s52, v102
	v_cvt_pk_bf16_f32 v95, v104, v105
	v_cvt_pk_bf16_f32 v96, v96, v97
	v_cvt_pk_bf16_f32 v97, v106, v107
	global_store_dwordx4 v[112:113], v[94:97], off offset:64
	s_nop 0
	v_cndmask_b32_e32 v102, v102, v103, vcc
	v_rsq_f32_e32 v102, v102
	v_lshlrev_b64 v[96:97], 11, v[168:169]
	v_lshl_add_u64 v[96:97], s[28:29], 0, v[96:97]
	v_lshl_add_u64 v[96:97], v[96:97], 0, v[124:125]
	v_mul_f32_e32 v94, 0x45800000, v102
	v_cndmask_b32_e32 v94, v102, v94, vcc
	v_mul_f32_e32 v94, v202, v94
	v_pk_mul_f32 v[90:91], v[90:91], v[94:95] op_sel_hi:[1,0]
	v_pk_mul_f32 v[92:93], v[92:93], v[94:95] op_sel_hi:[1,0]
	v_pk_mul_f32 v[98:99], v[98:99], v[94:95] op_sel_hi:[1,0]
	v_pk_mul_f32 v[100:101], v[100:101], v[94:95] op_sel_hi:[1,0]
	v_pk_mul_f32 v[102:103], v[156:157], v[92:93]
	v_pk_mul_f32 v[92:93], v[160:161], v[90:91]
	v_pk_mul_f32 v[100:101], v[162:163], v[100:101]
	v_pk_mul_f32 v[98:99], v[164:165], v[98:99]
	v_pk_mul_f32 v[86:87], v[86:87], v[94:95] op_sel_hi:[1,0]
	v_cvt_pk_bf16_f32 v90, v98, v99
	v_cvt_pk_bf16_f32 v91, v100, v101
	v_cvt_pk_bf16_f32 v92, v92, v93
	v_cvt_pk_bf16_f32 v93, v102, v103
	global_store_dwordx4 v[96:97], v[90:93], off
	v_pk_mul_f32 v[88:89], v[88:89], v[94:95] op_sel_hi:[1,0]
	v_mul_f32_e32 v95, v66, v66
	v_pk_mul_f32 v[90:91], v[84:85], v[84:85]
	v_pk_mul_f32 v[92:93], v[82:83], v[82:83]
	v_pk_mul_f32 v[86:87], v[154:155], v[86:87]
	v_pk_mov_b32 v[98:99], v[92:93], v[90:91] op_sel:[1,0]
	v_mov_b32_e32 v93, v91
	v_pk_add_f32 v[90:91], v[98:99], v[92:93]
	v_pk_mul_f32 v[92:93], v[76:77], v[76:77]
	v_pk_mul_f32 v[98:99], v[74:75], v[74:75]
	v_pk_add_f32 v[90:91], v[90:91], v[90:91] op_sel:[0,1] op_sel_hi:[1,0]
	v_pk_mov_b32 v[100:101], v[98:99], v[92:93] op_sel:[1,0]
	v_mov_b32_e32 v99, v93
	v_pk_add_f32 v[92:93], v[100:101], v[98:99]
	v_mul_f32_e32 v98, v67, v67
	v_pk_add_f32 v[92:93], v[92:93], v[92:93] op_sel:[0,1] op_sel_hi:[1,0]
	v_mov_b32_e32 v91, v95
	v_mov_b32_e32 v93, v98
	v_pk_add_f32 v[90:91], v[90:91], v[92:93]
	v_mul_f32_e32 v92, v71, v71
	v_mul_f32_e32 v99, v68, v68
	v_pk_fma_f32 v[92:93], v[70:71], v[70:71], v[92:93] op_sel_hi:[1,1,0]
	v_mul_f32_e32 v98, v73, v73
	v_mul_f32_e32 v100, v69, v69
	v_mov_b32_e32 v93, v99
	v_pk_fma_f32 v[98:99], v[72:73], v[72:73], v[98:99] op_sel_hi:[1,1,0]
	v_pk_mul_f32 v[78:79], v[78:79], v[94:95] op_sel_hi:[1,0]
	v_mov_b32_e32 v99, v100
	v_pk_add_f32 v[92:93], v[92:93], v[98:99]
	v_pk_mul_f32 v[80:81], v[80:81], v[94:95] op_sel_hi:[1,0]
	v_pk_add_f32 v[90:91], v[90:91], v[92:93]
	v_pk_mul_f32 v[88:89], v[140:141], v[88:89]
	v_add_f32_e32 v90, v90, v91
	ds_bpermute_b32 v91, v176, v90
	s_waitcnt lgkmcnt(0)
	v_add_f32_e32 v92, v90, v91
	ds_bpermute_b32 v93, v177, v92
	v_pk_mul_f32 v[90:91], v[142:143], v[80:81]
	v_pk_mul_f32 v[80:81], v[144:145], v[78:79]
	v_cvt_pk_bf16_f32 v78, v86, v87
	v_mul_f32_e32 v87, v203, v203
	s_waitcnt lgkmcnt(0)
	v_add_f32_e32 v86, v92, v93
	v_mul_f32_e32 v87, 0x3c800000, v87
	v_fmaak_f32 v86, v87, v86, 0x358637bd
	v_mul_f32_e32 v87, 0x4b800000, v86
	v_cmp_gt_f32_e32 vcc, s52, v86
	v_cvt_pk_bf16_f32 v79, v88, v89
	v_cvt_pk_bf16_f32 v80, v80, v81
	v_cvt_pk_bf16_f32 v81, v90, v91
	global_store_dwordx4 v[96:97], v[78:81], off offset:64
	s_nop 0
	v_cndmask_b32_e32 v86, v86, v87, vcc
	v_rsq_f32_e32 v86, v86
	v_lshlrev_b64 v[80:81], 11, v[166:167]
	v_lshl_add_u64 v[80:81], s[28:29], 0, v[80:81]
	v_lshl_add_u64 v[80:81], v[80:81], 0, v[124:125]
	v_mul_f32_e32 v78, 0x45800000, v86
	v_cndmask_b32_e32 v78, v86, v78, vcc
	v_mul_f32_e32 v78, v203, v78
	v_pk_mul_f32 v[74:75], v[74:75], v[78:79] op_sel_hi:[1,0]
	v_pk_mul_f32 v[76:77], v[76:77], v[78:79] op_sel_hi:[1,0]
	v_pk_mul_f32 v[82:83], v[82:83], v[78:79] op_sel_hi:[1,0]
	v_pk_mul_f32 v[84:85], v[84:85], v[78:79] op_sel_hi:[1,0]
	v_pk_mul_f32 v[86:87], v[156:157], v[76:77]
	v_pk_mul_f32 v[76:77], v[160:161], v[74:75]
	v_pk_mul_f32 v[84:85], v[162:163], v[84:85]
	v_pk_mul_f32 v[82:83], v[164:165], v[82:83]
	v_pk_mul_f32 v[70:71], v[70:71], v[78:79] op_sel_hi:[1,0]
	v_cvt_pk_bf16_f32 v74, v82, v83
	v_cvt_pk_bf16_f32 v75, v84, v85
	v_cvt_pk_bf16_f32 v76, v76, v77
	v_cvt_pk_bf16_f32 v77, v86, v87
	global_store_dwordx4 v[80:81], v[74:77], off
	v_pk_mul_f32 v[72:73], v[72:73], v[78:79] op_sel_hi:[1,0]
	v_mul_f32_e32 v79, v46, v46
	v_pk_mul_f32 v[74:75], v[64:65], v[64:65]
	v_pk_mul_f32 v[76:77], v[62:63], v[62:63]
	v_pk_mul_f32 v[70:71], v[154:155], v[70:71]
	v_pk_mov_b32 v[82:83], v[76:77], v[74:75] op_sel:[1,0]
	v_mov_b32_e32 v77, v75
	v_pk_add_f32 v[74:75], v[82:83], v[76:77]
	v_pk_mul_f32 v[76:77], v[60:61], v[60:61]
	v_pk_mul_f32 v[82:83], v[58:59], v[58:59]
	v_pk_add_f32 v[74:75], v[74:75], v[74:75] op_sel:[0,1] op_sel_hi:[1,0]
	v_pk_mov_b32 v[84:85], v[82:83], v[76:77] op_sel:[1,0]
	v_mov_b32_e32 v83, v77
	v_pk_add_f32 v[76:77], v[84:85], v[82:83]
	v_mul_f32_e32 v82, v47, v47
	v_pk_add_f32 v[76:77], v[76:77], v[76:77] op_sel:[0,1] op_sel_hi:[1,0]
	v_mov_b32_e32 v75, v79
	v_mov_b32_e32 v77, v82
	v_pk_add_f32 v[74:75], v[74:75], v[76:77]
	v_mul_f32_e32 v76, v55, v55
	v_mul_f32_e32 v83, v48, v48
	v_pk_fma_f32 v[76:77], v[54:55], v[54:55], v[76:77] op_sel_hi:[1,1,0]
	v_mul_f32_e32 v82, v57, v57
	v_mul_f32_e32 v84, v49, v49
	v_mov_b32_e32 v77, v83
	v_pk_fma_f32 v[82:83], v[56:57], v[56:57], v[82:83] op_sel_hi:[1,1,0]
	v_pk_mul_f32 v[66:67], v[66:67], v[78:79] op_sel_hi:[1,0]
	v_mov_b32_e32 v83, v84
	v_pk_add_f32 v[76:77], v[76:77], v[82:83]
	v_pk_mul_f32 v[68:69], v[68:69], v[78:79] op_sel_hi:[1,0]
	v_pk_add_f32 v[74:75], v[74:75], v[76:77]
	v_pk_mul_f32 v[72:73], v[140:141], v[72:73]
	v_add_f32_e32 v74, v74, v75
	ds_bpermute_b32 v75, v176, v74
	s_waitcnt lgkmcnt(0)
	v_add_f32_e32 v76, v74, v75
	ds_bpermute_b32 v77, v177, v76
	v_pk_mul_f32 v[74:75], v[142:143], v[68:69]
	v_pk_mul_f32 v[68:69], v[144:145], v[66:67]
	v_cvt_pk_bf16_f32 v66, v70, v71
	v_mul_f32_e32 v71, v180, v180
	s_waitcnt lgkmcnt(0)
	v_add_f32_e32 v70, v76, v77
	v_mul_f32_e32 v71, 0x3c800000, v71
	v_fmaak_f32 v70, v71, v70, 0x358637bd
	v_mul_f32_e32 v71, 0x4b800000, v70
	v_cmp_gt_f32_e32 vcc, s52, v70
	v_cvt_pk_bf16_f32 v67, v72, v73
	v_cvt_pk_bf16_f32 v68, v68, v69
	v_cvt_pk_bf16_f32 v69, v74, v75
	global_store_dwordx4 v[80:81], v[66:69], off offset:64
	s_nop 0
	v_cndmask_b32_e32 v70, v70, v71, vcc
	v_rsq_f32_e32 v70, v70
	s_nop 0
	v_mul_f32_e32 v66, 0x45800000, v70
	v_cndmask_b32_e32 v66, v70, v66, vcc
	v_mul_f32_e32 v66, v180, v66
	v_pk_mul_f32 v[64:65], v[64:65], v[66:67] op_sel_hi:[1,0]
	v_pk_mul_f32 v[62:63], v[62:63], v[66:67] op_sel_hi:[1,0]
	v_pk_mul_f32 v[64:65], v[162:163], v[64:65]
	v_pk_mul_f32 v[58:59], v[58:59], v[66:67] op_sel_hi:[1,0]
	v_pk_mul_f32 v[60:61], v[60:61], v[66:67] op_sel_hi:[1,0]
	v_pk_mul_f32 v[62:63], v[164:165], v[62:63]
	v_pk_mul_f32 v[68:69], v[156:157], v[60:61]
	v_pk_mul_f32 v[60:61], v[160:161], v[58:59]
	v_cvt_pk_bf16_f32 v58, v62, v63
	v_cvt_pk_bf16_f32 v59, v64, v65
	v_add_co_u32_e32 v64, vcc, s19, v122
	v_cvt_pk_bf16_f32 v60, v60, v61
	v_cvt_pk_bf16_f32 v61, v68, v69
	v_pk_mul_f32 v[54:55], v[54:55], v[66:67] op_sel_hi:[1,0]
	s_nop 0
	v_addc_co_u32_e32 v65, vcc, 0, v123, vcc
	global_store_dwordx4 v[64:65], v[58:61], off
	v_pk_mul_f32 v[56:57], v[56:57], v[66:67] op_sel_hi:[1,0]
	v_mul_f32_e32 v67, v32, v32
	v_pk_mul_f32 v[58:59], v[52:53], v[52:53]
	v_pk_mul_f32 v[60:61], v[50:51], v[50:51]
	v_pk_mul_f32 v[54:55], v[154:155], v[54:55]
	v_pk_mov_b32 v[64:65], v[60:61], v[58:59] op_sel:[1,0]
	v_mov_b32_e32 v61, v59
	v_pk_add_f32 v[58:59], v[64:65], v[60:61]
	v_pk_mul_f32 v[60:61], v[44:45], v[44:45]
	v_pk_mul_f32 v[64:65], v[42:43], v[42:43]
	v_pk_add_f32 v[58:59], v[58:59], v[58:59] op_sel:[0,1] op_sel_hi:[1,0]
	v_pk_mov_b32 v[68:69], v[64:65], v[60:61] op_sel:[1,0]
	v_mov_b32_e32 v65, v61
	v_pk_add_f32 v[60:61], v[68:69], v[64:65]
	v_mul_f32_e32 v64, v30, v30
	v_mul_f32_e32 v65, v31, v31
	v_pk_add_f32 v[60:61], v[60:61], v[60:61] op_sel:[0,1] op_sel_hi:[1,0]
	v_mov_b32_e32 v59, v64
	v_mov_b32_e32 v61, v65
	v_pk_add_f32 v[58:59], v[58:59], v[60:61]
	v_mul_f32_e32 v60, v39, v39
	v_mul_f32_e32 v64, v41, v41
	v_mul_f32_e32 v68, v33, v33
	v_pk_fma_f32 v[60:61], v[38:39], v[38:39], v[60:61] op_sel_hi:[1,1,0]
	v_pk_fma_f32 v[64:65], v[40:41], v[40:41], v[64:65] op_sel_hi:[1,1,0]
	v_mov_b32_e32 v61, v67
	v_mov_b32_e32 v65, v68
	v_pk_add_f32 v[60:61], v[60:61], v[64:65]
	v_pk_mul_f32 v[46:47], v[46:47], v[66:67] op_sel_hi:[1,0]
	v_pk_add_f32 v[58:59], v[58:59], v[60:61]
	v_pk_mul_f32 v[48:49], v[48:49], v[66:67] op_sel_hi:[1,0]
	v_add_f32_e32 v58, v58, v59
	ds_bpermute_b32 v59, v176, v58
	v_lshl_add_u64 v[62:63], v[122:123], 0, s[36:37]
	v_pk_mul_f32 v[56:57], v[140:141], v[56:57]
	s_mov_b32 s19, 0x48000
	s_mov_b64 s[36:37], 0x48000
	s_waitcnt lgkmcnt(0)
	v_add_f32_e32 v60, v58, v59
	ds_bpermute_b32 v61, v177, v60
	v_pk_mul_f32 v[58:59], v[142:143], v[48:49]
	v_pk_mul_f32 v[48:49], v[144:145], v[46:47]
	v_cvt_pk_bf16_f32 v46, v54, v55
	v_mul_f32_e32 v55, v179, v179
	s_waitcnt lgkmcnt(0)
	v_add_f32_e32 v54, v60, v61
	v_mul_f32_e32 v55, 0x3c800000, v55
	v_fmaak_f32 v54, v55, v54, 0x358637bd
	v_mul_f32_e32 v55, 0x4b800000, v54
	v_cmp_gt_f32_e32 vcc, s52, v54
	v_cvt_pk_bf16_f32 v47, v56, v57
	v_cvt_pk_bf16_f32 v48, v48, v49
	v_cvt_pk_bf16_f32 v49, v58, v59
	global_store_dwordx4 v[62:63], v[46:49], off offset:64
	s_nop 0
	v_cndmask_b32_e32 v54, v54, v55, vcc
	v_rsq_f32_e32 v54, v54
	s_nop 0
	v_mul_f32_e32 v46, 0x45800000, v54
	v_cndmask_b32_e32 v46, v54, v46, vcc
	v_mul_f32_e32 v46, v179, v46
	v_pk_mul_f32 v[48:49], v[50:51], v[46:47] op_sel_hi:[1,0]
	v_pk_mul_f32 v[50:51], v[52:53], v[46:47] op_sel_hi:[1,0]
	v_pk_mul_f32 v[42:43], v[42:43], v[46:47] op_sel_hi:[1,0]
	v_pk_mul_f32 v[50:51], v[162:163], v[50:51]
	v_pk_mul_f32 v[44:45], v[44:45], v[46:47] op_sel_hi:[1,0]
	v_pk_mul_f32 v[48:49], v[164:165], v[48:49]
	v_pk_mul_f32 v[52:53], v[156:157], v[44:45]
	v_pk_mul_f32 v[44:45], v[160:161], v[42:43]
	v_cvt_pk_bf16_f32 v42, v48, v49
	v_cvt_pk_bf16_f32 v43, v50, v51
	v_add_co_u32_e32 v50, vcc, s19, v122
	v_cvt_pk_bf16_f32 v44, v44, v45
	v_cvt_pk_bf16_f32 v45, v52, v53
	v_pk_mul_f32 v[38:39], v[38:39], v[46:47] op_sel_hi:[1,0]
	s_nop 0
	v_addc_co_u32_e32 v51, vcc, 0, v123, vcc
	global_store_dwordx4 v[50:51], v[42:45], off
	v_pk_mul_f32 v[40:41], v[40:41], v[46:47] op_sel_hi:[1,0]
	v_mul_f32_e32 v47, v14, v14
	v_pk_mul_f32 v[42:43], v[36:37], v[36:37]
	v_pk_mul_f32 v[44:45], v[34:35], v[34:35]
	v_pk_mul_f32 v[38:39], v[154:155], v[38:39]
	v_pk_mov_b32 v[50:51], v[44:45], v[42:43] op_sel:[1,0]
	v_mov_b32_e32 v45, v43
	v_pk_add_f32 v[42:43], v[50:51], v[44:45]
	v_pk_mul_f32 v[44:45], v[28:29], v[28:29]
	v_pk_mul_f32 v[50:51], v[26:27], v[26:27]
	v_pk_add_f32 v[42:43], v[42:43], v[42:43] op_sel:[0,1] op_sel_hi:[1,0]
	v_pk_mov_b32 v[52:53], v[50:51], v[44:45] op_sel:[1,0]
	v_mov_b32_e32 v51, v45
	v_pk_add_f32 v[44:45], v[52:53], v[50:51]
	v_mul_f32_e32 v50, v15, v15
	v_pk_add_f32 v[44:45], v[44:45], v[44:45] op_sel:[0,1] op_sel_hi:[1,0]
	v_mov_b32_e32 v43, v47
	v_mov_b32_e32 v45, v50
	v_pk_add_f32 v[42:43], v[42:43], v[44:45]
	v_mul_f32_e32 v44, v23, v23
	v_mul_f32_e32 v51, v16, v16
	v_pk_fma_f32 v[44:45], v[22:23], v[22:23], v[44:45] op_sel_hi:[1,1,0]
	v_mul_f32_e32 v50, v25, v25
	v_mul_f32_e32 v52, v17, v17
	v_mov_b32_e32 v45, v51
	v_pk_fma_f32 v[50:51], v[24:25], v[24:25], v[50:51] op_sel_hi:[1,1,0]
	v_pk_mul_f32 v[30:31], v[30:31], v[46:47] op_sel_hi:[1,0]
	v_mov_b32_e32 v51, v52
	v_pk_add_f32 v[44:45], v[44:45], v[50:51]
	v_pk_mul_f32 v[32:33], v[32:33], v[46:47] op_sel_hi:[1,0]
	v_pk_add_f32 v[42:43], v[42:43], v[44:45]
	v_lshl_add_u64 v[48:49], v[122:123], 0, s[36:37]
	v_add_f32_e32 v42, v42, v43
	ds_bpermute_b32 v43, v176, v42
	v_pk_mul_f32 v[40:41], v[140:141], v[40:41]
	s_mov_b64 s[36:37], 0x50000
	s_waitcnt lgkmcnt(0)
	v_add_f32_e32 v44, v42, v43
	ds_bpermute_b32 v45, v177, v44
	v_pk_mul_f32 v[42:43], v[142:143], v[32:33]
	v_pk_mul_f32 v[32:33], v[144:145], v[30:31]
	v_cvt_pk_bf16_f32 v30, v38, v39
	v_mul_f32_e32 v39, v178, v178
	s_waitcnt lgkmcnt(0)
	v_add_f32_e32 v38, v44, v45
	v_mul_f32_e32 v39, 0x3c800000, v39
	v_fmaak_f32 v38, v39, v38, 0x358637bd
	v_mul_f32_e32 v39, 0x4b800000, v38
	v_cmp_gt_f32_e32 vcc, s52, v38
	v_cvt_pk_bf16_f32 v31, v40, v41
	v_cvt_pk_bf16_f32 v32, v32, v33
	v_cvt_pk_bf16_f32 v33, v42, v43
	global_store_dwordx4 v[48:49], v[30:33], off offset:64
	s_nop 0
	v_cndmask_b32_e32 v38, v38, v39, vcc
	v_rsq_f32_e32 v38, v38
	s_nop 0
	v_mul_f32_e32 v30, 0x45800000, v38
	v_cndmask_b32_e32 v30, v38, v30, vcc
	v_mul_f32_e32 v30, v178, v30
	v_pk_mul_f32 v[32:33], v[34:35], v[30:31] op_sel_hi:[1,0]
	v_pk_mul_f32 v[34:35], v[36:37], v[30:31] op_sel_hi:[1,0]
	v_pk_mul_f32 v[26:27], v[26:27], v[30:31] op_sel_hi:[1,0]
	v_pk_mul_f32 v[34:35], v[162:163], v[34:35]
	v_pk_mul_f32 v[28:29], v[28:29], v[30:31] op_sel_hi:[1,0]
	v_pk_mul_f32 v[32:33], v[164:165], v[32:33]
	v_pk_mul_f32 v[36:37], v[156:157], v[28:29]
	v_pk_mul_f32 v[28:29], v[160:161], v[26:27]
	v_cvt_pk_bf16_f32 v26, v32, v33
	v_cvt_pk_bf16_f32 v27, v34, v35
	v_add_co_u32_e32 v34, vcc, s53, v122
	v_cvt_pk_bf16_f32 v28, v28, v29
	v_cvt_pk_bf16_f32 v29, v36, v37
	v_pk_mul_f32 v[22:23], v[22:23], v[30:31] op_sel_hi:[1,0]
	s_nop 0
	v_addc_co_u32_e32 v35, vcc, 0, v123, vcc
	global_store_dwordx4 v[34:35], v[26:29], off
	v_pk_mul_f32 v[24:25], v[24:25], v[30:31] op_sel_hi:[1,0]
	v_mul_f32_e32 v31, v2, v2
	v_pk_mul_f32 v[26:27], v[20:21], v[20:21]
	v_pk_mul_f32 v[28:29], v[18:19], v[18:19]
	v_pk_mul_f32 v[22:23], v[154:155], v[22:23]
	v_pk_mov_b32 v[34:35], v[28:29], v[26:27] op_sel:[1,0]
	v_mov_b32_e32 v29, v27
	v_pk_add_f32 v[26:27], v[34:35], v[28:29]
	v_pk_mul_f32 v[28:29], v[12:13], v[12:13]
	v_pk_mul_f32 v[34:35], v[10:11], v[10:11]
	v_pk_add_f32 v[26:27], v[26:27], v[26:27] op_sel:[0,1] op_sel_hi:[1,0]
	v_pk_mov_b32 v[36:37], v[34:35], v[28:29] op_sel:[1,0]
	v_mov_b32_e32 v35, v29
	v_pk_add_f32 v[28:29], v[36:37], v[34:35]
	v_mul_f32_e32 v34, v3, v3
	v_pk_add_f32 v[28:29], v[28:29], v[28:29] op_sel:[0,1] op_sel_hi:[1,0]
	v_mov_b32_e32 v27, v31
	v_mov_b32_e32 v29, v34
	v_pk_add_f32 v[26:27], v[26:27], v[28:29]
	v_mul_f32_e32 v28, v7, v7
	v_mul_f32_e32 v35, v4, v4
	v_pk_fma_f32 v[28:29], v[6:7], v[6:7], v[28:29] op_sel_hi:[1,1,0]
	v_mul_f32_e32 v34, v9, v9
	v_mul_f32_e32 v36, v5, v5
	v_mov_b32_e32 v29, v35
	v_pk_fma_f32 v[34:35], v[8:9], v[8:9], v[34:35] op_sel_hi:[1,1,0]
	v_pk_mul_f32 v[14:15], v[14:15], v[30:31] op_sel_hi:[1,0]
	v_mov_b32_e32 v35, v36
	v_pk_add_f32 v[28:29], v[28:29], v[34:35]
	v_pk_mul_f32 v[16:17], v[16:17], v[30:31] op_sel_hi:[1,0]
	v_pk_add_f32 v[26:27], v[26:27], v[28:29]
	v_lshl_add_u64 v[32:33], v[122:123], 0, s[36:37]
	v_add_f32_e32 v26, v26, v27
	ds_bpermute_b32 v27, v176, v26
	v_pk_mul_f32 v[24:25], v[140:141], v[24:25]
	s_waitcnt lgkmcnt(0)
	v_add_f32_e32 v28, v26, v27
	ds_bpermute_b32 v29, v177, v28
	v_pk_mul_f32 v[26:27], v[142:143], v[16:17]
	v_pk_mul_f32 v[16:17], v[144:145], v[14:15]
	v_cvt_pk_bf16_f32 v14, v22, v23
	v_mul_f32_e32 v23, v175, v175
	s_waitcnt lgkmcnt(0)
	v_add_f32_e32 v22, v28, v29
	v_mul_f32_e32 v23, 0x3c800000, v23
	v_fmaak_f32 v22, v23, v22, 0x358637bd
	v_mul_f32_e32 v23, 0x4b800000, v22
	v_cmp_gt_f32_e32 vcc, s52, v22
	v_cvt_pk_bf16_f32 v15, v24, v25
	v_cvt_pk_bf16_f32 v16, v16, v17
	v_cvt_pk_bf16_f32 v17, v26, v27
	global_store_dwordx4 v[32:33], v[14:17], off offset:64
	s_nop 0
	v_cndmask_b32_e32 v22, v22, v23, vcc
	v_rsq_f32_e32 v22, v22
	s_nop 0
	v_mul_f32_e32 v14, 0x45800000, v22
	v_cndmask_b32_e32 v14, v22, v14, vcc
	v_mul_f32_e32 v14, v175, v14
	v_pk_mul_f32 v[16:17], v[18:19], v[14:15] op_sel_hi:[1,0]
	v_pk_mul_f32 v[18:19], v[20:21], v[14:15] op_sel_hi:[1,0]
	v_pk_mul_f32 v[10:11], v[10:11], v[14:15] op_sel_hi:[1,0]
	v_pk_mul_f32 v[18:19], v[162:163], v[18:19]
	v_pk_mul_f32 v[12:13], v[12:13], v[14:15] op_sel_hi:[1,0]
	v_pk_mul_f32 v[16:17], v[164:165], v[16:17]
	v_pk_mul_f32 v[20:21], v[156:157], v[12:13]
	v_pk_mul_f32 v[12:13], v[160:161], v[10:11]
	v_cvt_pk_bf16_f32 v10, v16, v17
	v_cvt_pk_bf16_f32 v11, v18, v19
	v_add_co_u32_e32 v18, vcc, s56, v122
	v_pk_mul_f32 v[2:3], v[2:3], v[14:15] op_sel_hi:[1,0]
	s_nop 0
	v_addc_co_u32_e32 v19, vcc, 0, v123, vcc
	v_pk_mul_f32 v[4:5], v[4:5], v[14:15] op_sel_hi:[1,0]
	v_cvt_pk_bf16_f32 v12, v12, v13
	v_cvt_pk_bf16_f32 v13, v20, v21
	v_lshl_add_u64 v[16:17], v[122:123], 0, s[16:17]
	global_store_dwordx4 v[18:19], v[10:13], off
	v_pk_mul_f32 v[6:7], v[6:7], v[14:15] op_sel_hi:[1,0]
	v_pk_mul_f32 v[8:9], v[8:9], v[14:15] op_sel_hi:[1,0]
	v_pk_mul_f32 v[10:11], v[142:143], v[4:5]
	v_pk_mul_f32 v[4:5], v[144:145], v[2:3]
	s_andn2_b64 vcc, exec, s[4:5]
	s_mov_b64 s[4:5], -1
	v_pk_mul_f32 v[8:9], v[140:141], v[8:9]
	v_pk_mul_f32 v[6:7], v[154:155], v[6:7]
	s_nop 0
	v_cvt_pk_bf16_f32 v2, v6, v7
	v_cvt_pk_bf16_f32 v3, v8, v9
	v_cvt_pk_bf16_f32 v4, v4, v5
	v_cvt_pk_bf16_f32 v5, v10, v11
	global_store_dwordx4 v[16:17], v[2:5], off offset:64
	s_cbranch_vccnz .LBB0_1591
	s_andn2_b64 vcc, exec, s[6:7]
	s_cbranch_vccnz .LBB0_1590
	s_barrier
	s_branch .LBB0_1590

.LBB0_1745:
.LBB0_1746:
	s_lshl_b32 s8, s48, 8
	v_mov_b32_e32 v35, v34
	s_add_i32 s30, s8, 0
	s_nop 0
	v_permlane32_swap_b32_e32 v34, v35
	s_and_saveexec_b64 s[8:9], s[4:5]
	v_and_b32_e32 v36, 63, v0
	v_lshl_add_u32 v36, v36, 2, s30
	v_add_f32_e32 v34, v34, v35
	ds_write_b32 v36, v34 offset:49280
	s_or_b64 exec, exec, s[8:9]
	s_waitcnt lgkmcnt(0)
	v_add_u32_e32 v42, s30, v1
	ds_read_b128 v[34:37], v42 offset:49280
	ds_read_b128 v[38:41], v42 offset:49312
	s_mulk_i32 s48, 0xf00
	s_add_i32 s30, s30, s48
	v_lshlrev_b32_e32 v196, 1, v198
	s_waitcnt lgkmcnt(1)
	v_rcp_f32_e32 v43, v34
	v_rcp_f32_e32 v44, v35
	v_rcp_f32_e32 v45, v36
	v_rcp_f32_e32 v46, v37
	s_waitcnt lgkmcnt(0)
	v_rcp_f32_e32 v47, v38
	ds_read_b128 v[34:37], v42 offset:49344
	v_rcp_f32_e32 v48, v39
	v_rcp_f32_e32 v49, v40
	v_rcp_f32_e32 v50, v41
	ds_read_b128 v[38:41], v42 offset:49376
	v_lshlrev_b32_e32 v42, 1, v205
	v_mul_f32_e32 v2, v2, v43
	v_add3_u32 v42, s30, v207, v42
	v_cvt_pk_bf16_f32 v2, v2, s0
	ds_write_b16 v42, v2 offset:51200
	v_mul_f32_e32 v2, v18, v43
	v_cvt_pk_bf16_f32 v2, v2, s0
	ds_write_b16 v42, v2 offset:51264
	v_mul_f32_e32 v2, v3, v44
	v_cvt_pk_bf16_f32 v2, v2, s0
	ds_write_b16 v42, v2 offset:51328
	v_mul_f32_e32 v2, v19, v44
	v_cvt_pk_bf16_f32 v2, v2, s0
	ds_write_b16 v42, v2 offset:51392
	v_mul_f32_e32 v2, v4, v45
	v_cvt_pk_bf16_f32 v2, v2, s0
	ds_write_b16 v42, v2 offset:51456
	v_mul_f32_e32 v2, v20, v45
	v_cvt_pk_bf16_f32 v2, v2, s0
	ds_write_b16 v42, v2 offset:51520
	v_mul_f32_e32 v2, v5, v46
	v_cvt_pk_bf16_f32 v2, v2, s0
	ds_write_b16 v42, v2 offset:51584
	v_mul_f32_e32 v2, v21, v46
	v_cvt_pk_bf16_f32 v2, v2, s0
	ds_write_b16 v42, v2 offset:51648
	v_mul_f32_e32 v2, v6, v47
	v_cvt_pk_bf16_f32 v2, v2, s0
	ds_write_b16 v42, v2 offset:52224
	v_mul_f32_e32 v2, v22, v47
	v_cvt_pk_bf16_f32 v2, v2, s0
	ds_write_b16 v42, v2 offset:52288
	v_mul_f32_e32 v2, v7, v48
	v_cvt_pk_bf16_f32 v2, v2, s0
	ds_write_b16 v42, v2 offset:52352
	v_mul_f32_e32 v2, v23, v48
	v_cvt_pk_bf16_f32 v2, v2, s0
	ds_write_b16 v42, v2 offset:52416
	v_mul_f32_e32 v2, v8, v49
	v_cvt_pk_bf16_f32 v2, v2, s0
	ds_write_b16 v42, v2 offset:52480
	v_mul_f32_e32 v2, v24, v49
	v_cvt_pk_bf16_f32 v2, v2, s0
	s_waitcnt lgkmcnt(14)
	v_rcp_f32_e32 v34, v34
	ds_write_b16 v42, v2 offset:52544
	v_mul_f32_e32 v2, v9, v50
	v_cvt_pk_bf16_f32 v2, v2, s0
	ds_write_b16 v42, v2 offset:52608
	v_mul_f32_e32 v2, v25, v50
	v_cvt_pk_bf16_f32 v2, v2, s0
	v_rcp_f32_e32 v35, v35
	ds_write_b16 v42, v2 offset:52672
	v_mul_f32_e32 v2, v10, v34
	v_cvt_pk_bf16_f32 v2, v2, s0
	ds_write_b16 v42, v2 offset:53248
	v_mul_f32_e32 v2, v26, v34
	v_cvt_pk_bf16_f32 v2, v2, s0
	v_rcp_f32_e32 v36, v36
	ds_write_b16 v42, v2 offset:53312
	v_mul_f32_e32 v2, v11, v35
	v_cvt_pk_bf16_f32 v2, v2, s0
	ds_write_b16 v42, v2 offset:53376
	v_mul_f32_e32 v2, v27, v35
	v_cvt_pk_bf16_f32 v2, v2, s0
	v_rcp_f32_e32 v37, v37
	ds_write_b16 v42, v2 offset:53440
	v_mul_f32_e32 v2, v12, v36
	v_cvt_pk_bf16_f32 v2, v2, s0
	ds_write_b16 v42, v2 offset:53504
	v_mul_f32_e32 v2, v28, v36
	v_cvt_pk_bf16_f32 v2, v2, s0
	s_waitcnt lgkmcnt(14)
	v_rcp_f32_e32 v38, v38
	ds_write_b16 v42, v2 offset:53568
	v_mul_f32_e32 v2, v13, v37
	v_cvt_pk_bf16_f32 v2, v2, s0
	ds_write_b16 v42, v2 offset:53632
	v_mul_f32_e32 v2, v29, v37
	v_cvt_pk_bf16_f32 v2, v2, s0
	v_rcp_f32_e32 v39, v39
	ds_write_b16 v42, v2 offset:53696
	v_mul_f32_e32 v2, v14, v38
	v_cvt_pk_bf16_f32 v2, v2, s0
	ds_write_b16 v42, v2 offset:54272
	v_mul_f32_e32 v2, v30, v38
	v_cvt_pk_bf16_f32 v2, v2, s0
	v_rcp_f32_e32 v40, v40
	ds_write_b16 v42, v2 offset:54336
	v_mul_f32_e32 v2, v15, v39
	v_cvt_pk_bf16_f32 v2, v2, s0
	ds_write_b16 v42, v2 offset:54400
	v_mul_f32_e32 v2, v31, v39
	v_cvt_pk_bf16_f32 v2, v2, s0
	v_rcp_f32_e32 v41, v41
	ds_write_b16 v42, v2 offset:54464
	v_mul_f32_e32 v2, v16, v40
	v_cvt_pk_bf16_f32 v2, v2, s0
	ds_write_b16 v42, v2 offset:54528
	v_mul_f32_e32 v2, v32, v40
	v_cvt_pk_bf16_f32 v2, v2, s0
	ds_write_b16 v42, v2 offset:54592
	v_mul_f32_e32 v2, v17, v41
	v_cvt_pk_bf16_f32 v2, v2, s0
	ds_write_b16 v42, v2 offset:54656
	v_mul_f32_e32 v2, v33, v41
	v_cvt_pk_bf16_f32 v2, v2, s0
	ds_write_b16 v42, v2 offset:54720
	v_add_u32_e32 v14, s30, v196
	s_waitcnt lgkmcnt(0)
	v_add_u32_e32 v2, v14, v195
	ds_read_b128 v[2:5], v2 offset:51200
	v_add_u32_e32 v6, v14, v199
	ds_read_b128 v[6:9], v6 offset:51200
	v_lshl_add_u64 v[10:11], s[34:35], 0, v[196:197]
	v_lshlrev_b32_e32 v196, 1, v200
	v_lshl_add_u64 v[12:13], v[10:11], 0, v[196:197]
	v_lshlrev_b32_e32 v196, 1, v202
	s_waitcnt lgkmcnt(1)
	global_store_dwordx4 v[12:13], v[2:5], off
	s_nop 1
	v_lshl_add_u64 v[2:3], v[10:11], 0, v[196:197]
	s_waitcnt lgkmcnt(0)
	global_store_dwordx4 v[2:3], v[6:9], off
	v_add_u32_e32 v2, v14, v201
	ds_read_b128 v[2:5], v2 offset:51200
	v_add_u32_e32 v6, v14, v203
	ds_read_b128 v[6:9], v6 offset:51200
	v_lshlrev_b32_e32 v196, 1, v204
	v_lshl_add_u64 v[12:13], v[10:11], 0, v[196:197]
	v_lshlrev_b32_e32 v196, 1, v206
	s_waitcnt lgkmcnt(1)
	global_store_dwordx4 v[12:13], v[2:5], off
	s_nop 1
	v_lshl_add_u64 v[2:3], v[10:11], 0, v[196:197]
	s_waitcnt lgkmcnt(0)
	global_store_dwordx4 v[2:3], v[6:9], off

.LBB0_1766:
	s_mov_b64 s[10:11], exec
	s_lshl_b32 s8, s76, 8
	v_mbcnt_lo_u32_b32 v3, s10, 0
	s_add_u32 s8, s84, s8
	v_mbcnt_hi_u32_b32 v3, s11, v3
	s_addc_u32 s9, s85, 0
	v_cmp_eq_u32_e32 vcc, 0, v3
	s_and_saveexec_b64 s[12:13], vcc
	s_cbranch_execz .LBB0_1768
	s_bcnt1_i32_b64 s10, s[10:11]
	v_mov_b32_e32 v5, 0x1000
	v_mov_b32_e32 v6, s10
	global_atomic_add v5, v5, v6, s[8:9] offset:1024 sc0
	buffer_inv sc1

.LBB0_1799:
	s_or_b64 exec, exec, s[10:11]
	s_mov_b64 s[10:11], exec
	v_mbcnt_lo_u32_b32 v2, s10, 0
	v_mbcnt_hi_u32_b32 v2, s11, v2
	v_cmp_eq_u32_e32 vcc, 0, v2
	s_waitcnt vmcnt(0)
	s_and_saveexec_b64 s[12:13], vcc
	s_cbranch_execz .LBB0_1801
	s_bcnt1_i32_b64 s10, s[10:11]
	v_mov_b32_e32 v2, 0x2000
	v_mov_b32_e32 v3, s10
	global_atomic_add v2, v3, s[8:9] offset:1024

.LBB0_1808:
	s_or_b64 exec, exec, s[8:9]
	v_add_f32_e32 v32, v32, v39
	v_add_f32_e32 v39, v54, v47
	s_waitcnt lgkmcnt(0)
	v_add_u32_e32 v54, s11, v1
	v_add_f32_e32 v2, v2, v22
	v_add_f32_e32 v7, v7, v23
	v_add_f32_e32 v28, v20, v28
	v_add_f32_e32 v29, v21, v29
	ds_read_b128 v[20:23], v54 offset:49280
	v_add_f32_e32 v9, v9, v24
	v_add_f32_e32 v11, v11, v25
	v_add_f32_e32 v13, v13, v26
	v_add_f32_e32 v19, v19, v27
	v_add_f32_e32 v33, v33, v40
	v_add_f32_e32 v40, v55, v48
	ds_read_b128 v[24:27], v54 offset:49312
	s_waitcnt lgkmcnt(1)
	v_rcp_f32_e32 v55, v20
	v_add_f32_e32 v34, v34, v41
	v_add_f32_e32 v41, v56, v49
	v_rcp_f32_e32 v56, v21
	v_mul_f32_e32 v2, v2, v55
	v_add_f32_e32 v31, v31, v38
	v_add_f32_e32 v38, v46, v45
	v_cvt_pk_bf16_f32 v2, v2, s0
	v_add_f32_e32 v35, v35, v42
	v_add_f32_e32 v36, v36, v43
	v_add_f32_e32 v37, v37, v44
	v_add_f32_e32 v42, v57, v50
	v_add_f32_e32 v43, v58, v51
	v_add_f32_e32 v44, v59, v52
	v_add_f32_e32 v45, v60, v53
	s_waitcnt vmcnt(6)
	v_add_f32_e32 v46, v61, v70
	s_waitcnt vmcnt(5)
	v_add_f32_e32 v47, v62, v71
	v_rcp_f32_e32 v57, v22
	v_rcp_f32_e32 v58, v23
	s_waitcnt lgkmcnt(0)
	v_rcp_f32_e32 v59, v24
	ds_read_b128 v[20:23], v54 offset:49344
	v_rcp_f32_e32 v60, v25
	v_rcp_f32_e32 v61, v26
	v_rcp_f32_e32 v62, v27
	ds_read_b128 v[24:27], v54 offset:49376
	ds_write_b16 v16, v2 offset:51200
	v_mul_f32_e32 v2, v38, v55
	v_cvt_pk_bf16_f32 v2, v2, s0
	ds_write_b16 v16, v2 offset:51264
	v_mul_f32_e32 v2, v7, v56
	v_cvt_pk_bf16_f32 v2, v2, s0
	ds_write_b16 v16, v2 offset:51328
	v_mul_f32_e32 v2, v39, v56
	v_cvt_pk_bf16_f32 v2, v2, s0
	ds_write_b16 v16, v2 offset:51392
	v_mul_f32_e32 v2, v9, v57
	v_cvt_pk_bf16_f32 v2, v2, s0
	ds_write_b16 v16, v2 offset:51456
	v_mul_f32_e32 v2, v40, v57
	v_cvt_pk_bf16_f32 v2, v2, s0
	ds_write_b16 v16, v2 offset:51520
	v_mul_f32_e32 v2, v11, v58
	v_cvt_pk_bf16_f32 v2, v2, s0
	ds_write_b16 v16, v2 offset:51584
	v_mul_f32_e32 v2, v41, v58
	v_cvt_pk_bf16_f32 v2, v2, s0
	ds_write_b16 v16, v2 offset:51648
	v_mul_f32_e32 v2, v13, v59
	v_cvt_pk_bf16_f32 v2, v2, s0
	ds_write_b16 v16, v2 offset:52224
	v_mul_f32_e32 v2, v42, v59
	v_cvt_pk_bf16_f32 v2, v2, s0
	ds_write_b16 v16, v2 offset:52288
	v_mul_f32_e32 v2, v19, v60
	v_cvt_pk_bf16_f32 v2, v2, s0
	ds_write_b16 v16, v2 offset:52352
	v_mul_f32_e32 v2, v43, v60
	v_cvt_pk_bf16_f32 v2, v2, s0
	ds_write_b16 v16, v2 offset:52416
	v_mul_f32_e32 v2, v28, v61
	v_cvt_pk_bf16_f32 v2, v2, s0
	ds_write_b16 v16, v2 offset:52480
	v_mul_f32_e32 v2, v44, v61
	v_cvt_pk_bf16_f32 v2, v2, s0
	s_waitcnt lgkmcnt(14)
	v_rcp_f32_e32 v20, v20
	ds_write_b16 v16, v2 offset:52544
	v_mul_f32_e32 v2, v29, v62
	v_cvt_pk_bf16_f32 v2, v2, s0
	ds_write_b16 v16, v2 offset:52608
	v_mul_f32_e32 v2, v45, v62
	v_add_f32_e32 v30, v30, v77
	v_cvt_pk_bf16_f32 v2, v2, s0
	v_rcp_f32_e32 v21, v21
	ds_write_b16 v16, v2 offset:52672
	v_mul_f32_e32 v2, v30, v20
	v_cvt_pk_bf16_f32 v2, v2, s0
	ds_write_b16 v16, v2 offset:53248
	v_mul_f32_e32 v2, v46, v20
	v_cvt_pk_bf16_f32 v2, v2, s0
	v_rcp_f32_e32 v22, v22
	ds_write_b16 v16, v2 offset:53312
	v_mul_f32_e32 v2, v31, v21
	v_cvt_pk_bf16_f32 v2, v2, s0
	ds_write_b16 v16, v2 offset:53376
	v_mul_f32_e32 v2, v47, v21
	v_cvt_pk_bf16_f32 v2, v2, s0
	v_rcp_f32_e32 v23, v23
	ds_write_b16 v16, v2 offset:53440
	v_mul_f32_e32 v2, v32, v22
	s_waitcnt vmcnt(4)
	v_add_f32_e32 v48, v63, v72
	v_cvt_pk_bf16_f32 v2, v2, s0
	ds_write_b16 v16, v2 offset:53504
	v_mul_f32_e32 v2, v48, v22
	v_cvt_pk_bf16_f32 v2, v2, s0
	s_waitcnt lgkmcnt(14)
	v_rcp_f32_e32 v24, v24
	ds_write_b16 v16, v2 offset:53568
	v_mul_f32_e32 v2, v33, v23
	s_waitcnt vmcnt(3)
	v_add_f32_e32 v49, v64, v73
	v_cvt_pk_bf16_f32 v2, v2, s0
	ds_write_b16 v16, v2 offset:53632
	v_mul_f32_e32 v2, v49, v23
	v_cvt_pk_bf16_f32 v2, v2, s0
	v_rcp_f32_e32 v25, v25
	ds_write_b16 v16, v2 offset:53696
	v_mul_f32_e32 v2, v34, v24
	s_waitcnt vmcnt(2)
	v_add_f32_e32 v50, v65, v74
	v_cvt_pk_bf16_f32 v2, v2, s0
	ds_write_b16 v16, v2 offset:54272
	v_mul_f32_e32 v2, v50, v24
	v_cvt_pk_bf16_f32 v2, v2, s0
	v_rcp_f32_e32 v26, v26
	ds_write_b16 v16, v2 offset:54336
	v_mul_f32_e32 v2, v35, v25
	s_waitcnt vmcnt(1)
	v_add_f32_e32 v51, v66, v75
	v_cvt_pk_bf16_f32 v2, v2, s0
	s_lshl_b32 s6, s20, 8
	ds_write_b16 v16, v2 offset:54400
	v_mul_f32_e32 v2, v51, v25
	s_ashr_i32 s8, s20, 9
	s_and_b32 s6, s6, 0x1f00
	v_cvt_pk_bf16_f32 v2, v2, s0
	s_ashr_i32 s9, s8, 31
	s_add_i32 s6, s6, s10
	v_rcp_f32_e32 v27, v27
	ds_write_b16 v16, v2 offset:54464
	v_mul_f32_e32 v2, v36, v26
	s_waitcnt vmcnt(0)
	v_add_f32_e32 v52, v67, v76
	s_lshl_b64 s[8:9], s[8:9], 24
	s_lshl_b64 s[22:23], s[6:7], 11
	v_cvt_pk_bf16_f32 v2, v2, s0
	s_add_u32 s6, s28, s8
	ds_write_b16 v16, v2 offset:54528
	v_mul_f32_e32 v2, v52, v26
	s_addc_u32 s8, s29, s9
	v_cvt_pk_bf16_f32 v2, v2, s0
	s_add_u32 s6, s6, s22
	ds_write_b16 v16, v2 offset:54592
	v_mul_f32_e32 v2, v37, v27
	v_add_f32_e32 v53, v68, v69
	s_addc_u32 s9, s8, s23
	s_lshl_b32 s8, s20, 2
	v_cvt_pk_bf16_f32 v2, v2, s0
	s_and_b32 s8, s8, 0x780
	ds_write_b16 v16, v2 offset:54656
	v_mul_f32_e32 v2, v53, v27
	s_add_u32 s8, s6, s8
	v_cvt_pk_bf16_f32 v2, v2, s0
	s_addc_u32 s9, s9, 0
	ds_write_b16 v16, v2 offset:54720
	v_lshlrev_b32_e32 v2, 1, v198
	s_waitcnt lgkmcnt(0)
	v_lshl_add_u64 v[28:29], s[8:9], 0, v[2:3]
	v_add_u32_e32 v2, v17, v195
	ds_read_b128 v[20:23], v2 offset:51200
	v_add_u32_e32 v2, v17, v199
	ds_read_b128 v[24:27], v2 offset:51200
	v_mov_b32_e32 v7, v3
	v_lshl_add_u64 v[30:31], v[28:29], 0, v[6:7]
	v_mov_b32_e32 v9, v3
	s_waitcnt lgkmcnt(1)
	global_store_dwordx4 v[30:31], v[20:23], off
	v_add_u32_e32 v2, v17, v201
	v_mov_b32_e32 v11, v3
	v_lshl_add_u64 v[20:21], v[28:29], 0, v[8:9]
	s_waitcnt lgkmcnt(0)
	global_store_dwordx4 v[20:21], v[24:27], off
	ds_read_b128 v[20:23], v2 offset:51200
	v_add_u32_e32 v2, v17, v203
	ds_read_b128 v[24:27], v2 offset:51200
	v_lshl_add_u64 v[30:31], v[28:29], 0, v[10:11]
	v_mov_b32_e32 v13, v3
	s_waitcnt lgkmcnt(1)
	global_store_dwordx4 v[30:31], v[20:23], off
	s_add_i32 s19, s19, s33
	v_cmp_lt_i32_e32 vcc, s19, v14
	v_lshl_add_u64 v[20:21], v[28:29], 0, v[12:13]
	s_waitcnt lgkmcnt(0)
	global_store_dwordx4 v[20:21], v[24:27], off
	s_waitcnt lgkmcnt(0)
	s_barrier
	s_add_i32 s12, s12, s13
	s_add_i32 s14, s14, s15
	s_cbranch_vccz .LBB0_1811

.LBB0_1886:
	v_lshl_or_b32 v146, s47, 8, v163
	v_lshl_add_u32 v150, s20, 8, v1
	v_ashrrev_i32_e32 v147, 31, v146
	v_lshlrev_b64 v[146:147], 1, v[146:147]
	v_ashrrev_i32_e32 v151, 31, v150
	v_lshl_add_u64 v[148:149], s[2:3], 0, v[146:147]
	v_lshlrev_b64 v[192:193], 11, v[150:151]
	v_lshl_add_u64 v[152:153], v[148:149], 0, v[192:193]
	global_load_dwordx4 v[156:159], v[152:153], off
	global_load_dwordx4 v[168:171], v[152:153], off offset:256
	v_or_b32_e32 v152, 16, v150
	v_ashrrev_i32_e32 v153, 31, v152
	v_lshlrev_b64 v[200:201], 11, v[152:153]
	v_lshl_add_u64 v[152:153], v[148:149], 0, v[200:201]
	global_load_dwordx4 v[172:175], v[152:153], off
	global_load_dwordx4 v[176:179], v[152:153], off offset:256
	v_or_b32_e32 v152, 32, v150
	v_ashrrev_i32_e32 v153, 31, v152
	v_lshlrev_b64 v[154:155], 11, v[152:153]
	v_lshl_add_u64 v[152:153], v[148:149], 0, v[154:155]
	global_load_dwordx4 v[180:183], v[152:153], off
	global_load_dwordx4 v[184:187], v[152:153], off offset:256
	v_or_b32_e32 v152, 48, v150
	v_ashrrev_i32_e32 v153, 31, v152
	v_lshlrev_b64 v[152:153], 11, v[152:153]
	v_lshl_add_u64 v[160:161], v[148:149], 0, v[152:153]
	global_load_dwordx4 v[188:191], v[160:161], off
	global_load_dwordx4 v[196:199], v[160:161], off offset:256
	s_andn2_b64 vcc, exec, s[4:5]
	s_mov_b64 s[4:5], -1
	s_waitcnt vmcnt(0)
	v_lshlrev_b32_e32 v202, 16, v156
	v_and_b32_e32 v203, 0xffff0000, v156
	v_lshlrev_b32_e32 v206, 16, v158
	v_and_b32_e32 v207, 0xffff0000, v158
	v_lshlrev_b32_e32 v208, 16, v159
	v_and_b32_e32 v209, 0xffff0000, v159
	v_pk_add_f32 v[126:127], v[126:127], v[202:203]
	v_lshlrev_b32_e32 v204, 16, v157
	v_and_b32_e32 v205, 0xffff0000, v157
	v_lshlrev_b32_e32 v210, 16, v168
	v_and_b32_e32 v211, 0xffff0000, v168
	v_lshlrev_b32_e32 v168, 16, v169
	v_and_b32_e32 v169, 0xffff0000, v169
	v_lshlrev_b32_e32 v212, 16, v170
	v_and_b32_e32 v213, 0xffff0000, v170
	v_lshlrev_b32_e32 v170, 16, v171
	v_lshlrev_b32_e32 v156, 16, v198
	v_and_b32_e32 v157, 0xffff0000, v198
	v_lshlrev_b32_e32 v160, 16, v199
	v_and_b32_e32 v161, 0xffff0000, v199
	v_pk_add_f32 v[198:199], v[124:125], v[208:209]
	v_pk_add_f32 v[124:125], v[122:123], v[206:207]
	v_cvt_pk_bf16_f32 v122, v126, v127
	v_lshl_add_u64 v[126:127], s[82:83], 0, v[192:193]
	v_and_b32_e32 v171, 0xffff0000, v171
	v_pk_add_f32 v[128:129], v[128:129], v[204:205]
	v_lshl_add_u64 v[126:127], v[126:127], 0, v[146:147]
	v_cvt_pk_bf16_f32 v123, v128, v129
	v_lshlrev_b32_e32 v214, 16, v172
	v_and_b32_e32 v215, 0xffff0000, v172
	v_lshlrev_b32_e32 v172, 16, v173
	v_and_b32_e32 v173, 0xffff0000, v173
	v_cvt_pk_bf16_f32 v124, v124, v125
	v_cvt_pk_bf16_f32 v125, v198, v199
	global_store_dwordx4 v[126:127], v[122:125], off
	v_pk_add_f32 v[120:121], v[120:121], v[168:169]
	v_pk_add_f32 v[118:119], v[118:119], v[210:211]
	v_pk_add_f32 v[122:123], v[112:113], v[170:171]
	v_pk_add_f32 v[112:113], v[110:111], v[212:213]
	v_cvt_pk_bf16_f32 v110, v118, v119
	v_cvt_pk_bf16_f32 v111, v120, v121
	v_lshlrev_b32_e32 v216, 16, v174
	v_and_b32_e32 v217, 0xffff0000, v174
	v_lshlrev_b32_e32 v174, 16, v175
	v_and_b32_e32 v175, 0xffff0000, v175
	v_cvt_pk_bf16_f32 v112, v112, v113
	v_cvt_pk_bf16_f32 v113, v122, v123
	global_store_dwordx4 v[126:127], v[110:113], off offset:256
	v_lshlrev_b32_e32 v218, 16, v176
	v_and_b32_e32 v219, 0xffff0000, v176
	v_pk_add_f32 v[110:111], v[116:117], v[172:173]
	v_pk_add_f32 v[112:113], v[114:115], v[214:215]
	v_pk_add_f32 v[114:115], v[108:109], v[174:175]
	v_pk_add_f32 v[108:109], v[106:107], v[216:217]
	v_cvt_pk_bf16_f32 v106, v112, v113
	v_cvt_pk_bf16_f32 v107, v110, v111
	v_lshl_add_u64 v[110:111], s[82:83], 0, v[200:201]
	v_lshlrev_b32_e32 v176, 16, v177
	v_and_b32_e32 v177, 0xffff0000, v177
	v_lshlrev_b32_e32 v220, 16, v178
	v_and_b32_e32 v221, 0xffff0000, v178
	v_lshlrev_b32_e32 v178, 16, v179
	v_and_b32_e32 v179, 0xffff0000, v179
	v_lshl_add_u64 v[110:111], v[110:111], 0, v[146:147]
	v_lshlrev_b32_e32 v230, 16, v180
	v_and_b32_e32 v231, 0xffff0000, v180
	v_lshlrev_b32_e32 v180, 16, v181
	v_and_b32_e32 v181, 0xffff0000, v181
	v_cvt_pk_bf16_f32 v108, v108, v109
	v_cvt_pk_bf16_f32 v109, v114, v115
	global_store_dwordx4 v[110:111], v[106:109], off
	v_pk_add_f32 v[104:105], v[104:105], v[176:177]
	v_pk_add_f32 v[102:103], v[102:103], v[218:219]
	v_pk_add_f32 v[106:107], v[96:97], v[178:179]
	v_pk_add_f32 v[96:97], v[94:95], v[220:221]
	v_cvt_pk_bf16_f32 v94, v102, v103
	v_cvt_pk_bf16_f32 v95, v104, v105
	v_lshlrev_b32_e32 v232, 16, v182
	v_and_b32_e32 v233, 0xffff0000, v182
	v_lshlrev_b32_e32 v182, 16, v183
	v_and_b32_e32 v183, 0xffff0000, v183
	v_cvt_pk_bf16_f32 v96, v96, v97
	v_cvt_pk_bf16_f32 v97, v106, v107
	global_store_dwordx4 v[110:111], v[94:97], off offset:256
	v_lshlrev_b32_e32 v234, 16, v184
	v_and_b32_e32 v235, 0xffff0000, v184
	v_pk_add_f32 v[94:95], v[100:101], v[180:181]
	v_pk_add_f32 v[96:97], v[98:99], v[230:231]
	v_pk_add_f32 v[98:99], v[92:93], v[182:183]
	v_pk_add_f32 v[92:93], v[90:91], v[232:233]
	v_cvt_pk_bf16_f32 v90, v96, v97
	v_cvt_pk_bf16_f32 v91, v94, v95
	v_lshl_add_u64 v[94:95], s[82:83], 0, v[154:155]
	v_lshlrev_b32_e32 v184, 16, v185
	v_and_b32_e32 v185, 0xffff0000, v185
	v_lshlrev_b32_e32 v236, 16, v186
	v_and_b32_e32 v237, 0xffff0000, v186
	v_lshlrev_b32_e32 v186, 16, v187
	v_and_b32_e32 v187, 0xffff0000, v187
	v_lshl_add_u64 v[94:95], v[94:95], 0, v[146:147]
	v_lshlrev_b32_e32 v238, 16, v188
	v_and_b32_e32 v239, 0xffff0000, v188
	v_lshlrev_b32_e32 v188, 16, v189
	v_and_b32_e32 v189, 0xffff0000, v189
	v_cvt_pk_bf16_f32 v92, v92, v93
	v_cvt_pk_bf16_f32 v93, v98, v99
	global_store_dwordx4 v[94:95], v[90:93], off
	v_pk_add_f32 v[88:89], v[88:89], v[184:185]
	v_pk_add_f32 v[86:87], v[86:87], v[234:235]
	v_pk_add_f32 v[90:91], v[80:81], v[186:187]
	v_pk_add_f32 v[80:81], v[78:79], v[236:237]
	v_cvt_pk_bf16_f32 v78, v86, v87
	v_cvt_pk_bf16_f32 v79, v88, v89
	v_lshlrev_b32_e32 v240, 16, v190
	v_and_b32_e32 v241, 0xffff0000, v190
	v_lshlrev_b32_e32 v190, 16, v191
	v_and_b32_e32 v191, 0xffff0000, v191
	v_cvt_pk_bf16_f32 v80, v80, v81
	v_cvt_pk_bf16_f32 v81, v90, v91
	global_store_dwordx4 v[94:95], v[78:81], off offset:256
	v_lshlrev_b32_e32 v158, 16, v196
	v_and_b32_e32 v159, 0xffff0000, v196
	v_pk_add_f32 v[78:79], v[84:85], v[188:189]
	v_pk_add_f32 v[80:81], v[82:83], v[238:239]
	v_pk_add_f32 v[82:83], v[76:77], v[190:191]
	v_pk_add_f32 v[76:77], v[74:75], v[240:241]
	v_cvt_pk_bf16_f32 v74, v80, v81
	v_cvt_pk_bf16_f32 v75, v78, v79
	v_lshl_add_u64 v[78:79], s[82:83], 0, v[152:153]
	v_lshl_add_u64 v[78:79], v[78:79], 0, v[146:147]
	v_lshlrev_b32_e32 v196, 16, v197
	v_and_b32_e32 v197, 0xffff0000, v197
	v_cvt_pk_bf16_f32 v76, v76, v77
	v_cvt_pk_bf16_f32 v77, v82, v83
	global_store_dwordx4 v[78:79], v[74:77], off
	v_pk_add_f32 v[70:71], v[70:71], v[158:159]
	v_pk_add_f32 v[72:73], v[72:73], v[196:197]
	v_pk_add_f32 v[74:75], v[68:69], v[160:161]
	v_pk_add_f32 v[68:69], v[66:67], v[156:157]
	v_cvt_pk_bf16_f32 v66, v70, v71
	v_cvt_pk_bf16_f32 v67, v72, v73
	v_add_u32_e32 v70, 0x80, v150
	v_cvt_pk_bf16_f32 v68, v68, v69
	v_cvt_pk_bf16_f32 v69, v74, v75
	global_store_dwordx4 v[78:79], v[66:69], off offset:256
	v_ashrrev_i32_e32 v71, 31, v70
	v_lshlrev_b64 v[102:103], 11, v[70:71]
	v_add_u32_e32 v66, 0x90, v150
	v_ashrrev_i32_e32 v67, 31, v66
	v_lshlrev_b64 v[104:105], 11, v[66:67]
	v_lshl_add_u64 v[74:75], v[148:149], 0, v[102:103]
	v_lshl_add_u64 v[66:67], v[148:149], 0, v[104:105]
	global_load_dwordx4 v[70:73], v[74:75], off
	s_waitcnt vmcnt(0)
	v_lshlrev_b32_e32 v106, 16, v70
	global_load_dwordx4 v[74:77], v[74:75], off offset:256
	s_nop 0
	global_load_dwordx4 v[78:81], v[66:67], off
	global_load_dwordx4 v[82:85], v[66:67], off offset:256
	v_add_u32_e32 v66, 0xa0, v150
	v_ashrrev_i32_e32 v67, 31, v66
	v_lshlrev_b64 v[68:69], 11, v[66:67]
	v_lshl_add_u64 v[66:67], v[148:149], 0, v[68:69]
	global_load_dwordx4 v[86:89], v[66:67], off
	global_load_dwordx4 v[90:93], v[66:67], off offset:256
	v_add_u32_e32 v66, 0xb0, v150
	v_ashrrev_i32_e32 v67, 31, v66
	v_lshlrev_b64 v[66:67], 11, v[66:67]
	v_lshl_add_u64 v[98:99], v[148:149], 0, v[66:67]
	global_load_dwordx4 v[94:97], v[98:99], off
	s_nop 0
	global_load_dwordx4 v[98:101], v[98:99], off offset:256
	v_and_b32_e32 v107, 0xffff0000, v70
	v_lshlrev_b32_e32 v110, 16, v72
	v_and_b32_e32 v111, 0xffff0000, v72
	v_lshlrev_b32_e32 v112, 16, v73
	v_and_b32_e32 v113, 0xffff0000, v73
	v_pk_add_f32 v[62:63], v[62:63], v[106:107]
	v_lshlrev_b32_e32 v108, 16, v71
	v_and_b32_e32 v109, 0xffff0000, v71
	v_pk_add_f32 v[64:65], v[64:65], v[108:109]
	s_waitcnt vmcnt(6)
	v_lshlrev_b32_e32 v114, 16, v74
	v_and_b32_e32 v115, 0xffff0000, v74
	v_lshlrev_b32_e32 v116, 16, v75
	v_and_b32_e32 v117, 0xffff0000, v75
	v_lshlrev_b32_e32 v118, 16, v76
	v_and_b32_e32 v119, 0xffff0000, v76
	v_lshlrev_b32_e32 v76, 16, v77
	v_and_b32_e32 v77, 0xffff0000, v77
	s_waitcnt vmcnt(5)
	v_lshlrev_b32_e32 v120, 16, v78
	v_and_b32_e32 v121, 0xffff0000, v78
	v_lshlrev_b32_e32 v78, 16, v79
	s_waitcnt vmcnt(0)
	v_lshlrev_b32_e32 v70, 16, v100
	v_and_b32_e32 v71, 0xffff0000, v100
	v_lshlrev_b32_e32 v74, 16, v101
	v_and_b32_e32 v75, 0xffff0000, v101
	v_pk_add_f32 v[100:101], v[60:61], v[112:113]
	v_pk_add_f32 v[60:61], v[58:59], v[110:111]
	v_cvt_pk_bf16_f32 v58, v62, v63
	v_lshl_add_u64 v[62:63], s[82:83], 0, v[102:103]
	v_cvt_pk_bf16_f32 v59, v64, v65
	v_lshl_add_u64 v[62:63], v[62:63], 0, v[146:147]
	v_and_b32_e32 v79, 0xffff0000, v79
	v_cvt_pk_bf16_f32 v60, v60, v61
	v_cvt_pk_bf16_f32 v61, v100, v101
	global_store_dwordx4 v[62:63], v[58:61], off
	v_pk_add_f32 v[56:57], v[56:57], v[116:117]
	v_pk_add_f32 v[54:55], v[54:55], v[114:115]
	v_pk_add_f32 v[58:59], v[48:49], v[76:77]
	v_pk_add_f32 v[48:49], v[46:47], v[118:119]
	v_cvt_pk_bf16_f32 v46, v54, v55
	v_cvt_pk_bf16_f32 v47, v56, v57
	v_lshlrev_b32_e32 v122, 16, v80
	v_and_b32_e32 v123, 0xffff0000, v80
	v_lshlrev_b32_e32 v80, 16, v81
	v_and_b32_e32 v81, 0xffff0000, v81
	v_cvt_pk_bf16_f32 v48, v48, v49
	v_cvt_pk_bf16_f32 v49, v58, v59
	global_store_dwordx4 v[62:63], v[46:49], off offset:256
	v_lshlrev_b32_e32 v124, 16, v82
	v_and_b32_e32 v125, 0xffff0000, v82
	v_pk_add_f32 v[46:47], v[52:53], v[78:79]
	v_pk_add_f32 v[48:49], v[50:51], v[120:121]
	v_pk_add_f32 v[50:51], v[44:45], v[80:81]
	v_pk_add_f32 v[44:45], v[42:43], v[122:123]
	v_cvt_pk_bf16_f32 v42, v48, v49
	v_cvt_pk_bf16_f32 v43, v46, v47
	v_lshl_add_u64 v[46:47], s[82:83], 0, v[104:105]
	v_lshlrev_b32_e32 v82, 16, v83
	v_and_b32_e32 v83, 0xffff0000, v83
	v_lshlrev_b32_e32 v126, 16, v84
	v_and_b32_e32 v127, 0xffff0000, v84
	v_lshlrev_b32_e32 v84, 16, v85
	v_and_b32_e32 v85, 0xffff0000, v85
	v_lshl_add_u64 v[46:47], v[46:47], 0, v[146:147]
	v_lshlrev_b32_e32 v128, 16, v86
	v_and_b32_e32 v129, 0xffff0000, v86
	v_lshlrev_b32_e32 v86, 16, v87
	v_and_b32_e32 v87, 0xffff0000, v87
	v_cvt_pk_bf16_f32 v44, v44, v45
	v_cvt_pk_bf16_f32 v45, v50, v51
	global_store_dwordx4 v[46:47], v[42:45], off
	v_pk_add_f32 v[40:41], v[40:41], v[82:83]
	v_pk_add_f32 v[38:39], v[38:39], v[124:125]
	v_pk_add_f32 v[42:43], v[32:33], v[84:85]
	v_pk_add_f32 v[32:33], v[30:31], v[126:127]
	v_cvt_pk_bf16_f32 v30, v38, v39
	v_cvt_pk_bf16_f32 v31, v40, v41
	v_lshlrev_b32_e32 v148, 16, v88
	v_and_b32_e32 v149, 0xffff0000, v88
	v_lshlrev_b32_e32 v88, 16, v89
	v_and_b32_e32 v89, 0xffff0000, v89
	v_cvt_pk_bf16_f32 v32, v32, v33
	v_cvt_pk_bf16_f32 v33, v42, v43
	global_store_dwordx4 v[46:47], v[30:33], off offset:256
	v_lshlrev_b32_e32 v150, 16, v90
	v_and_b32_e32 v151, 0xffff0000, v90
	v_pk_add_f32 v[30:31], v[36:37], v[86:87]
	v_pk_add_f32 v[32:33], v[34:35], v[128:129]
	v_pk_add_f32 v[34:35], v[28:29], v[88:89]
	v_pk_add_f32 v[28:29], v[26:27], v[148:149]
	v_cvt_pk_bf16_f32 v26, v32, v33
	v_cvt_pk_bf16_f32 v27, v30, v31
	v_lshl_add_u64 v[30:31], s[82:83], 0, v[68:69]
	v_lshlrev_b32_e32 v90, 16, v91
	v_and_b32_e32 v91, 0xffff0000, v91
	v_lshlrev_b32_e32 v152, 16, v92
	v_and_b32_e32 v153, 0xffff0000, v92
	v_lshlrev_b32_e32 v92, 16, v93
	v_and_b32_e32 v93, 0xffff0000, v93
	v_lshl_add_u64 v[30:31], v[30:31], 0, v[146:147]
	v_lshlrev_b32_e32 v154, 16, v94
	v_and_b32_e32 v155, 0xffff0000, v94
	v_lshlrev_b32_e32 v94, 16, v95
	v_and_b32_e32 v95, 0xffff0000, v95
	v_cvt_pk_bf16_f32 v28, v28, v29
	v_cvt_pk_bf16_f32 v29, v34, v35
	global_store_dwordx4 v[30:31], v[26:29], off
	v_pk_add_f32 v[24:25], v[24:25], v[90:91]
	v_pk_add_f32 v[22:23], v[22:23], v[150:151]
	v_pk_add_f32 v[26:27], v[16:17], v[92:93]
	v_pk_add_f32 v[16:17], v[14:15], v[152:153]
	v_cvt_pk_bf16_f32 v14, v22, v23
	v_cvt_pk_bf16_f32 v15, v24, v25
	v_lshlrev_b32_e32 v156, 16, v96
	v_and_b32_e32 v157, 0xffff0000, v96
	v_lshlrev_b32_e32 v96, 16, v97
	v_and_b32_e32 v97, 0xffff0000, v97
	v_cvt_pk_bf16_f32 v16, v16, v17
	v_cvt_pk_bf16_f32 v17, v26, v27
	global_store_dwordx4 v[30:31], v[14:17], off offset:256
	v_lshlrev_b32_e32 v72, 16, v98
	v_and_b32_e32 v73, 0xffff0000, v98
	v_pk_add_f32 v[14:15], v[20:21], v[94:95]
	v_pk_add_f32 v[16:17], v[18:19], v[154:155]
	v_pk_add_f32 v[18:19], v[12:13], v[96:97]
	v_pk_add_f32 v[12:13], v[10:11], v[156:157]
	v_cvt_pk_bf16_f32 v10, v16, v17
	v_cvt_pk_bf16_f32 v11, v14, v15
	v_lshl_add_u64 v[14:15], s[82:83], 0, v[66:67]
	v_lshl_add_u64 v[14:15], v[14:15], 0, v[146:147]
	v_lshlrev_b32_e32 v98, 16, v99
	v_and_b32_e32 v99, 0xffff0000, v99
	v_cvt_pk_bf16_f32 v12, v12, v13
	v_cvt_pk_bf16_f32 v13, v18, v19
	global_store_dwordx4 v[14:15], v[10:13], off
	v_pk_add_f32 v[8:9], v[8:9], v[98:99]
	v_pk_add_f32 v[6:7], v[6:7], v[72:73]
	v_pk_add_f32 v[10:11], v[4:5], v[74:75]
	v_pk_add_f32 v[4:5], v[2:3], v[70:71]
	v_cvt_pk_bf16_f32 v2, v6, v7
	v_cvt_pk_bf16_f32 v3, v8, v9
	s_nop 0
	v_cvt_pk_bf16_f32 v4, v4, v5
	v_cvt_pk_bf16_f32 v5, v10, v11
	global_store_dwordx4 v[14:15], v[2:5], off offset:256
	s_cbranch_vccnz .LBB0_1875
	s_andn2_b64 vcc, exec, s[6:7]
	s_cbranch_vccnz .LBB0_1874
	s_barrier
	s_branch .LBB0_1874

.LBB0_1907:
	s_mov_b64 s[6:7], exec
	s_lshl_b32 s4, s76, 8
	v_mbcnt_lo_u32_b32 v2, s6, 0
	s_add_u32 s4, s84, s4
	v_mbcnt_hi_u32_b32 v2, s7, v2
	s_addc_u32 s5, s85, 0
	v_cmp_eq_u32_e32 vcc, 0, v2
	s_and_saveexec_b64 s[8:9], vcc
	s_cbranch_execz .LBB0_1909
	s_bcnt1_i32_b64 s6, s[6:7]
	v_mov_b32_e32 v4, 0x1000
	v_mov_b32_e32 v5, s6
	global_atomic_add v4, v4, v5, s[4:5] offset:1024 sc0
	buffer_inv sc1

.LBB0_1922:
	s_or_b64 exec, exec, s[8:9]
	s_waitcnt vmcnt(0)
	s_waitcnt vmcnt(0)

.LBB0_1940:
	s_or_b64 exec, exec, s[6:7]
	s_mov_b64 s[6:7], exec
	v_mbcnt_lo_u32_b32 v1, s6, 0
	v_mbcnt_hi_u32_b32 v1, s7, v1
	v_cmp_eq_u32_e32 vcc, 0, v1
	s_waitcnt vmcnt(0)
	s_and_saveexec_b64 s[8:9], vcc
	s_cbranch_execz .LBB0_1942
	s_bcnt1_i32_b64 s6, s[6:7]
	v_mov_b32_e32 v1, 0x2000
	v_mov_b32_e32 v2, s6
	global_atomic_add v1, v2, s[4:5] offset:1024
